# GEMM K-loops: the two waits closing each load segment (vmcnt, then lgkmcnt) merged into one s_waitcnt in front of the barrier
# baseline (speedup 1.0000x reference)
; #define PG8_STAGE(bufoff, gbase, voff) do { _Pragma("unroll") for (int _i = 0; _i < 2; ++_i) \
;         __builtin_amdgcn_global_load_lds((const unsigned*)((const char*)(gbase) + (voff)[_i]), (LAS unsigned*)(lds + (bufoff) + ldsw + _i * 8192), 16, 0, 0); } while (0)
; #define PG8_LDA(dst, b, h) do { _Pragma("unroll") for (int m = 0; m < 4; ++m) dst[m] = PG8_LD32(lds + PG8_SA(b, h) + aoff + m * 2048); } while (0)
; #define PG8_LDB(dst, b, h) do { _Pragma("unroll") for (int n = 0; n < 2; ++n) dst[n] = PG8_LD32(lds + PG8_SB(b, h) + boff + n * 2048); } while (0)
; #define PG8_WAIT_V(n) asm volatile("s_waitcnt vmcnt(" #n ")" ::: "memory")
; #define PG8_WAIT_L(n) asm volatile("s_waitcnt lgkmcnt(" #n ")" ::: "memory")
; #define PG8_BAR __builtin_amdgcn_s_barrier()
; #define PG8_SCHED __builtin_amdgcn_sched_barrier(0)
; #define PG8_STA(bufoff, nextflag, h, koff) do { if constexpr (Sched::GATHER) { unsigned _o[2]; _o[0] = (nextflag) ? nxtA[h][0] : curA[h][0]; _o[1] = (nextflag) ? nxtA[h][1] : curA[h][1]; PG8_STAGE(bufoff, Ab + (koff), _o); } \
;         else { PG8_STAGE(bufoff, ((nextflag) ? nA : cA) + (size_t)(h) * hstep + (koff), voffA); } } while (0)
; template <class Epi, class Sched, bool ALIGN_EPI, int DT>
; __device__ __forceinline__ void gemm_phase(LAS unsigned char* lds, const int KB, const Sched& S, const Epi& E) {
;     ...
;             const size_t k1 = (size_t)(t + 1) * kstep, k2 = last ? 0 : (size_t)(t + 2) * kstep, k3 = k2 + kstep;
;             const char* b2 = last ? nB : cB + (size_t)(t + 2) * kstep; const char* b3 = b2 + kstep;
;             PG8_LDB(B0, 0, 0); PG8_LDB(B1, 0, 1); PG8_SCHED; PG8_LDA(At, 0, 0); PG8_STA(PG8_SA(1, 1), false, 1, k1);
;             PG8_WAIT_V(8); PG8_WAIT_L(0); PG8_BAR; PG8_MMA(0, 0, At, B0); PG8_MMA(0, 1, At, B1); PG8_BAR; PG8_SCHED;
;             PG8_LDA(At, 0, 1); PG8_STAGE(PG8_SB(0, 0), b2, voffB); PG8_STAGE(PG8_SB(0, 1), b2 + hstep, voffB); PG8_STA(PG8_SA(0, 0), last, 0, k2);
;             PG8_WAIT_V(8); PG8_WAIT_L(0); PG8_BAR; PG8_MMA(1, 0, At, B0); PG8_MMA(1, 1, At, B1); PG8_BAR; PG8_SCHED;
.LBB0_193:
	ds_read_b128 v[152:155], v175
	ds_read_b128 v[156:159], v175 offset:1024
	ds_read_b128 v[160:163], v175 offset:2048
	ds_read_b128 v[164:167], v175 offset:3072
	ds_read_b128 v[168:171], v176
	ds_read_b128 v[182:185], v176 offset:1024
	ds_read_b128 v[186:189], v176 offset:2048
	ds_read_b128 v[190:193], v176 offset:3072
	s_add_u32 s38, s36, 0x100
	s_addc_u32 s39, s37, 0
	s_add_u32 s68, s25, s36
	s_addc_u32 s69, s66, s37
	s_cmp_eq_u32 s67, 12
	s_cselect_b64 s[42:43], -1, 0
	s_and_b64 s[40:41], s[42:43], exec
	s_cselect_b32 s70, 0, s38
	s_cselect_b32 s41, s0, s69
	s_cselect_b32 s40, s23, s68
	v_lshl_add_u64 v[228:229], v[148:149], 0, s[36:37]
	s_add_i32 m0, s45, 0xc000
	ds_read_b128 v[196:199], v177
	ds_read_b128 v[200:203], v177 offset:1024
	ds_read_b128 v[204:207], v177 offset:2048
	ds_read_b128 v[208:211], v177 offset:3072
	ds_read_b128 v[212:215], v177 offset:4096
	ds_read_b128 v[216:219], v177 offset:5120
	ds_read_b128 v[220:223], v177 offset:6144
	ds_read_b128 v[224:227], v177 offset:7168
	global_load_lds_dwordx4 v[228:229], off
	v_lshl_add_u64 v[228:229], v[150:151], 0, s[36:37]
	s_add_i32 m0, s45, 0xe000
	s_nop 0
	global_load_lds_dwordx4 v[228:229], off
	s_waitcnt vmcnt(8) lgkmcnt(0)
	s_barrier
	s_setprio 1
	s_waitcnt lgkmcnt(0)
	v_mfma_i32_16x16x64_i8 v[126:129], v[152:155], v[196:199], v[126:129]
	v_mfma_i32_16x16x64_i8 v[122:125], v[160:163], v[196:199], v[122:125]
	v_mfma_i32_16x16x64_i8 v[110:113], v[152:155], v[204:207], v[110:113]
	v_mfma_i32_16x16x64_i8 v[106:109], v[160:163], v[204:207], v[106:109]
	v_mfma_i32_16x16x64_i8 v[94:97], v[152:155], v[212:215], v[94:97]
	v_mfma_i32_16x16x64_i8 v[90:93], v[160:163], v[212:215], v[90:93]
	v_mfma_i32_16x16x64_i8 v[78:81], v[152:155], v[220:223], v[78:81]
	v_mfma_i32_16x16x64_i8 v[74:77], v[160:163], v[220:223], v[74:77]
	v_mfma_i32_16x16x64_i8 v[126:129], v[156:159], v[200:203], v[126:129]
	v_mfma_i32_16x16x64_i8 v[122:125], v[164:167], v[200:203], v[122:125]
	v_mfma_i32_16x16x64_i8 v[110:113], v[156:159], v[208:211], v[110:113]
	v_mfma_i32_16x16x64_i8 v[106:109], v[164:167], v[208:211], v[106:109]
	v_mfma_i32_16x16x64_i8 v[94:97], v[156:159], v[216:219], v[94:97]
	v_mfma_i32_16x16x64_i8 v[90:93], v[164:167], v[216:219], v[90:93]
	v_mfma_i32_16x16x64_i8 v[78:81], v[156:159], v[224:227], v[78:81]
	v_mfma_i32_16x16x64_i8 v[74:77], v[164:167], v[224:227], v[74:77]
	s_setprio 0
	s_setprio 1
	v_mfma_i32_16x16x64_i8 v[118:121], v[168:171], v[196:199], v[118:121]
	v_mfma_i32_16x16x64_i8 v[114:117], v[186:189], v[196:199], v[114:117]
	v_mfma_i32_16x16x64_i8 v[102:105], v[168:171], v[204:207], v[102:105]
	v_mfma_i32_16x16x64_i8 v[98:101], v[186:189], v[204:207], v[98:101]
	v_mfma_i32_16x16x64_i8 v[86:89], v[168:171], v[212:215], v[86:89]
	v_mfma_i32_16x16x64_i8 v[82:85], v[186:189], v[212:215], v[82:85]
	v_mfma_i32_16x16x64_i8 v[70:73], v[168:171], v[220:223], v[70:73]
	v_mfma_i32_16x16x64_i8 v[66:69], v[186:189], v[220:223], v[66:69]
	v_mfma_i32_16x16x64_i8 v[118:121], v[182:185], v[200:203], v[118:121]
	v_mfma_i32_16x16x64_i8 v[114:117], v[190:193], v[200:203], v[114:117]
	v_mfma_i32_16x16x64_i8 v[102:105], v[182:185], v[208:211], v[102:105]
	v_mfma_i32_16x16x64_i8 v[98:101], v[190:193], v[208:211], v[98:101]
	v_mfma_i32_16x16x64_i8 v[86:89], v[182:185], v[216:219], v[86:89]
	v_mfma_i32_16x16x64_i8 v[82:85], v[190:193], v[216:219], v[82:85]
	v_mfma_i32_16x16x64_i8 v[70:73], v[182:185], v[224:227], v[70:73]
	v_mfma_i32_16x16x64_i8 v[66:69], v[190:193], v[224:227], v[66:69]
	s_setprio 0
	s_barrier
	s_add_i32 s36, s62, s5
	v_lshl_add_u64 v[228:229], s[40:41], 0, v[134:135]
	s_mov_b32 m0, s36
	ds_read_b128 v[196:199], v177 offset:16384
	ds_read_b128 v[200:203], v177 offset:17408
	ds_read_b128 v[204:207], v177 offset:18432
	ds_read_b128 v[208:211], v177 offset:19456
	ds_read_b128 v[212:215], v177 offset:20480
	ds_read_b128 v[216:219], v177 offset:21504
	ds_read_b128 v[220:223], v177 offset:22528
	ds_read_b128 v[224:227], v177 offset:23552
	global_load_lds_dwordx4 v[228:229], off
	s_add_i32 m0, s36, 0x2000
	s_add_u32 s36, s40, 0x40000
	v_lshl_add_u64 v[230:231], s[40:41], 0, v[132:133]
	s_addc_u32 s37, s41, 0
	s_add_i32 s68, s63, s5
	global_load_lds_dwordx4 v[230:231], off
	v_lshl_add_u64 v[232:233], s[36:37], 0, v[134:135]
	s_mov_b32 m0, s68
	s_nop 0
	global_load_lds_dwordx4 v[232:233], off
	v_lshl_add_u64 v[232:233], s[36:37], 0, v[132:133]
	s_add_i32 m0, s68, 0x2000
	s_and_b64 s[36:37], s[8:9], s[42:43]
	s_and_b64 s[36:37], s[36:37], exec
	s_cselect_b32 s36, s26, s34
	s_cselect_b32 s37, s27, s35
	s_add_u32 s36, s36, s70
	s_addc_u32 s37, s37, 0
	global_load_lds_dwordx4 v[232:233], off
	v_lshl_add_u64 v[232:233], s[36:37], 0, v[136:137]
	s_mov_b32 m0, s45
	v_lshl_add_u64 v[234:235], s[36:37], 0, v[138:139]
	global_load_lds_dwordx4 v[232:233], off
	s_mov_b32 m0, s46
	s_nop 0
	global_load_lds_dwordx4 v[234:235], off
	s_waitcnt vmcnt(8) lgkmcnt(0)
	s_barrier
; #define PG8_LDA(dst, b, h) do { _Pragma("unroll") for (int m = 0; m < 4; ++m) dst[m] = PG8_LD32(lds + PG8_SA(b, h) + aoff + m * 2048); } while (0)
; #define PG8_LDB(dst, b, h) do { _Pragma("unroll") for (int n = 0; n < 2; ++n) dst[n] = PG8_LD32(lds + PG8_SB(b, h) + boff + n * 2048); } while (0)
; #define PG8_WAIT_V(n) asm volatile("s_waitcnt vmcnt(" #n ")" ::: "memory")
; #define PG8_WAIT_L(n) asm volatile("s_waitcnt lgkmcnt(" #n ")" ::: "memory")
; #define PG8_BAR __builtin_amdgcn_s_barrier()
; #define PG8_SCHED __builtin_amdgcn_sched_barrier(0)
; #define PG8_STA(bufoff, nextflag, h, koff) do { if constexpr (Sched::GATHER) { unsigned _o[2]; _o[0] = (nextflag) ? nxtA[h][0] : curA[h][0]; _o[1] = (nextflag) ? nxtA[h][1] : curA[h][1]; PG8_STAGE(bufoff, Ab + (koff), _o); } \
;         else { PG8_STAGE(bufoff, ((nextflag) ? nA : cA) + (size_t)(h) * hstep + (koff), voffA); } } while (0)
; template <class Epi, class Sched, bool ALIGN_EPI, int DT>
; __device__ __forceinline__ void gemm_phase(LAS unsigned char* lds, const int KB, const Sched& S, const Epi& E) {
;     ...
;             PG8_WAIT_V(8); PG8_WAIT_L(0); PG8_BAR; PG8_MMA(1, 0, At, B0); PG8_MMA(1, 1, At, B1); PG8_BAR; PG8_SCHED;
;             PG8_LDB(B0, 1, 0); PG8_LDB(B1, 1, 1); PG8_SCHED; PG8_LDA(At, 1, 0); PG8_STA(PG8_SA(0, 1), last, 1, k2);
;             PG8_WAIT_V(8); PG8_WAIT_L(0); PG8_BAR; PG8_MMA(0, 0, At, B0); PG8_MMA(0, 1, At, B1); PG8_BAR; PG8_SCHED;
	s_setprio 1
	s_waitcnt lgkmcnt(0)
	v_mfma_i32_16x16x64_i8 v[62:65], v[152:155], v[196:199], v[62:65]
	v_mfma_i32_16x16x64_i8 v[58:61], v[160:163], v[196:199], v[58:61]
	v_mfma_i32_16x16x64_i8 v[46:49], v[152:155], v[204:207], v[46:49]
	v_mfma_i32_16x16x64_i8 v[42:45], v[160:163], v[204:207], v[42:45]
	v_mfma_i32_16x16x64_i8 v[30:33], v[152:155], v[212:215], v[30:33]
	v_mfma_i32_16x16x64_i8 v[26:29], v[160:163], v[212:215], v[26:29]
	v_mfma_i32_16x16x64_i8 v[6:9], v[152:155], v[220:223], v[6:9]
	v_mfma_i32_16x16x64_i8 v[2:5], v[160:163], v[220:223], v[2:5]
	v_mfma_i32_16x16x64_i8 v[62:65], v[156:159], v[200:203], v[62:65]
	v_mfma_i32_16x16x64_i8 v[58:61], v[164:167], v[200:203], v[58:61]
	v_mfma_i32_16x16x64_i8 v[46:49], v[156:159], v[208:211], v[46:49]
	v_mfma_i32_16x16x64_i8 v[42:45], v[164:167], v[208:211], v[42:45]
	v_mfma_i32_16x16x64_i8 v[30:33], v[156:159], v[216:219], v[30:33]
	v_mfma_i32_16x16x64_i8 v[26:29], v[164:167], v[216:219], v[26:29]
	v_mfma_i32_16x16x64_i8 v[6:9], v[156:159], v[224:227], v[6:9]
	v_mfma_i32_16x16x64_i8 v[2:5], v[164:167], v[224:227], v[2:5]
	s_setprio 0
	s_setprio 1
	v_mfma_i32_16x16x64_i8 v[54:57], v[168:171], v[196:199], v[54:57]
	v_mfma_i32_16x16x64_i8 v[50:53], v[186:189], v[196:199], v[50:53]
	v_mfma_i32_16x16x64_i8 v[38:41], v[168:171], v[204:207], v[38:41]
	v_mfma_i32_16x16x64_i8 v[34:37], v[186:189], v[204:207], v[34:37]
	v_mfma_i32_16x16x64_i8 v[14:17], v[168:171], v[212:215], v[14:17]
	v_mfma_i32_16x16x64_i8 v[10:13], v[186:189], v[212:215], v[10:13]
	v_mfma_i32_16x16x64_i8 v[22:25], v[168:171], v[220:223], v[22:25]
	v_mfma_i32_16x16x64_i8 v[18:21], v[186:189], v[220:223], v[18:21]
	v_mfma_i32_16x16x64_i8 v[54:57], v[182:185], v[200:203], v[54:57]
	v_mfma_i32_16x16x64_i8 v[50:53], v[190:193], v[200:203], v[50:53]
	v_mfma_i32_16x16x64_i8 v[38:41], v[182:185], v[208:211], v[38:41]
	v_mfma_i32_16x16x64_i8 v[34:37], v[190:193], v[208:211], v[34:37]
	v_mfma_i32_16x16x64_i8 v[14:17], v[182:185], v[216:219], v[14:17]
	v_mfma_i32_16x16x64_i8 v[10:13], v[190:193], v[216:219], v[10:13]
	v_mfma_i32_16x16x64_i8 v[22:25], v[182:185], v[224:227], v[22:25]
	v_mfma_i32_16x16x64_i8 v[18:21], v[190:193], v[224:227], v[18:21]
	s_setprio 0
	s_barrier
	s_add_i32 s42, 0, 0x18000
	v_add_u32_e32 v1, s42, v173
	s_add_i32 s43, 0, 0x1c000
	ds_read_b128 v[152:155], v1
	ds_read_b128 v[156:159], v1 offset:1024
	ds_read_b128 v[160:163], v1 offset:2048
	ds_read_b128 v[164:167], v1 offset:3072
	v_add_u32_e32 v1, s43, v173
	ds_read_b128 v[168:171], v1
	ds_read_b128 v[182:185], v1 offset:1024
	ds_read_b128 v[186:189], v1 offset:2048
	ds_read_b128 v[190:193], v1 offset:3072
	s_add_u32 s36, s36, 0x40000
	s_addc_u32 s37, s37, 0
	s_mov_b32 m0, s47
	v_lshl_add_u64 v[236:237], s[36:37], 0, v[136:137]
	ds_read_b128 v[196:199], v177 offset:32768
	ds_read_b128 v[200:203], v177 offset:33792
	ds_read_b128 v[204:207], v177 offset:34816
	ds_read_b128 v[208:211], v177 offset:35840
	ds_read_b128 v[212:215], v177 offset:36864
	ds_read_b128 v[216:219], v177 offset:37888
	ds_read_b128 v[220:223], v177 offset:38912
	ds_read_b128 v[224:227], v177 offset:39936
	global_load_lds_dwordx4 v[236:237], off
	v_lshl_add_u64 v[236:237], s[36:37], 0, v[138:139]
	s_mov_b32 m0, s49
	s_nop 0
	global_load_lds_dwordx4 v[236:237], off
	s_waitcnt vmcnt(8) lgkmcnt(0)
	s_barrier
	s_setprio 1
	s_waitcnt lgkmcnt(0)
	v_mfma_i32_16x16x64_i8 v[126:129], v[152:155], v[196:199], v[126:129]
	v_mfma_i32_16x16x64_i8 v[122:125], v[160:163], v[196:199], v[122:125]
	v_mfma_i32_16x16x64_i8 v[110:113], v[152:155], v[204:207], v[110:113]
	v_mfma_i32_16x16x64_i8 v[106:109], v[160:163], v[204:207], v[106:109]
	v_mfma_i32_16x16x64_i8 v[94:97], v[152:155], v[212:215], v[94:97]
	v_mfma_i32_16x16x64_i8 v[90:93], v[160:163], v[212:215], v[90:93]
	v_mfma_i32_16x16x64_i8 v[78:81], v[152:155], v[220:223], v[78:81]
	v_mfma_i32_16x16x64_i8 v[74:77], v[160:163], v[220:223], v[74:77]
	v_mfma_i32_16x16x64_i8 v[126:129], v[156:159], v[200:203], v[126:129]
	v_mfma_i32_16x16x64_i8 v[122:125], v[164:167], v[200:203], v[122:125]
	v_mfma_i32_16x16x64_i8 v[110:113], v[156:159], v[208:211], v[110:113]
	v_mfma_i32_16x16x64_i8 v[106:109], v[164:167], v[208:211], v[106:109]
	v_mfma_i32_16x16x64_i8 v[94:97], v[156:159], v[216:219], v[94:97]
	v_mfma_i32_16x16x64_i8 v[90:93], v[164:167], v[216:219], v[90:93]
	v_mfma_i32_16x16x64_i8 v[78:81], v[156:159], v[224:227], v[78:81]
	v_mfma_i32_16x16x64_i8 v[74:77], v[164:167], v[224:227], v[74:77]
	s_setprio 0
	s_setprio 1
	v_mfma_i32_16x16x64_i8 v[118:121], v[168:171], v[196:199], v[118:121]
	v_mfma_i32_16x16x64_i8 v[114:117], v[186:189], v[196:199], v[114:117]
	v_mfma_i32_16x16x64_i8 v[102:105], v[168:171], v[204:207], v[102:105]
	v_mfma_i32_16x16x64_i8 v[98:101], v[186:189], v[204:207], v[98:101]
	v_mfma_i32_16x16x64_i8 v[86:89], v[168:171], v[212:215], v[86:89]
	v_mfma_i32_16x16x64_i8 v[82:85], v[186:189], v[212:215], v[82:85]
	v_mfma_i32_16x16x64_i8 v[70:73], v[168:171], v[220:223], v[70:73]
	v_mfma_i32_16x16x64_i8 v[66:69], v[186:189], v[220:223], v[66:69]
	v_mfma_i32_16x16x64_i8 v[118:121], v[182:185], v[200:203], v[118:121]
	v_mfma_i32_16x16x64_i8 v[114:117], v[190:193], v[200:203], v[114:117]
	v_mfma_i32_16x16x64_i8 v[102:105], v[182:185], v[208:211], v[102:105]
	v_mfma_i32_16x16x64_i8 v[98:101], v[190:193], v[208:211], v[98:101]
	v_mfma_i32_16x16x64_i8 v[86:89], v[182:185], v[216:219], v[86:89]
	v_mfma_i32_16x16x64_i8 v[82:85], v[190:193], v[216:219], v[82:85]
	v_mfma_i32_16x16x64_i8 v[70:73], v[182:185], v[224:227], v[70:73]
	v_mfma_i32_16x16x64_i8 v[66:69], v[190:193], v[224:227], v[66:69]
	s_setprio 0
	s_barrier
; #define PG8_STAGE(bufoff, gbase, voff) do { _Pragma("unroll") for (int _i = 0; _i < 2; ++_i) \
;         __builtin_amdgcn_global_load_lds((const unsigned*)((const char*)(gbase) + (voff)[_i]), (LAS unsigned*)(lds + (bufoff) + ldsw + _i * 8192), 16, 0, 0); } while (0)
; #define PG8_LDA(dst, b, h) do { _Pragma("unroll") for (int m = 0; m < 4; ++m) dst[m] = PG8_LD32(lds + PG8_SA(b, h) + aoff + m * 2048); } while (0)
; #define PG8_WAIT_V(n) asm volatile("s_waitcnt vmcnt(" #n ")" ::: "memory")
; #define PG8_WAIT_L(n) asm volatile("s_waitcnt lgkmcnt(" #n ")" ::: "memory")
; #define PG8_BAR __builtin_amdgcn_s_barrier()
; #define PG8_SCHED __builtin_amdgcn_sched_barrier(0)
; #define PG8_STA(bufoff, nextflag, h, koff) do { if constexpr (Sched::GATHER) { unsigned _o[2]; _o[0] = (nextflag) ? nxtA[h][0] : curA[h][0]; _o[1] = (nextflag) ? nxtA[h][1] : curA[h][1]; PG8_STAGE(bufoff, Ab + (koff), _o); } \
;         else { PG8_STAGE(bufoff, ((nextflag) ? nA : cA) + (size_t)(h) * hstep + (koff), voffA); } } while (0)
; template <class Epi, class Sched, bool ALIGN_EPI, int DT>
; __device__ __forceinline__ void gemm_phase(LAS unsigned char* lds, const int KB, const Sched& S, const Epi& E) {
;     ...
;             PG8_LDA(At, 1, 1); PG8_STAGE(PG8_SB(1, 0), b3, voffB); PG8_STAGE(PG8_SB(1, 1), b3 + hstep, voffB); PG8_STA(PG8_SA(1, 0), last, 0, k3);
;             PG8_WAIT_V(8); PG8_WAIT_L(0); PG8_BAR; PG8_MMA(1, 0, At, B0); PG8_MMA(1, 1, At, B1); PG8_BAR; PG8_SCHED;
;         }
	s_add_i32 s36, s42, s5
	v_lshl_add_u64 v[228:229], v[228:229], 0, s[18:19]
	s_mov_b32 m0, s36
	ds_read_b128 v[196:199], v177 offset:49152
	ds_read_b128 v[200:203], v177 offset:50176
	ds_read_b128 v[204:207], v177 offset:51200
	ds_read_b128 v[208:211], v177 offset:52224
	ds_read_b128 v[212:215], v177 offset:53248
	ds_read_b128 v[216:219], v177 offset:54272
	ds_read_b128 v[220:223], v177 offset:55296
	ds_read_b128 v[224:227], v177 offset:56320
	global_load_lds_dwordx4 v[228:229], off
	s_add_i32 m0, s36, 0x2000
	s_add_u32 s36, s40, 0x40080
	v_lshl_add_u64 v[228:229], v[230:231], 0, s[18:19]
	s_addc_u32 s37, s41, 0
	s_add_i32 s40, s43, s5
	global_load_lds_dwordx4 v[228:229], off
	v_lshl_add_u64 v[228:229], s[36:37], 0, v[134:135]
	s_mov_b32 m0, s40
	s_nop 0
	global_load_lds_dwordx4 v[228:229], off
	v_lshl_add_u64 v[228:229], s[36:37], 0, v[132:133]
	s_add_i32 m0, s40, 0x2000
	s_nop 0
	global_load_lds_dwordx4 v[228:229], off
	v_lshl_add_u64 v[228:229], v[232:233], 0, s[18:19]
	s_mov_b32 m0, s55
	s_nop 0
	global_load_lds_dwordx4 v[228:229], off
	v_lshl_add_u64 v[228:229], v[234:235], 0, s[18:19]
	s_mov_b32 m0, s56
	s_nop 0
	global_load_lds_dwordx4 v[228:229], off
	s_waitcnt vmcnt(8) lgkmcnt(0)
	s_barrier
	s_setprio 1
	s_waitcnt lgkmcnt(0)
	v_mfma_i32_16x16x64_i8 v[62:65], v[152:155], v[196:199], v[62:65]
	v_mfma_i32_16x16x64_i8 v[58:61], v[160:163], v[196:199], v[58:61]
	v_mfma_i32_16x16x64_i8 v[46:49], v[152:155], v[204:207], v[46:49]
	v_mfma_i32_16x16x64_i8 v[42:45], v[160:163], v[204:207], v[42:45]
	v_mfma_i32_16x16x64_i8 v[30:33], v[152:155], v[212:215], v[30:33]
	v_mfma_i32_16x16x64_i8 v[26:29], v[160:163], v[212:215], v[26:29]
	v_mfma_i32_16x16x64_i8 v[6:9], v[152:155], v[220:223], v[6:9]
	v_mfma_i32_16x16x64_i8 v[2:5], v[160:163], v[220:223], v[2:5]
	v_mfma_i32_16x16x64_i8 v[62:65], v[156:159], v[200:203], v[62:65]
	v_mfma_i32_16x16x64_i8 v[58:61], v[164:167], v[200:203], v[58:61]
	v_mfma_i32_16x16x64_i8 v[46:49], v[156:159], v[208:211], v[46:49]
	v_mfma_i32_16x16x64_i8 v[42:45], v[164:167], v[208:211], v[42:45]
	v_mfma_i32_16x16x64_i8 v[30:33], v[156:159], v[216:219], v[30:33]
	v_mfma_i32_16x16x64_i8 v[26:29], v[164:167], v[216:219], v[26:29]
	v_mfma_i32_16x16x64_i8 v[6:9], v[156:159], v[224:227], v[6:9]
	v_mfma_i32_16x16x64_i8 v[2:5], v[164:167], v[224:227], v[2:5]
	s_setprio 0
	s_setprio 1
	v_mfma_i32_16x16x64_i8 v[54:57], v[168:171], v[196:199], v[54:57]
	v_mfma_i32_16x16x64_i8 v[50:53], v[186:189], v[196:199], v[50:53]
	v_mfma_i32_16x16x64_i8 v[38:41], v[168:171], v[204:207], v[38:41]
	v_mfma_i32_16x16x64_i8 v[34:37], v[186:189], v[204:207], v[34:37]
	v_mfma_i32_16x16x64_i8 v[14:17], v[168:171], v[212:215], v[14:17]
	v_mfma_i32_16x16x64_i8 v[10:13], v[186:189], v[212:215], v[10:13]
	v_mfma_i32_16x16x64_i8 v[22:25], v[168:171], v[220:223], v[22:25]
	v_mfma_i32_16x16x64_i8 v[18:21], v[186:189], v[220:223], v[18:21]
	v_mfma_i32_16x16x64_i8 v[54:57], v[182:185], v[200:203], v[54:57]
	v_mfma_i32_16x16x64_i8 v[50:53], v[190:193], v[200:203], v[50:53]
	v_mfma_i32_16x16x64_i8 v[38:41], v[182:185], v[208:211], v[38:41]
	v_mfma_i32_16x16x64_i8 v[34:37], v[190:193], v[208:211], v[34:37]
	v_mfma_i32_16x16x64_i8 v[14:17], v[182:185], v[216:219], v[14:17]
	v_mfma_i32_16x16x64_i8 v[10:13], v[190:193], v[216:219], v[10:13]
	v_mfma_i32_16x16x64_i8 v[22:25], v[182:185], v[224:227], v[22:25]
	v_mfma_i32_16x16x64_i8 v[18:21], v[190:193], v[224:227], v[18:21]
	s_setprio 0
	s_barrier
	s_add_i32 s67, s67, 2
	s_cmp_gt_u32 s67, 13
	s_mov_b64 s[36:37], s[38:39]
	s_cbranch_scc0 .LBB0_193
	s_and_b64 vcc, exec, s[20:21]
	s_cbranch_vccz .LBB0_196
	s_barrier

; #define PG8_STAGE(bufoff, gbase, voff) do { _Pragma("unroll") for (int _i = 0; _i < 2; ++_i) \
;         __builtin_amdgcn_global_load_lds((const unsigned*)((const char*)(gbase) + (voff)[_i]), (LAS unsigned*)(lds + (bufoff) + ldsw + _i * 8192), 16, 0, 0); } while (0)
; #define PG8_LDA(dst, b, h) do { _Pragma("unroll") for (int m = 0; m < 4; ++m) dst[m] = PG8_LD32(lds + PG8_SA(b, h) + aoff + m * 2048); } while (0)
; #define PG8_LDB(dst, b, h) do { _Pragma("unroll") for (int n = 0; n < 2; ++n) dst[n] = PG8_LD32(lds + PG8_SB(b, h) + boff + n * 2048); } while (0)
; #define PG8_WAIT_V(n) asm volatile("s_waitcnt vmcnt(" #n ")" ::: "memory")
; #define PG8_WAIT_L(n) asm volatile("s_waitcnt lgkmcnt(" #n ")" ::: "memory")
; #define PG8_BAR __builtin_amdgcn_s_barrier()
; #define PG8_SCHED __builtin_amdgcn_sched_barrier(0)
; #define PG8_STA(bufoff, nextflag, h, koff) do { if constexpr (Sched::GATHER) { unsigned _o[2]; _o[0] = (nextflag) ? nxtA[h][0] : curA[h][0]; _o[1] = (nextflag) ? nxtA[h][1] : curA[h][1]; PG8_STAGE(bufoff, Ab + (koff), _o); } \
;         else { PG8_STAGE(bufoff, ((nextflag) ? nA : cA) + (size_t)(h) * hstep + (koff), voffA); } } while (0)
; template <class Epi, class Sched, bool ALIGN_EPI, int DT>
; __device__ __forceinline__ void gemm_phase(LAS unsigned char* lds, const int KB, const Sched& S, const Epi& E) {
;     ...
;             const size_t k1 = (size_t)(t + 1) * kstep, k2 = last ? 0 : (size_t)(t + 2) * kstep, k3 = k2 + kstep;
;             const char* b2 = last ? nB : cB + (size_t)(t + 2) * kstep; const char* b3 = b2 + kstep;
;             PG8_LDB(B0, 0, 0); PG8_LDB(B1, 0, 1); PG8_SCHED; PG8_LDA(At, 0, 0); PG8_STA(PG8_SA(1, 1), false, 1, k1);
;             PG8_WAIT_V(8); PG8_WAIT_L(0); PG8_BAR; PG8_MMA(0, 0, At, B0); PG8_MMA(0, 1, At, B1); PG8_BAR; PG8_SCHED;
;             PG8_LDA(At, 0, 1); PG8_STAGE(PG8_SB(0, 0), b2, voffB); PG8_STAGE(PG8_SB(0, 1), b2 + hstep, voffB); PG8_STA(PG8_SA(0, 0), last, 0, k2);
;             PG8_WAIT_V(8); PG8_WAIT_L(0); PG8_BAR; PG8_MMA(1, 0, At, B0); PG8_MMA(1, 1, At, B1); PG8_BAR; PG8_SCHED;
.LBB0_1018:
	ds_read_b128 v[18:21], v193
	ds_read_b128 v[22:25], v193 offset:1024
	ds_read_b128 v[26:29], v193 offset:2048
	ds_read_b128 v[30:33], v193 offset:3072
	ds_read_b128 v[2:5], v195
	ds_read_b128 v[6:9], v195 offset:1024
	ds_read_b128 v[10:13], v195 offset:2048
	ds_read_b128 v[14:17], v195 offset:3072
	s_add_u32 s34, s38, 0x100
	s_addc_u32 s35, s39, 0
	s_add_u32 s68, s63, s38
	s_addc_u32 s69, s66, s39
	s_cmp_eq_u32 s67, 12
	s_cselect_b64 s[40:41], -1, 0
	s_and_b64 s[36:37], s[40:41], exec
	s_cselect_b32 s37, s21, s69
	s_cselect_b32 s36, s23, s68
	s_cselect_b32 s68, 0, s35
	s_cselect_b32 s69, 0, s34
	v_lshl_add_u64 v[222:223], v[178:179], 0, s[38:39]
	s_add_i32 m0, s29, 0xc000
	ds_read_b128 v[182:185], v196
	ds_read_b128 v[186:189], v196 offset:1024
	ds_read_b128 v[198:201], v196 offset:2048
	ds_read_b128 v[202:205], v196 offset:3072
	ds_read_b128 v[206:209], v196 offset:4096
	ds_read_b128 v[210:213], v196 offset:5120
	ds_read_b128 v[214:217], v196 offset:6144
	ds_read_b128 v[218:221], v196 offset:7168
	global_load_lds_dwordx4 v[222:223], off
	v_lshl_add_u64 v[222:223], v[180:181], 0, s[38:39]
	s_add_i32 m0, s29, 0xe000
	s_nop 0
	global_load_lds_dwordx4 v[222:223], off
	s_waitcnt vmcnt(8) lgkmcnt(0)
	s_barrier
	s_setprio 1
	s_waitcnt lgkmcnt(0)
	v_mfma_scale_f32_16x16x128_f8f6f4 v[158:161], v[18:25], v[182:189], v[158:161], v190, v190 op_sel_hi:[0,0,0]
	v_mfma_scale_f32_16x16x128_f8f6f4 v[154:157], v[26:33], v[182:189], v[154:157], v190, v190 op_sel_hi:[0,0,0]
	v_mfma_scale_f32_16x16x128_f8f6f4 v[150:153], v[18:25], v[198:205], v[150:153], v190, v190 op_sel_hi:[0,0,0]
	v_mfma_scale_f32_16x16x128_f8f6f4 v[142:145], v[26:33], v[198:205], v[142:145], v190, v190 op_sel_hi:[0,0,0]
	v_mfma_scale_f32_16x16x128_f8f6f4 v[134:137], v[18:25], v[206:213], v[134:137], v190, v190 op_sel_hi:[0,0,0]
	v_mfma_scale_f32_16x16x128_f8f6f4 v[126:129], v[26:33], v[206:213], v[126:129], v190, v190 op_sel_hi:[0,0,0]
	v_mfma_scale_f32_16x16x128_f8f6f4 v[118:121], v[18:25], v[214:221], v[118:121], v190, v190 op_sel_hi:[0,0,0]
	v_mfma_scale_f32_16x16x128_f8f6f4 v[110:113], v[26:33], v[214:221], v[110:113], v190, v190 op_sel_hi:[0,0,0]
	s_setprio 0
	s_setprio 1
	v_mfma_scale_f32_16x16x128_f8f6f4 v[146:149], v[2:9], v[182:189], v[146:149], v190, v190 op_sel_hi:[0,0,0]
	v_mfma_scale_f32_16x16x128_f8f6f4 v[138:141], v[10:17], v[182:189], v[138:141], v190, v190 op_sel_hi:[0,0,0]
	v_mfma_scale_f32_16x16x128_f8f6f4 v[130:133], v[2:9], v[198:205], v[130:133], v190, v190 op_sel_hi:[0,0,0]
	v_mfma_scale_f32_16x16x128_f8f6f4 v[122:125], v[10:17], v[198:205], v[122:125], v190, v190 op_sel_hi:[0,0,0]
	v_mfma_scale_f32_16x16x128_f8f6f4 v[114:117], v[2:9], v[206:213], v[114:117], v190, v190 op_sel_hi:[0,0,0]
	v_mfma_scale_f32_16x16x128_f8f6f4 v[106:109], v[10:17], v[206:213], v[106:109], v190, v190 op_sel_hi:[0,0,0]
	v_mfma_scale_f32_16x16x128_f8f6f4 v[102:105], v[2:9], v[214:221], v[102:105], v190, v190 op_sel_hi:[0,0,0]
	v_mfma_scale_f32_16x16x128_f8f6f4 v[98:101], v[10:17], v[214:221], v[98:101], v190, v190 op_sel_hi:[0,0,0]
	s_setprio 0
	s_barrier
	s_add_i32 s38, s53, s42
	v_lshl_add_u64 v[182:183], s[36:37], 0, v[162:163]
	s_mov_b32 m0, s38
	ds_read_b128 v[198:201], v196 offset:16384
	ds_read_b128 v[202:205], v196 offset:17408
	ds_read_b128 v[206:209], v196 offset:18432
	ds_read_b128 v[210:213], v196 offset:19456
	ds_read_b128 v[214:217], v196 offset:20480
	ds_read_b128 v[218:221], v196 offset:21504
	ds_read_b128 v[222:225], v196 offset:22528
	ds_read_b128 v[226:229], v196 offset:23552
	global_load_lds_dwordx4 v[182:183], off
	s_add_i32 m0, s38, 0x2000
	s_add_u32 s38, s36, 0x40000
	v_lshl_add_u64 v[184:185], s[36:37], 0, v[164:165]
	s_addc_u32 s39, s37, 0
	s_add_i32 s70, s54, s42
	global_load_lds_dwordx4 v[184:185], off
	v_lshl_add_u64 v[186:187], s[38:39], 0, v[162:163]
	s_mov_b32 m0, s70
	s_nop 0
	global_load_lds_dwordx4 v[186:187], off
	v_lshl_add_u64 v[186:187], s[38:39], 0, v[164:165]
	s_add_i32 m0, s70, 0x2000
	s_and_b64 s[38:39], s[6:7], s[40:41]
	s_and_b64 s[38:39], s[38:39], exec
	s_cselect_b32 s38, s24, s30
	s_cselect_b32 s39, s25, s31
	s_add_u32 s38, s38, s69
	s_addc_u32 s39, s39, s68
	global_load_lds_dwordx4 v[186:187], off
	v_lshl_add_u64 v[186:187], s[38:39], 0, v[166:167]
	s_mov_b32 m0, s29
	v_lshl_add_u64 v[188:189], s[38:39], 0, v[168:169]
	global_load_lds_dwordx4 v[186:187], off
	s_mov_b32 m0, s43
	s_nop 0
	global_load_lds_dwordx4 v[188:189], off
	s_waitcnt vmcnt(8) lgkmcnt(0)
	s_barrier
	s_setprio 1
	s_waitcnt lgkmcnt(0)
	v_mfma_scale_f32_16x16x128_f8f6f4 v[94:97], v[18:25], v[198:205], v[94:97], v190, v190 op_sel_hi:[0,0,0]
	v_mfma_scale_f32_16x16x128_f8f6f4 v[90:93], v[26:33], v[198:205], v[90:93], v190, v190 op_sel_hi:[0,0,0]
	v_mfma_scale_f32_16x16x128_f8f6f4 v[86:89], v[18:25], v[206:213], v[86:89], v190, v190 op_sel_hi:[0,0,0]
	v_mfma_scale_f32_16x16x128_f8f6f4 v[78:81], v[26:33], v[206:213], v[78:81], v190, v190 op_sel_hi:[0,0,0]
	v_mfma_scale_f32_16x16x128_f8f6f4 v[62:65], v[18:25], v[214:221], v[62:65], v190, v190 op_sel_hi:[0,0,0]
	v_mfma_scale_f32_16x16x128_f8f6f4 v[54:57], v[26:33], v[214:221], v[54:57], v190, v190 op_sel_hi:[0,0,0]
	v_mfma_scale_f32_16x16x128_f8f6f4 v[46:49], v[18:25], v[222:229], v[46:49], v190, v190 op_sel_hi:[0,0,0]
	v_mfma_scale_f32_16x16x128_f8f6f4 v[38:41], v[26:33], v[222:229], v[38:41], v190, v190 op_sel_hi:[0,0,0]
	s_setprio 0
	s_setprio 1
	v_mfma_scale_f32_16x16x128_f8f6f4 v[82:85], v[2:9], v[198:205], v[82:85], v190, v190 op_sel_hi:[0,0,0]
	v_mfma_scale_f32_16x16x128_f8f6f4 v[74:77], v[10:17], v[198:205], v[74:77], v190, v190 op_sel_hi:[0,0,0]
	v_mfma_scale_f32_16x16x128_f8f6f4 v[58:61], v[2:9], v[206:213], v[58:61], v190, v190 op_sel_hi:[0,0,0]
	v_mfma_scale_f32_16x16x128_f8f6f4 v[50:53], v[10:17], v[206:213], v[50:53], v190, v190 op_sel_hi:[0,0,0]
	v_mfma_scale_f32_16x16x128_f8f6f4 v[42:45], v[2:9], v[214:221], v[42:45], v190, v190 op_sel_hi:[0,0,0]
	v_mfma_scale_f32_16x16x128_f8f6f4 v[34:37], v[10:17], v[214:221], v[34:37], v190, v190 op_sel_hi:[0,0,0]
	v_mfma_scale_f32_16x16x128_f8f6f4 v[70:73], v[2:9], v[222:229], v[70:73], v190, v190 op_sel_hi:[0,0,0]
	v_mfma_scale_f32_16x16x128_f8f6f4 v[66:69], v[10:17], v[222:229], v[66:69], v190, v190 op_sel_hi:[0,0,0]
	s_setprio 0
	s_barrier
; #define PG8_STAGE(bufoff, gbase, voff) do { _Pragma("unroll") for (int _i = 0; _i < 2; ++_i) \
;         __builtin_amdgcn_global_load_lds((const unsigned*)((const char*)(gbase) + (voff)[_i]), (LAS unsigned*)(lds + (bufoff) + ldsw + _i * 8192), 16, 0, 0); } while (0)
; #define PG8_LDA(dst, b, h) do { _Pragma("unroll") for (int m = 0; m < 4; ++m) dst[m] = PG8_LD32(lds + PG8_SA(b, h) + aoff + m * 2048); } while (0)
; #define PG8_LDB(dst, b, h) do { _Pragma("unroll") for (int n = 0; n < 2; ++n) dst[n] = PG8_LD32(lds + PG8_SB(b, h) + boff + n * 2048); } while (0)
; #define PG8_WAIT_V(n) asm volatile("s_waitcnt vmcnt(" #n ")" ::: "memory")
; #define PG8_WAIT_L(n) asm volatile("s_waitcnt lgkmcnt(" #n ")" ::: "memory")
; #define PG8_BAR __builtin_amdgcn_s_barrier()
; #define PG8_SCHED __builtin_amdgcn_sched_barrier(0)
; #define PG8_STA(bufoff, nextflag, h, koff) do { if constexpr (Sched::GATHER) { unsigned _o[2]; _o[0] = (nextflag) ? nxtA[h][0] : curA[h][0]; _o[1] = (nextflag) ? nxtA[h][1] : curA[h][1]; PG8_STAGE(bufoff, Ab + (koff), _o); } \
;         else { PG8_STAGE(bufoff, ((nextflag) ? nA : cA) + (size_t)(h) * hstep + (koff), voffA); } } while (0)
; template <class Epi, class Sched, bool ALIGN_EPI, int DT>
; __device__ __forceinline__ void gemm_phase(LAS unsigned char* lds, const int KB, const Sched& S, const Epi& E) {
;     ...
;             PG8_LDB(B0, 1, 0); PG8_LDB(B1, 1, 1); PG8_SCHED; PG8_LDA(At, 1, 0); PG8_STA(PG8_SA(0, 1), last, 1, k2);
;             PG8_WAIT_V(8); PG8_WAIT_L(0); PG8_BAR; PG8_MMA(0, 0, At, B0); PG8_MMA(0, 1, At, B1); PG8_BAR; PG8_SCHED;
;             PG8_LDA(At, 1, 1); PG8_STAGE(PG8_SB(1, 0), b3, voffB); PG8_STAGE(PG8_SB(1, 1), b3 + hstep, voffB); PG8_STA(PG8_SA(1, 0), last, 0, k3);
;             PG8_WAIT_V(8); PG8_WAIT_L(0); PG8_BAR; PG8_MMA(1, 0, At, B0); PG8_MMA(1, 1, At, B1); PG8_BAR; PG8_SCHED;
;         }
;         if constexpr (ALIGN_EPI) { if (wr == 0) PG8_BAR; }
	s_add_i32 s40, 0, 0x18000
	s_add_i32 s41, 0, 0x1c000
	v_add_u32_e32 v14, s40, v191
	v_add_u32_e32 v30, s41, v191
	ds_read_b128 v[2:5], v14
	ds_read_b128 v[6:9], v14 offset:1024
	ds_read_b128 v[10:13], v14 offset:2048
	ds_read_b128 v[14:17], v14 offset:3072
	ds_read_b128 v[18:21], v30
	ds_read_b128 v[22:25], v30 offset:1024
	ds_read_b128 v[26:29], v30 offset:2048
	ds_read_b128 v[30:33], v30 offset:3072
	s_add_u32 s38, s38, 0x40000
	s_addc_u32 s39, s39, 0
	s_mov_b32 m0, s44
	v_lshl_add_u64 v[230:231], s[38:39], 0, v[166:167]
	ds_read_b128 v[198:201], v196 offset:32768
	ds_read_b128 v[202:205], v196 offset:33792
	ds_read_b128 v[206:209], v196 offset:34816
	ds_read_b128 v[210:213], v196 offset:35840
	ds_read_b128 v[214:217], v196 offset:36864
	ds_read_b128 v[218:221], v196 offset:37888
	ds_read_b128 v[222:225], v196 offset:38912
	ds_read_b128 v[226:229], v196 offset:39936
	global_load_lds_dwordx4 v[230:231], off
	v_lshl_add_u64 v[230:231], s[38:39], 0, v[168:169]
	s_mov_b32 m0, s45
	s_nop 0
	global_load_lds_dwordx4 v[230:231], off
	s_waitcnt vmcnt(8) lgkmcnt(0)
	s_barrier
	s_setprio 1
	s_waitcnt lgkmcnt(0)
	v_mfma_scale_f32_16x16x128_f8f6f4 v[158:161], v[2:9], v[198:205], v[158:161], v190, v190 op_sel_hi:[0,0,0]
	v_mfma_scale_f32_16x16x128_f8f6f4 v[154:157], v[10:17], v[198:205], v[154:157], v190, v190 op_sel_hi:[0,0,0]
	v_mfma_scale_f32_16x16x128_f8f6f4 v[150:153], v[2:9], v[206:213], v[150:153], v190, v190 op_sel_hi:[0,0,0]
	v_mfma_scale_f32_16x16x128_f8f6f4 v[142:145], v[10:17], v[206:213], v[142:145], v190, v190 op_sel_hi:[0,0,0]
	v_mfma_scale_f32_16x16x128_f8f6f4 v[134:137], v[2:9], v[214:221], v[134:137], v190, v190 op_sel_hi:[0,0,0]
	v_mfma_scale_f32_16x16x128_f8f6f4 v[126:129], v[10:17], v[214:221], v[126:129], v190, v190 op_sel_hi:[0,0,0]
	v_mfma_scale_f32_16x16x128_f8f6f4 v[118:121], v[2:9], v[222:229], v[118:121], v190, v190 op_sel_hi:[0,0,0]
	v_mfma_scale_f32_16x16x128_f8f6f4 v[110:113], v[10:17], v[222:229], v[110:113], v190, v190 op_sel_hi:[0,0,0]
	s_setprio 0
	s_setprio 1
	v_mfma_scale_f32_16x16x128_f8f6f4 v[146:149], v[18:25], v[198:205], v[146:149], v190, v190 op_sel_hi:[0,0,0]
	v_mfma_scale_f32_16x16x128_f8f6f4 v[138:141], v[26:33], v[198:205], v[138:141], v190, v190 op_sel_hi:[0,0,0]
	v_mfma_scale_f32_16x16x128_f8f6f4 v[130:133], v[18:25], v[206:213], v[130:133], v190, v190 op_sel_hi:[0,0,0]
	v_mfma_scale_f32_16x16x128_f8f6f4 v[122:125], v[26:33], v[206:213], v[122:125], v190, v190 op_sel_hi:[0,0,0]
	v_mfma_scale_f32_16x16x128_f8f6f4 v[114:117], v[18:25], v[214:221], v[114:117], v190, v190 op_sel_hi:[0,0,0]
	v_mfma_scale_f32_16x16x128_f8f6f4 v[106:109], v[26:33], v[214:221], v[106:109], v190, v190 op_sel_hi:[0,0,0]
	v_mfma_scale_f32_16x16x128_f8f6f4 v[102:105], v[18:25], v[222:229], v[102:105], v190, v190 op_sel_hi:[0,0,0]
	v_mfma_scale_f32_16x16x128_f8f6f4 v[98:101], v[26:33], v[222:229], v[98:101], v190, v190 op_sel_hi:[0,0,0]
	s_setprio 0
	s_barrier
	s_add_i32 s38, s40, s42
	v_lshl_add_u64 v[182:183], v[182:183], 0, s[10:11]
	s_mov_b32 m0, s38
	ds_read_b128 v[198:201], v196 offset:49152
	ds_read_b128 v[202:205], v196 offset:50176
	ds_read_b128 v[206:209], v196 offset:51200
	ds_read_b128 v[210:213], v196 offset:52224
	ds_read_b128 v[214:217], v196 offset:53248
	ds_read_b128 v[218:221], v196 offset:54272
	ds_read_b128 v[222:225], v196 offset:55296
	ds_read_b128 v[226:229], v196 offset:56320
	global_load_lds_dwordx4 v[182:183], off
	s_add_i32 m0, s38, 0x2000
	s_add_u32 s36, s36, 0x40080
	v_lshl_add_u64 v[182:183], v[184:185], 0, s[10:11]
	s_addc_u32 s37, s37, 0
	s_add_i32 s38, s41, s42
	global_load_lds_dwordx4 v[182:183], off
	v_lshl_add_u64 v[182:183], s[36:37], 0, v[162:163]
	s_mov_b32 m0, s38
	s_nop 0
	global_load_lds_dwordx4 v[182:183], off
	v_lshl_add_u64 v[182:183], s[36:37], 0, v[164:165]
	s_add_i32 m0, s38, 0x2000
	s_nop 0
	global_load_lds_dwordx4 v[182:183], off
	v_lshl_add_u64 v[182:183], v[186:187], 0, s[10:11]
	s_mov_b32 m0, s47
	s_nop 0
	global_load_lds_dwordx4 v[182:183], off
	v_lshl_add_u64 v[182:183], v[188:189], 0, s[10:11]
	s_mov_b32 m0, s49
	s_nop 0
	global_load_lds_dwordx4 v[182:183], off
	s_waitcnt vmcnt(8) lgkmcnt(0)
	s_barrier
	s_setprio 1
	s_waitcnt lgkmcnt(0)
	v_mfma_scale_f32_16x16x128_f8f6f4 v[94:97], v[2:9], v[198:205], v[94:97], v190, v190 op_sel_hi:[0,0,0]
	v_mfma_scale_f32_16x16x128_f8f6f4 v[90:93], v[10:17], v[198:205], v[90:93], v190, v190 op_sel_hi:[0,0,0]
	v_mfma_scale_f32_16x16x128_f8f6f4 v[86:89], v[2:9], v[206:213], v[86:89], v190, v190 op_sel_hi:[0,0,0]
	v_mfma_scale_f32_16x16x128_f8f6f4 v[78:81], v[10:17], v[206:213], v[78:81], v190, v190 op_sel_hi:[0,0,0]
	v_mfma_scale_f32_16x16x128_f8f6f4 v[62:65], v[2:9], v[214:221], v[62:65], v190, v190 op_sel_hi:[0,0,0]
	v_mfma_scale_f32_16x16x128_f8f6f4 v[54:57], v[10:17], v[214:221], v[54:57], v190, v190 op_sel_hi:[0,0,0]
	v_mfma_scale_f32_16x16x128_f8f6f4 v[46:49], v[2:9], v[222:229], v[46:49], v190, v190 op_sel_hi:[0,0,0]
	v_mfma_scale_f32_16x16x128_f8f6f4 v[38:41], v[10:17], v[222:229], v[38:41], v190, v190 op_sel_hi:[0,0,0]
	s_setprio 0
	s_setprio 1
	v_mfma_scale_f32_16x16x128_f8f6f4 v[82:85], v[18:25], v[198:205], v[82:85], v190, v190 op_sel_hi:[0,0,0]
	v_mfma_scale_f32_16x16x128_f8f6f4 v[74:77], v[26:33], v[198:205], v[74:77], v190, v190 op_sel_hi:[0,0,0]
	v_mfma_scale_f32_16x16x128_f8f6f4 v[58:61], v[18:25], v[206:213], v[58:61], v190, v190 op_sel_hi:[0,0,0]
	v_mfma_scale_f32_16x16x128_f8f6f4 v[50:53], v[26:33], v[206:213], v[50:53], v190, v190 op_sel_hi:[0,0,0]
	v_mfma_scale_f32_16x16x128_f8f6f4 v[42:45], v[18:25], v[214:221], v[42:45], v190, v190 op_sel_hi:[0,0,0]
	v_mfma_scale_f32_16x16x128_f8f6f4 v[34:37], v[26:33], v[214:221], v[34:37], v190, v190 op_sel_hi:[0,0,0]
	v_mfma_scale_f32_16x16x128_f8f6f4 v[70:73], v[18:25], v[222:229], v[70:73], v190, v190 op_sel_hi:[0,0,0]
	v_mfma_scale_f32_16x16x128_f8f6f4 v[66:69], v[26:33], v[222:229], v[66:69], v190, v190 op_sel_hi:[0,0,0]
	s_setprio 0
	s_barrier
	s_add_i32 s67, s67, 2
	s_cmp_gt_u32 s67, 13
	s_mov_b64 s[38:39], s[34:35]
	s_cbranch_scc0 .LBB0_1018
	s_and_b64 vcc, exec, s[12:13]
	s_cbranch_vccz .LBB0_1021
	s_barrier

; #define PG8_STAGE(bufoff, gbase, voff) do { _Pragma("unroll") for (int _i = 0; _i < 2; ++_i) \
;         __builtin_amdgcn_global_load_lds((const unsigned*)((const char*)(gbase) + (voff)[_i]), (LAS unsigned*)(lds + (bufoff) + ldsw + _i * 8192), 16, 0, 0); } while (0)
; #define PG8_LDA(dst, b, h) do { _Pragma("unroll") for (int m = 0; m < 4; ++m) dst[m] = PG8_LD32(lds + PG8_SA(b, h) + aoff + m * 2048); } while (0)
; #define PG8_LDB(dst, b, h) do { _Pragma("unroll") for (int n = 0; n < 2; ++n) dst[n] = PG8_LD32(lds + PG8_SB(b, h) + boff + n * 2048); } while (0)
; #define PG8_WAIT_V(n) asm volatile("s_waitcnt vmcnt(" #n ")" ::: "memory")
; #define PG8_WAIT_L(n) asm volatile("s_waitcnt lgkmcnt(" #n ")" ::: "memory")
; #define PG8_BAR __builtin_amdgcn_s_barrier()
; #define PG8_SCHED __builtin_amdgcn_sched_barrier(0)
; #define PG8_STA(bufoff, nextflag, h, koff) do { if constexpr (Sched::GATHER) { unsigned _o[2]; _o[0] = (nextflag) ? nxtA[h][0] : curA[h][0]; _o[1] = (nextflag) ? nxtA[h][1] : curA[h][1]; PG8_STAGE(bufoff, Ab + (koff), _o); } \
;         else { PG8_STAGE(bufoff, ((nextflag) ? nA : cA) + (size_t)(h) * hstep + (koff), voffA); } } while (0)
; template <class Epi, class Sched, bool ALIGN_EPI, int DT>
; __device__ __forceinline__ void gemm_phase(LAS unsigned char* lds, const int KB, const Sched& S, const Epi& E) {
;     ...
;             PG8_LDB(B0, 0, 0); PG8_LDB(B1, 0, 1); PG8_SCHED; PG8_LDA(At, 0, 0); PG8_STA(PG8_SA(1, 1), false, 1, k1);
;             PG8_WAIT_V(8); PG8_WAIT_L(0); PG8_BAR; PG8_MMA(0, 0, At, B0); PG8_MMA(0, 1, At, B1); PG8_BAR; PG8_SCHED;
;             PG8_LDA(At, 0, 1); PG8_STAGE(PG8_SB(0, 0), b2, voffB); PG8_STAGE(PG8_SB(0, 1), b2 + hstep, voffB); PG8_STA(PG8_SA(0, 0), last, 0, k2);
;             PG8_WAIT_V(8); PG8_WAIT_L(0); PG8_BAR; PG8_MMA(1, 0, At, B0); PG8_MMA(1, 1, At, B1); PG8_BAR; PG8_SCHED;
.LBB0_1154:
	ds_read_b128 v[70:73], v167
	ds_read_b128 v[156:159], v167 offset:1024
	ds_read_b128 v[160:163], v167 offset:2048
	ds_read_b128 v[172:175], v167 offset:3072
	ds_read_b128 v[176:179], v168
	ds_read_b128 v[180:183], v168 offset:1024
	ds_read_b128 v[184:187], v168 offset:2048
	ds_read_b128 v[188:191], v168 offset:3072
	s_add_u32 s30, s28, 0x100
	s_addc_u32 s31, s29, 0
	s_add_u32 s63, s56, s28
	s_addc_u32 s66, s57, s29
	s_cmp_eq_u32 s62, 12
	s_cselect_b64 s[36:37], -1, 0
	s_and_b64 s[34:35], s[36:37], exec
	s_cselect_b32 s67, 0, s30
	s_cselect_b32 s35, s17, s66
	s_cselect_b32 s34, s19, s63
	v_lshl_add_u64 v[192:193], v[66:67], 0, s[28:29]
	s_add_i32 m0, s25, 0xc000
	ds_read_b128 v[196:199], v169
	ds_read_b128 v[200:203], v169 offset:1024
	ds_read_b128 v[204:207], v169 offset:2048
	ds_read_b128 v[208:211], v169 offset:3072
	ds_read_b128 v[212:215], v169 offset:4096
	ds_read_b128 v[216:219], v169 offset:5120
	ds_read_b128 v[220:223], v169 offset:6144
	ds_read_b128 v[224:227], v169 offset:7168
	global_load_lds_dwordx4 v[192:193], off
	v_lshl_add_u64 v[192:193], v[68:69], 0, s[28:29]
	s_add_i32 m0, s25, 0xe000
	s_nop 0
	global_load_lds_dwordx4 v[192:193], off
	s_waitcnt vmcnt(8) lgkmcnt(0)
	s_barrier
	s_setprio 1
	s_waitcnt lgkmcnt(0)
	v_mfma_i32_16x16x64_i8 v[134:137], v[70:73], v[196:199], v[134:137]
	v_mfma_i32_16x16x64_i8 v[126:129], v[160:163], v[196:199], v[126:129]
	v_mfma_i32_16x16x64_i8 v[118:121], v[70:73], v[204:207], v[118:121]
	v_mfma_i32_16x16x64_i8 v[110:113], v[160:163], v[204:207], v[110:113]
	v_mfma_i32_16x16x64_i8 v[102:105], v[70:73], v[212:215], v[102:105]
	v_mfma_i32_16x16x64_i8 v[94:97], v[160:163], v[212:215], v[94:97]
	v_mfma_i32_16x16x64_i8 v[86:89], v[70:73], v[220:223], v[86:89]
	v_mfma_i32_16x16x64_i8 v[78:81], v[160:163], v[220:223], v[78:81]
	v_mfma_i32_16x16x64_i8 v[134:137], v[156:159], v[200:203], v[134:137]
	v_mfma_i32_16x16x64_i8 v[126:129], v[172:175], v[200:203], v[126:129]
	v_mfma_i32_16x16x64_i8 v[118:121], v[156:159], v[208:211], v[118:121]
	v_mfma_i32_16x16x64_i8 v[110:113], v[172:175], v[208:211], v[110:113]
	v_mfma_i32_16x16x64_i8 v[102:105], v[156:159], v[216:219], v[102:105]
	v_mfma_i32_16x16x64_i8 v[94:97], v[172:175], v[216:219], v[94:97]
	v_mfma_i32_16x16x64_i8 v[86:89], v[156:159], v[224:227], v[86:89]
	v_mfma_i32_16x16x64_i8 v[78:81], v[172:175], v[224:227], v[78:81]
	s_setprio 0
	s_setprio 1
	v_mfma_i32_16x16x64_i8 v[130:133], v[176:179], v[196:199], v[130:133]
	v_mfma_i32_16x16x64_i8 v[122:125], v[184:187], v[196:199], v[122:125]
	v_mfma_i32_16x16x64_i8 v[114:117], v[176:179], v[204:207], v[114:117]
	v_mfma_i32_16x16x64_i8 v[106:109], v[184:187], v[204:207], v[106:109]
	v_mfma_i32_16x16x64_i8 v[98:101], v[176:179], v[212:215], v[98:101]
	v_mfma_i32_16x16x64_i8 v[90:93], v[184:187], v[212:215], v[90:93]
	v_mfma_i32_16x16x64_i8 v[82:85], v[176:179], v[220:223], v[82:85]
	v_mfma_i32_16x16x64_i8 v[74:77], v[184:187], v[220:223], v[74:77]
	v_mfma_i32_16x16x64_i8 v[130:133], v[180:183], v[200:203], v[130:133]
	v_mfma_i32_16x16x64_i8 v[122:125], v[188:191], v[200:203], v[122:125]
	v_mfma_i32_16x16x64_i8 v[114:117], v[180:183], v[208:211], v[114:117]
	v_mfma_i32_16x16x64_i8 v[106:109], v[188:191], v[208:211], v[106:109]
	v_mfma_i32_16x16x64_i8 v[98:101], v[180:183], v[216:219], v[98:101]
	v_mfma_i32_16x16x64_i8 v[90:93], v[188:191], v[216:219], v[90:93]
	v_mfma_i32_16x16x64_i8 v[82:85], v[180:183], v[224:227], v[82:85]
	v_mfma_i32_16x16x64_i8 v[74:77], v[188:191], v[224:227], v[74:77]
	s_setprio 0
	s_barrier
	s_add_i32 s28, s49, s38
	v_lshl_add_u64 v[192:193], s[34:35], 0, v[140:141]
	s_mov_b32 m0, s28
	ds_read_b128 v[196:199], v169 offset:16384
	ds_read_b128 v[200:203], v169 offset:17408
	ds_read_b128 v[204:207], v169 offset:18432
	ds_read_b128 v[208:211], v169 offset:19456
	ds_read_b128 v[212:215], v169 offset:20480
	ds_read_b128 v[216:219], v169 offset:21504
	ds_read_b128 v[220:223], v169 offset:22528
	ds_read_b128 v[224:227], v169 offset:23552
	global_load_lds_dwordx4 v[192:193], off
	s_add_i32 m0, s28, 0x2000
	s_add_u32 s28, s34, 0x40000
	v_lshl_add_u64 v[228:229], s[34:35], 0, v[138:139]
	s_addc_u32 s29, s35, 0
	s_add_i32 s63, s52, s38
	global_load_lds_dwordx4 v[228:229], off
	v_lshl_add_u64 v[230:231], s[28:29], 0, v[140:141]
	s_mov_b32 m0, s63
	s_nop 0
	global_load_lds_dwordx4 v[230:231], off
	v_lshl_add_u64 v[230:231], s[28:29], 0, v[138:139]
	s_add_i32 m0, s63, 0x2000
	s_and_b64 s[28:29], s[6:7], s[36:37]
	s_and_b64 s[28:29], s[28:29], exec
	s_cselect_b32 s28, s20, s26
	s_cselect_b32 s29, s21, s27
	s_add_u32 s28, s28, s67
	s_addc_u32 s29, s29, 0
	global_load_lds_dwordx4 v[230:231], off
	v_lshl_add_u64 v[230:231], s[28:29], 0, v[142:143]
	s_mov_b32 m0, s25
	v_lshl_add_u64 v[232:233], s[28:29], 0, v[144:145]
	global_load_lds_dwordx4 v[230:231], off
	s_mov_b32 m0, s41
	s_nop 0
	global_load_lds_dwordx4 v[232:233], off
	s_waitcnt vmcnt(8) lgkmcnt(0)
	s_barrier
; #define PG8_LDA(dst, b, h) do { _Pragma("unroll") for (int m = 0; m < 4; ++m) dst[m] = PG8_LD32(lds + PG8_SA(b, h) + aoff + m * 2048); } while (0)
; #define PG8_LDB(dst, b, h) do { _Pragma("unroll") for (int n = 0; n < 2; ++n) dst[n] = PG8_LD32(lds + PG8_SB(b, h) + boff + n * 2048); } while (0)
; #define PG8_WAIT_V(n) asm volatile("s_waitcnt vmcnt(" #n ")" ::: "memory")
; #define PG8_WAIT_L(n) asm volatile("s_waitcnt lgkmcnt(" #n ")" ::: "memory")
; #define PG8_BAR __builtin_amdgcn_s_barrier()
; #define PG8_SCHED __builtin_amdgcn_sched_barrier(0)
; #define PG8_STA(bufoff, nextflag, h, koff) do { if constexpr (Sched::GATHER) { unsigned _o[2]; _o[0] = (nextflag) ? nxtA[h][0] : curA[h][0]; _o[1] = (nextflag) ? nxtA[h][1] : curA[h][1]; PG8_STAGE(bufoff, Ab + (koff), _o); } \
;         else { PG8_STAGE(bufoff, ((nextflag) ? nA : cA) + (size_t)(h) * hstep + (koff), voffA); } } while (0)
; template <class Epi, class Sched, bool ALIGN_EPI, int DT>
; __device__ __forceinline__ void gemm_phase(LAS unsigned char* lds, const int KB, const Sched& S, const Epi& E) {
;     ...
;             PG8_WAIT_V(8); PG8_WAIT_L(0); PG8_BAR; PG8_MMA(1, 0, At, B0); PG8_MMA(1, 1, At, B1); PG8_BAR; PG8_SCHED;
;             PG8_LDB(B0, 1, 0); PG8_LDB(B1, 1, 1); PG8_SCHED; PG8_LDA(At, 1, 0); PG8_STA(PG8_SA(0, 1), last, 1, k2);
;             PG8_WAIT_V(8); PG8_WAIT_L(0); PG8_BAR; PG8_MMA(0, 0, At, B0); PG8_MMA(0, 1, At, B1); PG8_BAR; PG8_SCHED;
	s_setprio 1
	s_waitcnt lgkmcnt(0)
	v_mfma_i32_16x16x64_i8 v[62:65], v[70:73], v[196:199], v[62:65]
	v_mfma_i32_16x16x64_i8 v[54:57], v[160:163], v[196:199], v[54:57]
	v_mfma_i32_16x16x64_i8 v[46:49], v[70:73], v[204:207], v[46:49]
	v_mfma_i32_16x16x64_i8 v[38:41], v[160:163], v[204:207], v[38:41]
	v_mfma_i32_16x16x64_i8 v[30:33], v[70:73], v[212:215], v[30:33]
	v_mfma_i32_16x16x64_i8 v[22:25], v[160:163], v[212:215], v[22:25]
	v_mfma_i32_16x16x64_i8 v[6:9], v[70:73], v[220:223], v[6:9]
	v_mfma_i32_16x16x64_i8 v[2:5], v[160:163], v[220:223], v[2:5]
	v_mfma_i32_16x16x64_i8 v[62:65], v[156:159], v[200:203], v[62:65]
	v_mfma_i32_16x16x64_i8 v[54:57], v[172:175], v[200:203], v[54:57]
	v_mfma_i32_16x16x64_i8 v[46:49], v[156:159], v[208:211], v[46:49]
	v_mfma_i32_16x16x64_i8 v[38:41], v[172:175], v[208:211], v[38:41]
	v_mfma_i32_16x16x64_i8 v[30:33], v[156:159], v[216:219], v[30:33]
	v_mfma_i32_16x16x64_i8 v[22:25], v[172:175], v[216:219], v[22:25]
	v_mfma_i32_16x16x64_i8 v[6:9], v[156:159], v[224:227], v[6:9]
	v_mfma_i32_16x16x64_i8 v[2:5], v[172:175], v[224:227], v[2:5]
	s_setprio 0
	s_setprio 1
	v_mfma_i32_16x16x64_i8 v[58:61], v[176:179], v[196:199], v[58:61]
	v_mfma_i32_16x16x64_i8 v[50:53], v[184:187], v[196:199], v[50:53]
	v_mfma_i32_16x16x64_i8 v[42:45], v[176:179], v[204:207], v[42:45]
	v_mfma_i32_16x16x64_i8 v[34:37], v[184:187], v[204:207], v[34:37]
	v_mfma_i32_16x16x64_i8 v[26:29], v[176:179], v[212:215], v[26:29]
	v_mfma_i32_16x16x64_i8 v[18:21], v[184:187], v[212:215], v[18:21]
	v_mfma_i32_16x16x64_i8 v[14:17], v[176:179], v[220:223], v[14:17]
	v_mfma_i32_16x16x64_i8 v[10:13], v[184:187], v[220:223], v[10:13]
	v_mfma_i32_16x16x64_i8 v[58:61], v[180:183], v[200:203], v[58:61]
	v_mfma_i32_16x16x64_i8 v[50:53], v[188:191], v[200:203], v[50:53]
	v_mfma_i32_16x16x64_i8 v[42:45], v[180:183], v[208:211], v[42:45]
	v_mfma_i32_16x16x64_i8 v[34:37], v[188:191], v[208:211], v[34:37]
	v_mfma_i32_16x16x64_i8 v[26:29], v[180:183], v[216:219], v[26:29]
	v_mfma_i32_16x16x64_i8 v[18:21], v[188:191], v[216:219], v[18:21]
	v_mfma_i32_16x16x64_i8 v[14:17], v[180:183], v[224:227], v[14:17]
	v_mfma_i32_16x16x64_i8 v[10:13], v[188:191], v[224:227], v[10:13]
	s_setprio 0
	s_barrier
	s_add_i32 s36, 0, 0x18000
	v_add_u32_e32 v1, s36, v165
	s_add_i32 s37, 0, 0x1c000
	ds_read_b128 v[70:73], v1
	ds_read_b128 v[156:159], v1 offset:1024
	ds_read_b128 v[160:163], v1 offset:2048
	ds_read_b128 v[172:175], v1 offset:3072
	v_add_u32_e32 v1, s37, v165
	ds_read_b128 v[176:179], v1
	ds_read_b128 v[180:183], v1 offset:1024
	ds_read_b128 v[184:187], v1 offset:2048
	ds_read_b128 v[188:191], v1 offset:3072
	s_add_u32 s28, s28, 0x40000
	s_addc_u32 s29, s29, 0
	s_mov_b32 m0, s42
	v_lshl_add_u64 v[234:235], s[28:29], 0, v[142:143]
	ds_read_b128 v[196:199], v169 offset:32768
	ds_read_b128 v[200:203], v169 offset:33792
	ds_read_b128 v[204:207], v169 offset:34816
	ds_read_b128 v[208:211], v169 offset:35840
	ds_read_b128 v[212:215], v169 offset:36864
	ds_read_b128 v[216:219], v169 offset:37888
	ds_read_b128 v[220:223], v169 offset:38912
	ds_read_b128 v[224:227], v169 offset:39936
	global_load_lds_dwordx4 v[234:235], off
	v_lshl_add_u64 v[234:235], s[28:29], 0, v[144:145]
	s_mov_b32 m0, s43
	s_nop 0
	global_load_lds_dwordx4 v[234:235], off
	s_waitcnt vmcnt(8) lgkmcnt(0)
	s_barrier
	s_setprio 1
	s_waitcnt lgkmcnt(0)
	v_mfma_i32_16x16x64_i8 v[134:137], v[70:73], v[196:199], v[134:137]
	v_mfma_i32_16x16x64_i8 v[126:129], v[160:163], v[196:199], v[126:129]
	v_mfma_i32_16x16x64_i8 v[118:121], v[70:73], v[204:207], v[118:121]
	v_mfma_i32_16x16x64_i8 v[110:113], v[160:163], v[204:207], v[110:113]
	v_mfma_i32_16x16x64_i8 v[102:105], v[70:73], v[212:215], v[102:105]
	v_mfma_i32_16x16x64_i8 v[94:97], v[160:163], v[212:215], v[94:97]
	v_mfma_i32_16x16x64_i8 v[86:89], v[70:73], v[220:223], v[86:89]
	v_mfma_i32_16x16x64_i8 v[78:81], v[160:163], v[220:223], v[78:81]
	v_mfma_i32_16x16x64_i8 v[134:137], v[156:159], v[200:203], v[134:137]
	v_mfma_i32_16x16x64_i8 v[126:129], v[172:175], v[200:203], v[126:129]
	v_mfma_i32_16x16x64_i8 v[118:121], v[156:159], v[208:211], v[118:121]
	v_mfma_i32_16x16x64_i8 v[110:113], v[172:175], v[208:211], v[110:113]
	v_mfma_i32_16x16x64_i8 v[102:105], v[156:159], v[216:219], v[102:105]
	v_mfma_i32_16x16x64_i8 v[94:97], v[172:175], v[216:219], v[94:97]
	v_mfma_i32_16x16x64_i8 v[86:89], v[156:159], v[224:227], v[86:89]
	v_mfma_i32_16x16x64_i8 v[78:81], v[172:175], v[224:227], v[78:81]
	s_setprio 0
	s_setprio 1
	v_mfma_i32_16x16x64_i8 v[130:133], v[176:179], v[196:199], v[130:133]
	v_mfma_i32_16x16x64_i8 v[122:125], v[184:187], v[196:199], v[122:125]
	v_mfma_i32_16x16x64_i8 v[114:117], v[176:179], v[204:207], v[114:117]
	v_mfma_i32_16x16x64_i8 v[106:109], v[184:187], v[204:207], v[106:109]
	v_mfma_i32_16x16x64_i8 v[98:101], v[176:179], v[212:215], v[98:101]
	v_mfma_i32_16x16x64_i8 v[90:93], v[184:187], v[212:215], v[90:93]
	v_mfma_i32_16x16x64_i8 v[82:85], v[176:179], v[220:223], v[82:85]
	v_mfma_i32_16x16x64_i8 v[74:77], v[184:187], v[220:223], v[74:77]
	v_mfma_i32_16x16x64_i8 v[130:133], v[180:183], v[200:203], v[130:133]
	v_mfma_i32_16x16x64_i8 v[122:125], v[188:191], v[200:203], v[122:125]
	v_mfma_i32_16x16x64_i8 v[114:117], v[180:183], v[208:211], v[114:117]
	v_mfma_i32_16x16x64_i8 v[106:109], v[188:191], v[208:211], v[106:109]
	v_mfma_i32_16x16x64_i8 v[98:101], v[180:183], v[216:219], v[98:101]
	v_mfma_i32_16x16x64_i8 v[90:93], v[188:191], v[216:219], v[90:93]
	v_mfma_i32_16x16x64_i8 v[82:85], v[180:183], v[224:227], v[82:85]
	v_mfma_i32_16x16x64_i8 v[74:77], v[188:191], v[224:227], v[74:77]
	s_setprio 0
	s_barrier
; #define PG8_STAGE(bufoff, gbase, voff) do { _Pragma("unroll") for (int _i = 0; _i < 2; ++_i) \
;         __builtin_amdgcn_global_load_lds((const unsigned*)((const char*)(gbase) + (voff)[_i]), (LAS unsigned*)(lds + (bufoff) + ldsw + _i * 8192), 16, 0, 0); } while (0)
; #define PG8_LDA(dst, b, h) do { _Pragma("unroll") for (int m = 0; m < 4; ++m) dst[m] = PG8_LD32(lds + PG8_SA(b, h) + aoff + m * 2048); } while (0)
; #define PG8_WAIT_V(n) asm volatile("s_waitcnt vmcnt(" #n ")" ::: "memory")
; #define PG8_WAIT_L(n) asm volatile("s_waitcnt lgkmcnt(" #n ")" ::: "memory")
; #define PG8_BAR __builtin_amdgcn_s_barrier()
; #define PG8_SCHED __builtin_amdgcn_sched_barrier(0)
; #define PG8_STA(bufoff, nextflag, h, koff) do { if constexpr (Sched::GATHER) { unsigned _o[2]; _o[0] = (nextflag) ? nxtA[h][0] : curA[h][0]; _o[1] = (nextflag) ? nxtA[h][1] : curA[h][1]; PG8_STAGE(bufoff, Ab + (koff), _o); } \
;         else { PG8_STAGE(bufoff, ((nextflag) ? nA : cA) + (size_t)(h) * hstep + (koff), voffA); } } while (0)
; template <class Epi, class Sched, bool ALIGN_EPI, int DT>
; __device__ __forceinline__ void gemm_phase(LAS unsigned char* lds, const int KB, const Sched& S, const Epi& E) {
;     ...
;             PG8_LDA(At, 1, 1); PG8_STAGE(PG8_SB(1, 0), b3, voffB); PG8_STAGE(PG8_SB(1, 1), b3 + hstep, voffB); PG8_STA(PG8_SA(1, 0), last, 0, k3);
;             PG8_WAIT_V(8); PG8_WAIT_L(0); PG8_BAR; PG8_MMA(1, 0, At, B0); PG8_MMA(1, 1, At, B1); PG8_BAR; PG8_SCHED;
;         }
;         if constexpr (ALIGN_EPI) { if (wr == 0) PG8_BAR; }
	s_add_i32 s28, s36, s38
	v_lshl_add_u64 v[192:193], v[192:193], 0, s[12:13]
	s_mov_b32 m0, s28
	ds_read_b128 v[196:199], v169 offset:49152
	ds_read_b128 v[200:203], v169 offset:50176
	ds_read_b128 v[204:207], v169 offset:51200
	ds_read_b128 v[208:211], v169 offset:52224
	ds_read_b128 v[212:215], v169 offset:53248
	ds_read_b128 v[216:219], v169 offset:54272
	ds_read_b128 v[220:223], v169 offset:55296
	ds_read_b128 v[224:227], v169 offset:56320
	global_load_lds_dwordx4 v[192:193], off
	s_add_i32 m0, s28, 0x2000
	s_add_u32 s28, s34, 0x40080
	v_lshl_add_u64 v[192:193], v[228:229], 0, s[12:13]
	s_addc_u32 s29, s35, 0
	s_add_i32 s34, s37, s38
	global_load_lds_dwordx4 v[192:193], off
	v_lshl_add_u64 v[192:193], s[28:29], 0, v[140:141]
	s_mov_b32 m0, s34
	s_nop 0
	global_load_lds_dwordx4 v[192:193], off
	v_lshl_add_u64 v[192:193], s[28:29], 0, v[138:139]
	s_add_i32 m0, s34, 0x2000
	s_nop 0
	global_load_lds_dwordx4 v[192:193], off
	v_lshl_add_u64 v[192:193], v[230:231], 0, s[12:13]
	s_mov_b32 m0, s45
	s_nop 0
	global_load_lds_dwordx4 v[192:193], off
	v_lshl_add_u64 v[192:193], v[232:233], 0, s[12:13]
	s_mov_b32 m0, s46
	s_nop 0
	global_load_lds_dwordx4 v[192:193], off
	s_waitcnt vmcnt(8) lgkmcnt(0)
	s_barrier
	s_setprio 1
	s_waitcnt lgkmcnt(0)
	v_mfma_i32_16x16x64_i8 v[62:65], v[70:73], v[196:199], v[62:65]
	v_mfma_i32_16x16x64_i8 v[54:57], v[160:163], v[196:199], v[54:57]
	v_mfma_i32_16x16x64_i8 v[46:49], v[70:73], v[204:207], v[46:49]
	v_mfma_i32_16x16x64_i8 v[38:41], v[160:163], v[204:207], v[38:41]
	v_mfma_i32_16x16x64_i8 v[30:33], v[70:73], v[212:215], v[30:33]
	v_mfma_i32_16x16x64_i8 v[22:25], v[160:163], v[212:215], v[22:25]
	v_mfma_i32_16x16x64_i8 v[6:9], v[70:73], v[220:223], v[6:9]
	v_mfma_i32_16x16x64_i8 v[2:5], v[160:163], v[220:223], v[2:5]
	v_mfma_i32_16x16x64_i8 v[62:65], v[156:159], v[200:203], v[62:65]
	v_mfma_i32_16x16x64_i8 v[54:57], v[172:175], v[200:203], v[54:57]
	v_mfma_i32_16x16x64_i8 v[46:49], v[156:159], v[208:211], v[46:49]
	v_mfma_i32_16x16x64_i8 v[38:41], v[172:175], v[208:211], v[38:41]
	v_mfma_i32_16x16x64_i8 v[30:33], v[156:159], v[216:219], v[30:33]
	v_mfma_i32_16x16x64_i8 v[22:25], v[172:175], v[216:219], v[22:25]
	v_mfma_i32_16x16x64_i8 v[6:9], v[156:159], v[224:227], v[6:9]
	v_mfma_i32_16x16x64_i8 v[2:5], v[172:175], v[224:227], v[2:5]
	s_setprio 0
	s_setprio 1
	v_mfma_i32_16x16x64_i8 v[58:61], v[176:179], v[196:199], v[58:61]
	v_mfma_i32_16x16x64_i8 v[50:53], v[184:187], v[196:199], v[50:53]
	v_mfma_i32_16x16x64_i8 v[42:45], v[176:179], v[204:207], v[42:45]
	v_mfma_i32_16x16x64_i8 v[34:37], v[184:187], v[204:207], v[34:37]
	v_mfma_i32_16x16x64_i8 v[26:29], v[176:179], v[212:215], v[26:29]
	v_mfma_i32_16x16x64_i8 v[18:21], v[184:187], v[212:215], v[18:21]
	v_mfma_i32_16x16x64_i8 v[14:17], v[176:179], v[220:223], v[14:17]
	v_mfma_i32_16x16x64_i8 v[10:13], v[184:187], v[220:223], v[10:13]
	v_mfma_i32_16x16x64_i8 v[58:61], v[180:183], v[200:203], v[58:61]
	v_mfma_i32_16x16x64_i8 v[50:53], v[188:191], v[200:203], v[50:53]
	v_mfma_i32_16x16x64_i8 v[42:45], v[180:183], v[208:211], v[42:45]
	v_mfma_i32_16x16x64_i8 v[34:37], v[188:191], v[208:211], v[34:37]
	v_mfma_i32_16x16x64_i8 v[26:29], v[180:183], v[216:219], v[26:29]
	v_mfma_i32_16x16x64_i8 v[18:21], v[188:191], v[216:219], v[18:21]
	v_mfma_i32_16x16x64_i8 v[14:17], v[180:183], v[224:227], v[14:17]
	v_mfma_i32_16x16x64_i8 v[10:13], v[188:191], v[224:227], v[10:13]
	s_setprio 0
	s_barrier
	s_add_i32 s62, s62, 2
	s_cmp_gt_u32 s62, 13
	s_mov_b64 s[28:29], s[30:31]
	s_cbranch_scc0 .LBB0_1154
	s_and_b64 vcc, exec, s[14:15]
	s_cbranch_vccz .LBB0_1157
	s_barrier

; #define PG8_STAGE(bufoff, gbase, voff) do { _Pragma("unroll") for (int _i = 0; _i < 2; ++_i) \
;         __builtin_amdgcn_global_load_lds((const unsigned*)((const char*)(gbase) + (voff)[_i]), (LAS unsigned*)(lds + (bufoff) + ldsw + _i * 8192), 16, 0, 0); } while (0)
; #define PG8_LDA(dst, b, h) do { _Pragma("unroll") for (int m = 0; m < 4; ++m) dst[m] = PG8_LD32(lds + PG8_SA(b, h) + aoff + m * 2048); } while (0)
; #define PG8_LDB(dst, b, h) do { _Pragma("unroll") for (int n = 0; n < 2; ++n) dst[n] = PG8_LD32(lds + PG8_SB(b, h) + boff + n * 2048); } while (0)
; #define PG8_WAIT_V(n) asm volatile("s_waitcnt vmcnt(" #n ")" ::: "memory")
; #define PG8_WAIT_L(n) asm volatile("s_waitcnt lgkmcnt(" #n ")" ::: "memory")
; #define PG8_BAR __builtin_amdgcn_s_barrier()
; #define PG8_SCHED __builtin_amdgcn_sched_barrier(0)
; #define PG8_STA(bufoff, nextflag, h, koff) do { if constexpr (Sched::GATHER) { unsigned _o[2]; _o[0] = (nextflag) ? nxtA[h][0] : curA[h][0]; _o[1] = (nextflag) ? nxtA[h][1] : curA[h][1]; PG8_STAGE(bufoff, Ab + (koff), _o); } \
;         else { PG8_STAGE(bufoff, ((nextflag) ? nA : cA) + (size_t)(h) * hstep + (koff), voffA); } } while (0)
; template <class Epi, class Sched, bool ALIGN_EPI, int DT>
; __device__ __forceinline__ void gemm_phase(LAS unsigned char* lds, const int KB, const Sched& S, const Epi& E) {
;     ...
;             PG8_LDB(B0, 0, 0); PG8_LDB(B1, 0, 1); PG8_SCHED; PG8_LDA(At, 0, 0); PG8_STA(PG8_SA(1, 1), false, 1, k1);
;             PG8_WAIT_V(8); PG8_WAIT_L(0); PG8_BAR; PG8_MMA(0, 0, At, B0); PG8_MMA(0, 1, At, B1); PG8_BAR; PG8_SCHED;
;             PG8_LDA(At, 0, 1); PG8_STAGE(PG8_SB(0, 0), b2, voffB); PG8_STAGE(PG8_SB(0, 1), b2 + hstep, voffB); PG8_STA(PG8_SA(0, 0), last, 0, k2);
;             PG8_WAIT_V(8); PG8_WAIT_L(0); PG8_BAR; PG8_MMA(1, 0, At, B0); PG8_MMA(1, 1, At, B1); PG8_BAR; PG8_SCHED;
.LBB0_1237:
	ds_read_b128 v[18:21], v193
	ds_read_b128 v[22:25], v193 offset:1024
	ds_read_b128 v[26:29], v193 offset:2048
	ds_read_b128 v[30:33], v193 offset:3072
	ds_read_b128 v[2:5], v195
	ds_read_b128 v[6:9], v195 offset:1024
	ds_read_b128 v[10:13], v195 offset:2048
	ds_read_b128 v[14:17], v195 offset:3072
	s_add_u32 s26, s30, 0x100
	s_addc_u32 s27, s31, 0
	s_add_u32 s28, s56, s30
	s_addc_u32 s29, s57, s31
	s_add_i32 s68, s43, s34
	s_add_i32 m0, s35, 0xc000
	s_add_i32 s69, s35, 0xe000
	s_add_i32 s63, s68, 0x2000
	s_cmp_eq_u32 s62, 40
	s_cselect_b32 s29, s23, s29
	s_cselect_b32 s28, s22, s28
	s_cselect_b32 s66, 0, s27
	s_cselect_b32 s67, 0, s26
	v_lshl_add_u64 v[222:223], v[178:179], 0, s[30:31]
	ds_read_b128 v[182:185], v196
	ds_read_b128 v[186:189], v196 offset:1024
	ds_read_b128 v[198:201], v196 offset:2048
	ds_read_b128 v[202:205], v196 offset:3072
	ds_read_b128 v[206:209], v196 offset:4096
	ds_read_b128 v[210:213], v196 offset:5120
	ds_read_b128 v[214:217], v196 offset:6144
	ds_read_b128 v[218:221], v196 offset:7168
	global_load_lds_dwordx4 v[222:223], off
	v_lshl_add_u64 v[222:223], v[180:181], 0, s[30:31]
	s_mov_b32 m0, s69
	s_nop 0
	global_load_lds_dwordx4 v[222:223], off
	s_waitcnt vmcnt(8) lgkmcnt(0)
	s_barrier
	s_setprio 1
	s_waitcnt lgkmcnt(0)
	v_mfma_scale_f32_16x16x128_f8f6f4 v[158:161], v[18:25], v[182:189], v[158:161], v190, v190 op_sel_hi:[0,0,0]
	v_mfma_scale_f32_16x16x128_f8f6f4 v[154:157], v[26:33], v[182:189], v[154:157], v190, v190 op_sel_hi:[0,0,0]
	v_mfma_scale_f32_16x16x128_f8f6f4 v[150:153], v[18:25], v[198:205], v[150:153], v190, v190 op_sel_hi:[0,0,0]
	v_mfma_scale_f32_16x16x128_f8f6f4 v[142:145], v[26:33], v[198:205], v[142:145], v190, v190 op_sel_hi:[0,0,0]
	v_mfma_scale_f32_16x16x128_f8f6f4 v[134:137], v[18:25], v[206:213], v[134:137], v190, v190 op_sel_hi:[0,0,0]
	v_mfma_scale_f32_16x16x128_f8f6f4 v[126:129], v[26:33], v[206:213], v[126:129], v190, v190 op_sel_hi:[0,0,0]
	v_mfma_scale_f32_16x16x128_f8f6f4 v[118:121], v[18:25], v[214:221], v[118:121], v190, v190 op_sel_hi:[0,0,0]
	v_mfma_scale_f32_16x16x128_f8f6f4 v[110:113], v[26:33], v[214:221], v[110:113], v190, v190 op_sel_hi:[0,0,0]
	s_setprio 0
	s_setprio 1
	v_mfma_scale_f32_16x16x128_f8f6f4 v[146:149], v[2:9], v[182:189], v[146:149], v190, v190 op_sel_hi:[0,0,0]
	v_mfma_scale_f32_16x16x128_f8f6f4 v[138:141], v[10:17], v[182:189], v[138:141], v190, v190 op_sel_hi:[0,0,0]
	v_mfma_scale_f32_16x16x128_f8f6f4 v[130:133], v[2:9], v[198:205], v[130:133], v190, v190 op_sel_hi:[0,0,0]
	v_mfma_scale_f32_16x16x128_f8f6f4 v[122:125], v[10:17], v[198:205], v[122:125], v190, v190 op_sel_hi:[0,0,0]
	v_mfma_scale_f32_16x16x128_f8f6f4 v[114:117], v[2:9], v[206:213], v[114:117], v190, v190 op_sel_hi:[0,0,0]
	v_mfma_scale_f32_16x16x128_f8f6f4 v[106:109], v[10:17], v[206:213], v[106:109], v190, v190 op_sel_hi:[0,0,0]
	v_mfma_scale_f32_16x16x128_f8f6f4 v[102:105], v[2:9], v[214:221], v[102:105], v190, v190 op_sel_hi:[0,0,0]
	v_mfma_scale_f32_16x16x128_f8f6f4 v[98:101], v[10:17], v[214:221], v[98:101], v190, v190 op_sel_hi:[0,0,0]
	s_setprio 0
	s_barrier
	s_mov_b32 m0, s68
	v_lshl_add_u64 v[184:185], s[28:29], 0, v[162:163]
	ds_read_b128 v[198:201], v196 offset:16384
	ds_read_b128 v[202:205], v196 offset:17408
	ds_read_b128 v[206:209], v196 offset:18432
	ds_read_b128 v[210:213], v196 offset:19456
	ds_read_b128 v[214:217], v196 offset:20480
	ds_read_b128 v[218:221], v196 offset:21504
	ds_read_b128 v[222:225], v196 offset:22528
	ds_read_b128 v[226:229], v196 offset:23552
	global_load_lds_dwordx4 v[184:185], off
	s_mov_b32 m0, s63
	s_cselect_b32 s63, s9, s25
	s_cselect_b32 s68, s8, s24
	s_add_u32 s30, s28, 0xb0000
	v_lshl_add_u64 v[182:183], s[28:29], 0, v[164:165]
	s_addc_u32 s31, s29, 0
	s_add_i32 s69, s44, s34
	global_load_lds_dwordx4 v[182:183], off
	v_lshl_add_u64 v[186:187], s[30:31], 0, v[162:163]
	s_mov_b32 m0, s69
	s_nop 0
	global_load_lds_dwordx4 v[186:187], off
	s_add_i32 m0, s69, 0x2000
	v_lshl_add_u64 v[186:187], s[30:31], 0, v[164:165]
	s_add_u32 s30, s68, s67
	s_addc_u32 s31, s63, s66
	global_load_lds_dwordx4 v[186:187], off
	v_lshl_add_u64 v[186:187], s[30:31], 0, v[166:167]
	s_mov_b32 m0, s35
	v_lshl_add_u64 v[188:189], s[30:31], 0, v[168:169]
	global_load_lds_dwordx4 v[186:187], off
	s_mov_b32 m0, s36
	s_nop 0
	global_load_lds_dwordx4 v[188:189], off
	s_waitcnt vmcnt(8) lgkmcnt(0)
	s_barrier
	s_setprio 1
	s_waitcnt lgkmcnt(0)
	v_mfma_scale_f32_16x16x128_f8f6f4 v[94:97], v[18:25], v[198:205], v[94:97], v190, v190 op_sel_hi:[0,0,0]
	v_mfma_scale_f32_16x16x128_f8f6f4 v[90:93], v[26:33], v[198:205], v[90:93], v190, v190 op_sel_hi:[0,0,0]
	v_mfma_scale_f32_16x16x128_f8f6f4 v[86:89], v[18:25], v[206:213], v[86:89], v190, v190 op_sel_hi:[0,0,0]
	v_mfma_scale_f32_16x16x128_f8f6f4 v[78:81], v[26:33], v[206:213], v[78:81], v190, v190 op_sel_hi:[0,0,0]
	v_mfma_scale_f32_16x16x128_f8f6f4 v[62:65], v[18:25], v[214:221], v[62:65], v190, v190 op_sel_hi:[0,0,0]
	v_mfma_scale_f32_16x16x128_f8f6f4 v[54:57], v[26:33], v[214:221], v[54:57], v190, v190 op_sel_hi:[0,0,0]
	v_mfma_scale_f32_16x16x128_f8f6f4 v[46:49], v[18:25], v[222:229], v[46:49], v190, v190 op_sel_hi:[0,0,0]
	v_mfma_scale_f32_16x16x128_f8f6f4 v[38:41], v[26:33], v[222:229], v[38:41], v190, v190 op_sel_hi:[0,0,0]
	s_setprio 0
	s_setprio 1
	v_mfma_scale_f32_16x16x128_f8f6f4 v[82:85], v[2:9], v[198:205], v[82:85], v190, v190 op_sel_hi:[0,0,0]
	v_mfma_scale_f32_16x16x128_f8f6f4 v[74:77], v[10:17], v[198:205], v[74:77], v190, v190 op_sel_hi:[0,0,0]
	v_mfma_scale_f32_16x16x128_f8f6f4 v[58:61], v[2:9], v[206:213], v[58:61], v190, v190 op_sel_hi:[0,0,0]
	v_mfma_scale_f32_16x16x128_f8f6f4 v[50:53], v[10:17], v[206:213], v[50:53], v190, v190 op_sel_hi:[0,0,0]
	v_mfma_scale_f32_16x16x128_f8f6f4 v[42:45], v[2:9], v[214:221], v[42:45], v190, v190 op_sel_hi:[0,0,0]
	v_mfma_scale_f32_16x16x128_f8f6f4 v[34:37], v[10:17], v[214:221], v[34:37], v190, v190 op_sel_hi:[0,0,0]
	v_mfma_scale_f32_16x16x128_f8f6f4 v[70:73], v[2:9], v[222:229], v[70:73], v190, v190 op_sel_hi:[0,0,0]
	v_mfma_scale_f32_16x16x128_f8f6f4 v[66:69], v[10:17], v[222:229], v[66:69], v190, v190 op_sel_hi:[0,0,0]
	s_setprio 0
	s_barrier
; #define PG8_STAGE(bufoff, gbase, voff) do { _Pragma("unroll") for (int _i = 0; _i < 2; ++_i) \
;         __builtin_amdgcn_global_load_lds((const unsigned*)((const char*)(gbase) + (voff)[_i]), (LAS unsigned*)(lds + (bufoff) + ldsw + _i * 8192), 16, 0, 0); } while (0)
; #define PG8_LDA(dst, b, h) do { _Pragma("unroll") for (int m = 0; m < 4; ++m) dst[m] = PG8_LD32(lds + PG8_SA(b, h) + aoff + m * 2048); } while (0)
; #define PG8_LDB(dst, b, h) do { _Pragma("unroll") for (int n = 0; n < 2; ++n) dst[n] = PG8_LD32(lds + PG8_SB(b, h) + boff + n * 2048); } while (0)
; #define PG8_WAIT_V(n) asm volatile("s_waitcnt vmcnt(" #n ")" ::: "memory")
; #define PG8_WAIT_L(n) asm volatile("s_waitcnt lgkmcnt(" #n ")" ::: "memory")
; #define PG8_BAR __builtin_amdgcn_s_barrier()
; #define PG8_SCHED __builtin_amdgcn_sched_barrier(0)
; #define PG8_STA(bufoff, nextflag, h, koff) do { if constexpr (Sched::GATHER) { unsigned _o[2]; _o[0] = (nextflag) ? nxtA[h][0] : curA[h][0]; _o[1] = (nextflag) ? nxtA[h][1] : curA[h][1]; PG8_STAGE(bufoff, Ab + (koff), _o); } \
;         else { PG8_STAGE(bufoff, ((nextflag) ? nA : cA) + (size_t)(h) * hstep + (koff), voffA); } } while (0)
; template <class Epi, class Sched, bool ALIGN_EPI, int DT>
; __device__ __forceinline__ void gemm_phase(LAS unsigned char* lds, const int KB, const Sched& S, const Epi& E) {
;     ...
;             PG8_LDB(B0, 1, 0); PG8_LDB(B1, 1, 1); PG8_SCHED; PG8_LDA(At, 1, 0); PG8_STA(PG8_SA(0, 1), last, 1, k2);
;             PG8_WAIT_V(8); PG8_WAIT_L(0); PG8_BAR; PG8_MMA(0, 0, At, B0); PG8_MMA(0, 1, At, B1); PG8_BAR; PG8_SCHED;
;             PG8_LDA(At, 1, 1); PG8_STAGE(PG8_SB(1, 0), b3, voffB); PG8_STAGE(PG8_SB(1, 1), b3 + hstep, voffB); PG8_STA(PG8_SA(1, 0), last, 0, k3);
;             PG8_WAIT_V(8); PG8_WAIT_L(0); PG8_BAR; PG8_MMA(1, 0, At, B0); PG8_MMA(1, 1, At, B1); PG8_BAR; PG8_SCHED;
;         }
;         if constexpr (ALIGN_EPI) { if (wr == 0) PG8_BAR; }
	s_add_i32 s63, 0, 0x18000
	s_add_i32 s66, 0, 0x1c000
	v_add_u32_e32 v14, s63, v191
	v_add_u32_e32 v30, s66, v191
	ds_read_b128 v[2:5], v14
	ds_read_b128 v[6:9], v14 offset:1024
	ds_read_b128 v[10:13], v14 offset:2048
	ds_read_b128 v[14:17], v14 offset:3072
	ds_read_b128 v[18:21], v30
	ds_read_b128 v[22:25], v30 offset:1024
	ds_read_b128 v[26:29], v30 offset:2048
	ds_read_b128 v[30:33], v30 offset:3072
	s_add_u32 s30, s30, 0xb0000
	s_addc_u32 s31, s31, 0
	s_mov_b32 m0, s37
	v_lshl_add_u64 v[230:231], s[30:31], 0, v[166:167]
	ds_read_b128 v[198:201], v196 offset:32768
	ds_read_b128 v[202:205], v196 offset:33792
	ds_read_b128 v[206:209], v196 offset:34816
	ds_read_b128 v[210:213], v196 offset:35840
	ds_read_b128 v[214:217], v196 offset:36864
	ds_read_b128 v[218:221], v196 offset:37888
	ds_read_b128 v[222:225], v196 offset:38912
	ds_read_b128 v[226:229], v196 offset:39936
	global_load_lds_dwordx4 v[230:231], off
	v_lshl_add_u64 v[230:231], s[30:31], 0, v[168:169]
	s_mov_b32 m0, s38
	s_nop 0
	global_load_lds_dwordx4 v[230:231], off
	s_waitcnt vmcnt(8) lgkmcnt(0)
	s_barrier
	s_setprio 1
	s_waitcnt lgkmcnt(0)
	v_mfma_scale_f32_16x16x128_f8f6f4 v[158:161], v[2:9], v[198:205], v[158:161], v190, v190 op_sel_hi:[0,0,0]
	v_mfma_scale_f32_16x16x128_f8f6f4 v[154:157], v[10:17], v[198:205], v[154:157], v190, v190 op_sel_hi:[0,0,0]
	v_mfma_scale_f32_16x16x128_f8f6f4 v[150:153], v[2:9], v[206:213], v[150:153], v190, v190 op_sel_hi:[0,0,0]
	v_mfma_scale_f32_16x16x128_f8f6f4 v[142:145], v[10:17], v[206:213], v[142:145], v190, v190 op_sel_hi:[0,0,0]
	v_mfma_scale_f32_16x16x128_f8f6f4 v[134:137], v[2:9], v[214:221], v[134:137], v190, v190 op_sel_hi:[0,0,0]
	v_mfma_scale_f32_16x16x128_f8f6f4 v[126:129], v[10:17], v[214:221], v[126:129], v190, v190 op_sel_hi:[0,0,0]
	v_mfma_scale_f32_16x16x128_f8f6f4 v[118:121], v[2:9], v[222:229], v[118:121], v190, v190 op_sel_hi:[0,0,0]
	v_mfma_scale_f32_16x16x128_f8f6f4 v[110:113], v[10:17], v[222:229], v[110:113], v190, v190 op_sel_hi:[0,0,0]
	s_setprio 0
	s_setprio 1
	v_mfma_scale_f32_16x16x128_f8f6f4 v[146:149], v[18:25], v[198:205], v[146:149], v190, v190 op_sel_hi:[0,0,0]
	v_mfma_scale_f32_16x16x128_f8f6f4 v[138:141], v[26:33], v[198:205], v[138:141], v190, v190 op_sel_hi:[0,0,0]
	v_mfma_scale_f32_16x16x128_f8f6f4 v[130:133], v[18:25], v[206:213], v[130:133], v190, v190 op_sel_hi:[0,0,0]
	v_mfma_scale_f32_16x16x128_f8f6f4 v[122:125], v[26:33], v[206:213], v[122:125], v190, v190 op_sel_hi:[0,0,0]
	v_mfma_scale_f32_16x16x128_f8f6f4 v[114:117], v[18:25], v[214:221], v[114:117], v190, v190 op_sel_hi:[0,0,0]
	v_mfma_scale_f32_16x16x128_f8f6f4 v[106:109], v[26:33], v[214:221], v[106:109], v190, v190 op_sel_hi:[0,0,0]
	v_mfma_scale_f32_16x16x128_f8f6f4 v[102:105], v[18:25], v[222:229], v[102:105], v190, v190 op_sel_hi:[0,0,0]
	v_mfma_scale_f32_16x16x128_f8f6f4 v[98:101], v[26:33], v[222:229], v[98:101], v190, v190 op_sel_hi:[0,0,0]
	s_setprio 0
	s_barrier
	s_add_i32 s30, s63, s34
	v_lshl_add_u64 v[184:185], v[184:185], 0, s[12:13]
	s_mov_b32 m0, s30
	ds_read_b128 v[198:201], v196 offset:49152
	ds_read_b128 v[202:205], v196 offset:50176
	ds_read_b128 v[206:209], v196 offset:51200
	ds_read_b128 v[210:213], v196 offset:52224
	ds_read_b128 v[214:217], v196 offset:53248
	ds_read_b128 v[218:221], v196 offset:54272
	ds_read_b128 v[222:225], v196 offset:55296
	ds_read_b128 v[226:229], v196 offset:56320
	global_load_lds_dwordx4 v[184:185], off
	s_add_i32 m0, s30, 0x2000
	s_add_u32 s28, s28, 0xb0080
	v_lshl_add_u64 v[182:183], v[182:183], 0, s[12:13]
	s_addc_u32 s29, s29, 0
	s_add_i32 s30, s66, s34
	global_load_lds_dwordx4 v[182:183], off
	v_lshl_add_u64 v[182:183], s[28:29], 0, v[162:163]
	s_mov_b32 m0, s30
	s_nop 0
	global_load_lds_dwordx4 v[182:183], off
	v_lshl_add_u64 v[182:183], s[28:29], 0, v[164:165]
	s_add_i32 m0, s30, 0x2000
	s_nop 0
	global_load_lds_dwordx4 v[182:183], off
	v_lshl_add_u64 v[182:183], v[186:187], 0, s[12:13]
	s_mov_b32 m0, s40
	s_nop 0
	global_load_lds_dwordx4 v[182:183], off
	v_lshl_add_u64 v[182:183], v[188:189], 0, s[12:13]
	s_mov_b32 m0, s41
	s_nop 0
	global_load_lds_dwordx4 v[182:183], off
	s_waitcnt vmcnt(8) lgkmcnt(0)
	s_barrier
	s_setprio 1
	s_waitcnt lgkmcnt(0)
	v_mfma_scale_f32_16x16x128_f8f6f4 v[94:97], v[2:9], v[198:205], v[94:97], v190, v190 op_sel_hi:[0,0,0]
	v_mfma_scale_f32_16x16x128_f8f6f4 v[90:93], v[10:17], v[198:205], v[90:93], v190, v190 op_sel_hi:[0,0,0]
	v_mfma_scale_f32_16x16x128_f8f6f4 v[86:89], v[2:9], v[206:213], v[86:89], v190, v190 op_sel_hi:[0,0,0]
	v_mfma_scale_f32_16x16x128_f8f6f4 v[78:81], v[10:17], v[206:213], v[78:81], v190, v190 op_sel_hi:[0,0,0]
	v_mfma_scale_f32_16x16x128_f8f6f4 v[62:65], v[2:9], v[214:221], v[62:65], v190, v190 op_sel_hi:[0,0,0]
	v_mfma_scale_f32_16x16x128_f8f6f4 v[54:57], v[10:17], v[214:221], v[54:57], v190, v190 op_sel_hi:[0,0,0]
	v_mfma_scale_f32_16x16x128_f8f6f4 v[46:49], v[2:9], v[222:229], v[46:49], v190, v190 op_sel_hi:[0,0,0]
	v_mfma_scale_f32_16x16x128_f8f6f4 v[38:41], v[10:17], v[222:229], v[38:41], v190, v190 op_sel_hi:[0,0,0]
	s_setprio 0
	s_setprio 1
	v_mfma_scale_f32_16x16x128_f8f6f4 v[82:85], v[18:25], v[198:205], v[82:85], v190, v190 op_sel_hi:[0,0,0]
	v_mfma_scale_f32_16x16x128_f8f6f4 v[74:77], v[26:33], v[198:205], v[74:77], v190, v190 op_sel_hi:[0,0,0]
	v_mfma_scale_f32_16x16x128_f8f6f4 v[58:61], v[18:25], v[206:213], v[58:61], v190, v190 op_sel_hi:[0,0,0]
	v_mfma_scale_f32_16x16x128_f8f6f4 v[50:53], v[26:33], v[206:213], v[50:53], v190, v190 op_sel_hi:[0,0,0]
	v_mfma_scale_f32_16x16x128_f8f6f4 v[42:45], v[18:25], v[214:221], v[42:45], v190, v190 op_sel_hi:[0,0,0]
	v_mfma_scale_f32_16x16x128_f8f6f4 v[34:37], v[26:33], v[214:221], v[34:37], v190, v190 op_sel_hi:[0,0,0]
	v_mfma_scale_f32_16x16x128_f8f6f4 v[70:73], v[18:25], v[222:229], v[70:73], v190, v190 op_sel_hi:[0,0,0]
	v_mfma_scale_f32_16x16x128_f8f6f4 v[66:69], v[26:33], v[222:229], v[66:69], v190, v190 op_sel_hi:[0,0,0]
	s_setprio 0
	s_barrier
	s_add_i32 s62, s62, 2
	s_cmp_gt_u32 s62, 41
	s_mov_b64 s[30:31], s[26:27]
	s_cbranch_scc0 .LBB0_1237
	s_and_b64 vcc, exec, s[14:15]
	s_cbranch_vccz .LBB0_1240
	s_barrier

; #define PG8_STAGE(bufoff, gbase, voff) do { _Pragma("unroll") for (int _i = 0; _i < 2; ++_i) \
;         __builtin_amdgcn_global_load_lds((const unsigned*)((const char*)(gbase) + (voff)[_i]), (LAS unsigned*)(lds + (bufoff) + ldsw + _i * 8192), 16, 0, 0); } while (0)
; #define PG8_LDA(dst, b, h) do { _Pragma("unroll") for (int m = 0; m < 4; ++m) dst[m] = PG8_LD32(lds + PG8_SA(b, h) + aoff + m * 2048); } while (0)
; #define PG8_LDB(dst, b, h) do { _Pragma("unroll") for (int n = 0; n < 2; ++n) dst[n] = PG8_LD32(lds + PG8_SB(b, h) + boff + n * 2048); } while (0)
; #define PG8_WAIT_V(n) asm volatile("s_waitcnt vmcnt(" #n ")" ::: "memory")
; #define PG8_WAIT_L(n) asm volatile("s_waitcnt lgkmcnt(" #n ")" ::: "memory")
; #define PG8_BAR __builtin_amdgcn_s_barrier()
; #define PG8_SCHED __builtin_amdgcn_sched_barrier(0)
; #define PG8_STA(bufoff, nextflag, h, koff) do { if constexpr (Sched::GATHER) { unsigned _o[2]; _o[0] = (nextflag) ? nxtA[h][0] : curA[h][0]; _o[1] = (nextflag) ? nxtA[h][1] : curA[h][1]; PG8_STAGE(bufoff, Ab + (koff), _o); } \
;         else { PG8_STAGE(bufoff, ((nextflag) ? nA : cA) + (size_t)(h) * hstep + (koff), voffA); } } while (0)
; template <class Epi, class Sched, bool ALIGN_EPI, int DT>
; __device__ __forceinline__ void gemm_phase(LAS unsigned char* lds, const int KB, const Sched& S, const Epi& E) {
;     ...
;             PG8_LDB(B0, 0, 0); PG8_LDB(B1, 0, 1); PG8_SCHED; PG8_LDA(At, 0, 0); PG8_STA(PG8_SA(1, 1), false, 1, k1);
;             PG8_WAIT_V(8); PG8_WAIT_L(0); PG8_BAR; PG8_MMA(0, 0, At, B0); PG8_MMA(0, 1, At, B1); PG8_BAR; PG8_SCHED;
;             PG8_LDA(At, 0, 1); PG8_STAGE(PG8_SB(0, 0), b2, voffB); PG8_STAGE(PG8_SB(0, 1), b2 + hstep, voffB); PG8_STA(PG8_SA(0, 0), last, 0, k2);
;             PG8_WAIT_V(8); PG8_WAIT_L(0); PG8_BAR; PG8_MMA(1, 0, At, B0); PG8_MMA(1, 1, At, B1); PG8_BAR; PG8_SCHED;
.LBB0_1385:
	ds_read_b128 v[152:155], v174
	ds_read_b128 v[156:159], v174 offset:1024
	ds_read_b128 v[160:163], v174 offset:2048
	ds_read_b128 v[164:167], v174 offset:3072
	ds_read_b128 v[168:171], v175
	ds_read_b128 v[180:183], v175 offset:1024
	ds_read_b128 v[184:187], v175 offset:2048
	ds_read_b128 v[188:191], v175 offset:3072
	s_add_u32 s38, s36, 0x100
	s_addc_u32 s39, s37, 0
	s_add_u32 s74, s25, s36
	s_addc_u32 s75, s70, s37
	s_cmp_eq_u32 s71, 12
	s_cselect_b64 s[42:43], -1, 0
	s_and_b64 s[40:41], s[42:43], exec
	s_cselect_b32 s76, 0, s38
	s_cselect_b32 s41, s0, s75
	s_cselect_b32 s40, s23, s74
	v_lshl_add_u64 v[192:193], v[148:149], 0, s[36:37]
	s_add_i32 m0, s47, 0xc000
	ds_read_b128 v[196:199], v176
	ds_read_b128 v[200:203], v176 offset:1024
	ds_read_b128 v[204:207], v176 offset:2048
	ds_read_b128 v[208:211], v176 offset:3072
	ds_read_b128 v[212:215], v176 offset:4096
	ds_read_b128 v[216:219], v176 offset:5120
	ds_read_b128 v[220:223], v176 offset:6144
	ds_read_b128 v[224:227], v176 offset:7168
	global_load_lds_dwordx4 v[192:193], off
	v_lshl_add_u64 v[192:193], v[150:151], 0, s[36:37]
	s_add_i32 m0, s47, 0xe000
	s_nop 0
	global_load_lds_dwordx4 v[192:193], off
	s_waitcnt vmcnt(8) lgkmcnt(0)
	s_barrier
	s_setprio 1
	s_waitcnt lgkmcnt(0)
	v_mfma_i32_16x16x64_i8 v[126:129], v[152:155], v[196:199], v[126:129]
	v_mfma_i32_16x16x64_i8 v[122:125], v[160:163], v[196:199], v[122:125]
	v_mfma_i32_16x16x64_i8 v[110:113], v[152:155], v[204:207], v[110:113]
	v_mfma_i32_16x16x64_i8 v[106:109], v[160:163], v[204:207], v[106:109]
	v_mfma_i32_16x16x64_i8 v[94:97], v[152:155], v[212:215], v[94:97]
	v_mfma_i32_16x16x64_i8 v[90:93], v[160:163], v[212:215], v[90:93]
	v_mfma_i32_16x16x64_i8 v[78:81], v[152:155], v[220:223], v[78:81]
	v_mfma_i32_16x16x64_i8 v[74:77], v[160:163], v[220:223], v[74:77]
	v_mfma_i32_16x16x64_i8 v[126:129], v[156:159], v[200:203], v[126:129]
	v_mfma_i32_16x16x64_i8 v[122:125], v[164:167], v[200:203], v[122:125]
	v_mfma_i32_16x16x64_i8 v[110:113], v[156:159], v[208:211], v[110:113]
	v_mfma_i32_16x16x64_i8 v[106:109], v[164:167], v[208:211], v[106:109]
	v_mfma_i32_16x16x64_i8 v[94:97], v[156:159], v[216:219], v[94:97]
	v_mfma_i32_16x16x64_i8 v[90:93], v[164:167], v[216:219], v[90:93]
	v_mfma_i32_16x16x64_i8 v[78:81], v[156:159], v[224:227], v[78:81]
	v_mfma_i32_16x16x64_i8 v[74:77], v[164:167], v[224:227], v[74:77]
	s_setprio 0
	s_setprio 1
	v_mfma_i32_16x16x64_i8 v[118:121], v[168:171], v[196:199], v[118:121]
	v_mfma_i32_16x16x64_i8 v[114:117], v[184:187], v[196:199], v[114:117]
	v_mfma_i32_16x16x64_i8 v[102:105], v[168:171], v[204:207], v[102:105]
	v_mfma_i32_16x16x64_i8 v[98:101], v[184:187], v[204:207], v[98:101]
	v_mfma_i32_16x16x64_i8 v[86:89], v[168:171], v[212:215], v[86:89]
	v_mfma_i32_16x16x64_i8 v[82:85], v[184:187], v[212:215], v[82:85]
	v_mfma_i32_16x16x64_i8 v[70:73], v[168:171], v[220:223], v[70:73]
	v_mfma_i32_16x16x64_i8 v[66:69], v[184:187], v[220:223], v[66:69]
	v_mfma_i32_16x16x64_i8 v[118:121], v[180:183], v[200:203], v[118:121]
	v_mfma_i32_16x16x64_i8 v[114:117], v[188:191], v[200:203], v[114:117]
	v_mfma_i32_16x16x64_i8 v[102:105], v[180:183], v[208:211], v[102:105]
	v_mfma_i32_16x16x64_i8 v[98:101], v[188:191], v[208:211], v[98:101]
	v_mfma_i32_16x16x64_i8 v[86:89], v[180:183], v[216:219], v[86:89]
	v_mfma_i32_16x16x64_i8 v[82:85], v[188:191], v[216:219], v[82:85]
	v_mfma_i32_16x16x64_i8 v[70:73], v[180:183], v[224:227], v[70:73]
	v_mfma_i32_16x16x64_i8 v[66:69], v[188:191], v[224:227], v[66:69]
	s_setprio 0
	s_barrier
	s_add_i32 s36, s66, s44
	v_lshl_add_u64 v[192:193], s[40:41], 0, v[134:135]
	s_mov_b32 m0, s36
	ds_read_b128 v[196:199], v176 offset:16384
	ds_read_b128 v[200:203], v176 offset:17408
	ds_read_b128 v[204:207], v176 offset:18432
	ds_read_b128 v[208:211], v176 offset:19456
	ds_read_b128 v[212:215], v176 offset:20480
	ds_read_b128 v[216:219], v176 offset:21504
	ds_read_b128 v[220:223], v176 offset:22528
	ds_read_b128 v[224:227], v176 offset:23552
	global_load_lds_dwordx4 v[192:193], off
	s_add_i32 m0, s36, 0x2000
	s_add_u32 s36, s40, 0x40000
	v_lshl_add_u64 v[228:229], s[40:41], 0, v[132:133]
	s_addc_u32 s37, s41, 0
	s_add_i32 s74, s67, s44
	global_load_lds_dwordx4 v[228:229], off
	v_lshl_add_u64 v[230:231], s[36:37], 0, v[134:135]
	s_mov_b32 m0, s74
	s_nop 0
	global_load_lds_dwordx4 v[230:231], off
	v_lshl_add_u64 v[230:231], s[36:37], 0, v[132:133]
	s_add_i32 m0, s74, 0x2000
	s_and_b64 s[36:37], s[8:9], s[42:43]
	s_and_b64 s[36:37], s[36:37], exec
	s_cselect_b32 s36, s26, s34
	s_cselect_b32 s37, s27, s35
	s_add_u32 s36, s36, s76
	s_addc_u32 s37, s37, 0
	global_load_lds_dwordx4 v[230:231], off
	v_lshl_add_u64 v[230:231], s[36:37], 0, v[136:137]
	s_mov_b32 m0, s47
	v_lshl_add_u64 v[232:233], s[36:37], 0, v[138:139]
	global_load_lds_dwordx4 v[230:231], off
	s_mov_b32 m0, s49
	s_nop 0
	global_load_lds_dwordx4 v[232:233], off
	s_waitcnt vmcnt(8) lgkmcnt(0)
	s_barrier
; #define PG8_LDA(dst, b, h) do { _Pragma("unroll") for (int m = 0; m < 4; ++m) dst[m] = PG8_LD32(lds + PG8_SA(b, h) + aoff + m * 2048); } while (0)
; #define PG8_LDB(dst, b, h) do { _Pragma("unroll") for (int n = 0; n < 2; ++n) dst[n] = PG8_LD32(lds + PG8_SB(b, h) + boff + n * 2048); } while (0)
; #define PG8_WAIT_V(n) asm volatile("s_waitcnt vmcnt(" #n ")" ::: "memory")
; #define PG8_WAIT_L(n) asm volatile("s_waitcnt lgkmcnt(" #n ")" ::: "memory")
; #define PG8_BAR __builtin_amdgcn_s_barrier()
; #define PG8_SCHED __builtin_amdgcn_sched_barrier(0)
; #define PG8_STA(bufoff, nextflag, h, koff) do { if constexpr (Sched::GATHER) { unsigned _o[2]; _o[0] = (nextflag) ? nxtA[h][0] : curA[h][0]; _o[1] = (nextflag) ? nxtA[h][1] : curA[h][1]; PG8_STAGE(bufoff, Ab + (koff), _o); } \
;         else { PG8_STAGE(bufoff, ((nextflag) ? nA : cA) + (size_t)(h) * hstep + (koff), voffA); } } while (0)
; template <class Epi, class Sched, bool ALIGN_EPI, int DT>
; __device__ __forceinline__ void gemm_phase(LAS unsigned char* lds, const int KB, const Sched& S, const Epi& E) {
;     ...
;             PG8_WAIT_V(8); PG8_WAIT_L(0); PG8_BAR; PG8_MMA(1, 0, At, B0); PG8_MMA(1, 1, At, B1); PG8_BAR; PG8_SCHED;
;             PG8_LDB(B0, 1, 0); PG8_LDB(B1, 1, 1); PG8_SCHED; PG8_LDA(At, 1, 0); PG8_STA(PG8_SA(0, 1), last, 1, k2);
;             PG8_WAIT_V(8); PG8_WAIT_L(0); PG8_BAR; PG8_MMA(0, 0, At, B0); PG8_MMA(0, 1, At, B1); PG8_BAR; PG8_SCHED;
	s_setprio 1
	s_waitcnt lgkmcnt(0)
	v_mfma_i32_16x16x64_i8 v[62:65], v[152:155], v[196:199], v[62:65]
	v_mfma_i32_16x16x64_i8 v[58:61], v[160:163], v[196:199], v[58:61]
	v_mfma_i32_16x16x64_i8 v[46:49], v[152:155], v[204:207], v[46:49]
	v_mfma_i32_16x16x64_i8 v[42:45], v[160:163], v[204:207], v[42:45]
	v_mfma_i32_16x16x64_i8 v[30:33], v[152:155], v[212:215], v[30:33]
	v_mfma_i32_16x16x64_i8 v[26:29], v[160:163], v[212:215], v[26:29]
	v_mfma_i32_16x16x64_i8 v[6:9], v[152:155], v[220:223], v[6:9]
	v_mfma_i32_16x16x64_i8 v[2:5], v[160:163], v[220:223], v[2:5]
	v_mfma_i32_16x16x64_i8 v[62:65], v[156:159], v[200:203], v[62:65]
	v_mfma_i32_16x16x64_i8 v[58:61], v[164:167], v[200:203], v[58:61]
	v_mfma_i32_16x16x64_i8 v[46:49], v[156:159], v[208:211], v[46:49]
	v_mfma_i32_16x16x64_i8 v[42:45], v[164:167], v[208:211], v[42:45]
	v_mfma_i32_16x16x64_i8 v[30:33], v[156:159], v[216:219], v[30:33]
	v_mfma_i32_16x16x64_i8 v[26:29], v[164:167], v[216:219], v[26:29]
	v_mfma_i32_16x16x64_i8 v[6:9], v[156:159], v[224:227], v[6:9]
	v_mfma_i32_16x16x64_i8 v[2:5], v[164:167], v[224:227], v[2:5]
	s_setprio 0
	s_setprio 1
	v_mfma_i32_16x16x64_i8 v[54:57], v[168:171], v[196:199], v[54:57]
	v_mfma_i32_16x16x64_i8 v[50:53], v[184:187], v[196:199], v[50:53]
	v_mfma_i32_16x16x64_i8 v[38:41], v[168:171], v[204:207], v[38:41]
	v_mfma_i32_16x16x64_i8 v[34:37], v[184:187], v[204:207], v[34:37]
	v_mfma_i32_16x16x64_i8 v[14:17], v[168:171], v[212:215], v[14:17]
	v_mfma_i32_16x16x64_i8 v[10:13], v[184:187], v[212:215], v[10:13]
	v_mfma_i32_16x16x64_i8 v[22:25], v[168:171], v[220:223], v[22:25]
	v_mfma_i32_16x16x64_i8 v[18:21], v[184:187], v[220:223], v[18:21]
	v_mfma_i32_16x16x64_i8 v[54:57], v[180:183], v[200:203], v[54:57]
	v_mfma_i32_16x16x64_i8 v[50:53], v[188:191], v[200:203], v[50:53]
	v_mfma_i32_16x16x64_i8 v[38:41], v[180:183], v[208:211], v[38:41]
	v_mfma_i32_16x16x64_i8 v[34:37], v[188:191], v[208:211], v[34:37]
	v_mfma_i32_16x16x64_i8 v[14:17], v[180:183], v[216:219], v[14:17]
	v_mfma_i32_16x16x64_i8 v[10:13], v[188:191], v[216:219], v[10:13]
	v_mfma_i32_16x16x64_i8 v[22:25], v[180:183], v[224:227], v[22:25]
	v_mfma_i32_16x16x64_i8 v[18:21], v[188:191], v[224:227], v[18:21]
	s_setprio 0
	s_barrier
	s_add_i32 s42, 0, 0x18000
	v_add_u32_e32 v1, s42, v172
	s_add_i32 s43, 0, 0x1c000
	ds_read_b128 v[152:155], v1
	ds_read_b128 v[156:159], v1 offset:1024
	ds_read_b128 v[160:163], v1 offset:2048
	ds_read_b128 v[164:167], v1 offset:3072
	v_add_u32_e32 v1, s43, v172
	ds_read_b128 v[168:171], v1
	ds_read_b128 v[180:183], v1 offset:1024
	ds_read_b128 v[184:187], v1 offset:2048
	ds_read_b128 v[188:191], v1 offset:3072
	s_add_u32 s36, s36, 0x40000
	s_addc_u32 s37, s37, 0
	s_mov_b32 m0, s52
	v_lshl_add_u64 v[234:235], s[36:37], 0, v[136:137]
	ds_read_b128 v[196:199], v176 offset:32768
	ds_read_b128 v[200:203], v176 offset:33792
	ds_read_b128 v[204:207], v176 offset:34816
	ds_read_b128 v[208:211], v176 offset:35840
	ds_read_b128 v[212:215], v176 offset:36864
	ds_read_b128 v[216:219], v176 offset:37888
	ds_read_b128 v[220:223], v176 offset:38912
	ds_read_b128 v[224:227], v176 offset:39936
	global_load_lds_dwordx4 v[234:235], off
	v_lshl_add_u64 v[234:235], s[36:37], 0, v[138:139]
	s_mov_b32 m0, s53
	s_nop 0
	global_load_lds_dwordx4 v[234:235], off
	s_waitcnt vmcnt(8) lgkmcnt(0)
	s_barrier
	s_setprio 1
	s_waitcnt lgkmcnt(0)
	v_mfma_i32_16x16x64_i8 v[126:129], v[152:155], v[196:199], v[126:129]
	v_mfma_i32_16x16x64_i8 v[122:125], v[160:163], v[196:199], v[122:125]
	v_mfma_i32_16x16x64_i8 v[110:113], v[152:155], v[204:207], v[110:113]
	v_mfma_i32_16x16x64_i8 v[106:109], v[160:163], v[204:207], v[106:109]
	v_mfma_i32_16x16x64_i8 v[94:97], v[152:155], v[212:215], v[94:97]
	v_mfma_i32_16x16x64_i8 v[90:93], v[160:163], v[212:215], v[90:93]
	v_mfma_i32_16x16x64_i8 v[78:81], v[152:155], v[220:223], v[78:81]
	v_mfma_i32_16x16x64_i8 v[74:77], v[160:163], v[220:223], v[74:77]
	v_mfma_i32_16x16x64_i8 v[126:129], v[156:159], v[200:203], v[126:129]
	v_mfma_i32_16x16x64_i8 v[122:125], v[164:167], v[200:203], v[122:125]
	v_mfma_i32_16x16x64_i8 v[110:113], v[156:159], v[208:211], v[110:113]
	v_mfma_i32_16x16x64_i8 v[106:109], v[164:167], v[208:211], v[106:109]
	v_mfma_i32_16x16x64_i8 v[94:97], v[156:159], v[216:219], v[94:97]
	v_mfma_i32_16x16x64_i8 v[90:93], v[164:167], v[216:219], v[90:93]
	v_mfma_i32_16x16x64_i8 v[78:81], v[156:159], v[224:227], v[78:81]
	v_mfma_i32_16x16x64_i8 v[74:77], v[164:167], v[224:227], v[74:77]
	s_setprio 0
	s_setprio 1
	v_mfma_i32_16x16x64_i8 v[118:121], v[168:171], v[196:199], v[118:121]
	v_mfma_i32_16x16x64_i8 v[114:117], v[184:187], v[196:199], v[114:117]
	v_mfma_i32_16x16x64_i8 v[102:105], v[168:171], v[204:207], v[102:105]
	v_mfma_i32_16x16x64_i8 v[98:101], v[184:187], v[204:207], v[98:101]
	v_mfma_i32_16x16x64_i8 v[86:89], v[168:171], v[212:215], v[86:89]
	v_mfma_i32_16x16x64_i8 v[82:85], v[184:187], v[212:215], v[82:85]
	v_mfma_i32_16x16x64_i8 v[70:73], v[168:171], v[220:223], v[70:73]
	v_mfma_i32_16x16x64_i8 v[66:69], v[184:187], v[220:223], v[66:69]
	v_mfma_i32_16x16x64_i8 v[118:121], v[180:183], v[200:203], v[118:121]
	v_mfma_i32_16x16x64_i8 v[114:117], v[188:191], v[200:203], v[114:117]
	v_mfma_i32_16x16x64_i8 v[102:105], v[180:183], v[208:211], v[102:105]
	v_mfma_i32_16x16x64_i8 v[98:101], v[188:191], v[208:211], v[98:101]
	v_mfma_i32_16x16x64_i8 v[86:89], v[180:183], v[216:219], v[86:89]
	v_mfma_i32_16x16x64_i8 v[82:85], v[188:191], v[216:219], v[82:85]
	v_mfma_i32_16x16x64_i8 v[70:73], v[180:183], v[224:227], v[70:73]
	v_mfma_i32_16x16x64_i8 v[66:69], v[188:191], v[224:227], v[66:69]
	s_setprio 0
	s_barrier
; #define PG8_STAGE(bufoff, gbase, voff) do { _Pragma("unroll") for (int _i = 0; _i < 2; ++_i) \
;         __builtin_amdgcn_global_load_lds((const unsigned*)((const char*)(gbase) + (voff)[_i]), (LAS unsigned*)(lds + (bufoff) + ldsw + _i * 8192), 16, 0, 0); } while (0)
; #define PG8_LDA(dst, b, h) do { _Pragma("unroll") for (int m = 0; m < 4; ++m) dst[m] = PG8_LD32(lds + PG8_SA(b, h) + aoff + m * 2048); } while (0)
; #define PG8_WAIT_V(n) asm volatile("s_waitcnt vmcnt(" #n ")" ::: "memory")
; #define PG8_WAIT_L(n) asm volatile("s_waitcnt lgkmcnt(" #n ")" ::: "memory")
; #define PG8_BAR __builtin_amdgcn_s_barrier()
; #define PG8_SCHED __builtin_amdgcn_sched_barrier(0)
; #define PG8_STA(bufoff, nextflag, h, koff) do { if constexpr (Sched::GATHER) { unsigned _o[2]; _o[0] = (nextflag) ? nxtA[h][0] : curA[h][0]; _o[1] = (nextflag) ? nxtA[h][1] : curA[h][1]; PG8_STAGE(bufoff, Ab + (koff), _o); } \
;         else { PG8_STAGE(bufoff, ((nextflag) ? nA : cA) + (size_t)(h) * hstep + (koff), voffA); } } while (0)
; template <class Epi, class Sched, bool ALIGN_EPI, int DT>
; __device__ __forceinline__ void gemm_phase(LAS unsigned char* lds, const int KB, const Sched& S, const Epi& E) {
;     ...
;             PG8_LDA(At, 1, 1); PG8_STAGE(PG8_SB(1, 0), b3, voffB); PG8_STAGE(PG8_SB(1, 1), b3 + hstep, voffB); PG8_STA(PG8_SA(1, 0), last, 0, k3);
;             PG8_WAIT_V(8); PG8_WAIT_L(0); PG8_BAR; PG8_MMA(1, 0, At, B0); PG8_MMA(1, 1, At, B1); PG8_BAR; PG8_SCHED;
;         }
;         if constexpr (ALIGN_EPI) { if (wr == 0) PG8_BAR; }
	s_add_i32 s36, s42, s44
	v_lshl_add_u64 v[192:193], v[192:193], 0, s[18:19]
	s_mov_b32 m0, s36
	ds_read_b128 v[196:199], v176 offset:49152
	ds_read_b128 v[200:203], v176 offset:50176
	ds_read_b128 v[204:207], v176 offset:51200
	ds_read_b128 v[208:211], v176 offset:52224
	ds_read_b128 v[212:215], v176 offset:53248
	ds_read_b128 v[216:219], v176 offset:54272
	ds_read_b128 v[220:223], v176 offset:55296
	ds_read_b128 v[224:227], v176 offset:56320
	global_load_lds_dwordx4 v[192:193], off
	s_add_i32 m0, s36, 0x2000
	s_add_u32 s36, s40, 0x40080
	v_lshl_add_u64 v[192:193], v[228:229], 0, s[18:19]
	s_addc_u32 s37, s41, 0
	s_add_i32 s40, s43, s44
	global_load_lds_dwordx4 v[192:193], off
	v_lshl_add_u64 v[192:193], s[36:37], 0, v[134:135]
	s_mov_b32 m0, s40
	s_nop 0
	global_load_lds_dwordx4 v[192:193], off
	v_lshl_add_u64 v[192:193], s[36:37], 0, v[132:133]
	s_add_i32 m0, s40, 0x2000
	s_nop 0
	global_load_lds_dwordx4 v[192:193], off
	v_lshl_add_u64 v[192:193], v[230:231], 0, s[18:19]
	s_mov_b32 m0, s57
	s_nop 0
	global_load_lds_dwordx4 v[192:193], off
	v_lshl_add_u64 v[192:193], v[232:233], 0, s[18:19]
	s_mov_b32 m0, s62
	s_nop 0
	global_load_lds_dwordx4 v[192:193], off
	s_waitcnt vmcnt(8) lgkmcnt(0)
	s_barrier
	s_setprio 1
	s_waitcnt lgkmcnt(0)
	v_mfma_i32_16x16x64_i8 v[62:65], v[152:155], v[196:199], v[62:65]
	v_mfma_i32_16x16x64_i8 v[58:61], v[160:163], v[196:199], v[58:61]
	v_mfma_i32_16x16x64_i8 v[46:49], v[152:155], v[204:207], v[46:49]
	v_mfma_i32_16x16x64_i8 v[42:45], v[160:163], v[204:207], v[42:45]
	v_mfma_i32_16x16x64_i8 v[30:33], v[152:155], v[212:215], v[30:33]
	v_mfma_i32_16x16x64_i8 v[26:29], v[160:163], v[212:215], v[26:29]
	v_mfma_i32_16x16x64_i8 v[6:9], v[152:155], v[220:223], v[6:9]
	v_mfma_i32_16x16x64_i8 v[2:5], v[160:163], v[220:223], v[2:5]
	v_mfma_i32_16x16x64_i8 v[62:65], v[156:159], v[200:203], v[62:65]
	v_mfma_i32_16x16x64_i8 v[58:61], v[164:167], v[200:203], v[58:61]
	v_mfma_i32_16x16x64_i8 v[46:49], v[156:159], v[208:211], v[46:49]
	v_mfma_i32_16x16x64_i8 v[42:45], v[164:167], v[208:211], v[42:45]
	v_mfma_i32_16x16x64_i8 v[30:33], v[156:159], v[216:219], v[30:33]
	v_mfma_i32_16x16x64_i8 v[26:29], v[164:167], v[216:219], v[26:29]
	v_mfma_i32_16x16x64_i8 v[6:9], v[156:159], v[224:227], v[6:9]
	v_mfma_i32_16x16x64_i8 v[2:5], v[164:167], v[224:227], v[2:5]
	s_setprio 0
	s_setprio 1
	v_mfma_i32_16x16x64_i8 v[54:57], v[168:171], v[196:199], v[54:57]
	v_mfma_i32_16x16x64_i8 v[50:53], v[184:187], v[196:199], v[50:53]
	v_mfma_i32_16x16x64_i8 v[38:41], v[168:171], v[204:207], v[38:41]
	v_mfma_i32_16x16x64_i8 v[34:37], v[184:187], v[204:207], v[34:37]
	v_mfma_i32_16x16x64_i8 v[14:17], v[168:171], v[212:215], v[14:17]
	v_mfma_i32_16x16x64_i8 v[10:13], v[184:187], v[212:215], v[10:13]
	v_mfma_i32_16x16x64_i8 v[22:25], v[168:171], v[220:223], v[22:25]
	v_mfma_i32_16x16x64_i8 v[18:21], v[184:187], v[220:223], v[18:21]
	v_mfma_i32_16x16x64_i8 v[54:57], v[180:183], v[200:203], v[54:57]
	v_mfma_i32_16x16x64_i8 v[50:53], v[188:191], v[200:203], v[50:53]
	v_mfma_i32_16x16x64_i8 v[38:41], v[180:183], v[208:211], v[38:41]
	v_mfma_i32_16x16x64_i8 v[34:37], v[188:191], v[208:211], v[34:37]
	v_mfma_i32_16x16x64_i8 v[14:17], v[180:183], v[216:219], v[14:17]
	v_mfma_i32_16x16x64_i8 v[10:13], v[188:191], v[216:219], v[10:13]
	v_mfma_i32_16x16x64_i8 v[22:25], v[180:183], v[224:227], v[22:25]
	v_mfma_i32_16x16x64_i8 v[18:21], v[188:191], v[224:227], v[18:21]
	s_setprio 0
	s_barrier
	s_add_i32 s71, s71, 2
	s_cmp_gt_u32 s71, 13
	s_mov_b64 s[36:37], s[38:39]
	s_cbranch_scc0 .LBB0_1385
	s_and_b64 vcc, exec, s[20:21]
	s_cbranch_vccz .LBB0_1388
	s_barrier

; #define PG8_STAGE(bufoff, gbase, voff) do { _Pragma("unroll") for (int _i = 0; _i < 2; ++_i) \
;         __builtin_amdgcn_global_load_lds((const unsigned*)((const char*)(gbase) + (voff)[_i]), (LAS unsigned*)(lds + (bufoff) + ldsw + _i * 8192), 16, 0, 0); } while (0)
; #define PG8_LDA(dst, b, h) do { _Pragma("unroll") for (int m = 0; m < 4; ++m) dst[m] = PG8_LD32(lds + PG8_SA(b, h) + aoff + m * 2048); } while (0)
; #define PG8_LDB(dst, b, h) do { _Pragma("unroll") for (int n = 0; n < 2; ++n) dst[n] = PG8_LD32(lds + PG8_SB(b, h) + boff + n * 2048); } while (0)
; #define PG8_WAIT_V(n) asm volatile("s_waitcnt vmcnt(" #n ")" ::: "memory")
; #define PG8_WAIT_L(n) asm volatile("s_waitcnt lgkmcnt(" #n ")" ::: "memory")
; #define PG8_BAR __builtin_amdgcn_s_barrier()
; #define PG8_SCHED __builtin_amdgcn_sched_barrier(0)
; #define PG8_STA(bufoff, nextflag, h, koff) do { if constexpr (Sched::GATHER) { unsigned _o[2]; _o[0] = (nextflag) ? nxtA[h][0] : curA[h][0]; _o[1] = (nextflag) ? nxtA[h][1] : curA[h][1]; PG8_STAGE(bufoff, Ab + (koff), _o); } \
;         else { PG8_STAGE(bufoff, ((nextflag) ? nA : cA) + (size_t)(h) * hstep + (koff), voffA); } } while (0)
; template <class Epi, class Sched, bool ALIGN_EPI, int DT>
; __device__ __forceinline__ void gemm_phase(LAS unsigned char* lds, const int KB, const Sched& S, const Epi& E) {
;     ...
;             PG8_LDB(B0, 0, 0); PG8_LDB(B1, 0, 1); PG8_SCHED; PG8_LDA(At, 0, 0); PG8_STA(PG8_SA(1, 1), false, 1, k1);
;             PG8_WAIT_V(8); PG8_WAIT_L(0); PG8_BAR; PG8_MMA(0, 0, At, B0); PG8_MMA(0, 1, At, B1); PG8_BAR; PG8_SCHED;
;             PG8_LDA(At, 0, 1); PG8_STAGE(PG8_SB(0, 0), b2, voffB); PG8_STAGE(PG8_SB(0, 1), b2 + hstep, voffB); PG8_STA(PG8_SA(0, 0), last, 0, k2);
;             PG8_WAIT_V(8); PG8_WAIT_L(0); PG8_BAR; PG8_MMA(1, 0, At, B0); PG8_MMA(1, 1, At, B1); PG8_BAR; PG8_SCHED;
.LBB0_2108:
	ds_read_b128 v[18:21], v193
	ds_read_b128 v[22:25], v193 offset:1024
	ds_read_b128 v[26:29], v193 offset:2048
	ds_read_b128 v[30:33], v193 offset:3072
	ds_read_b128 v[2:5], v195
	ds_read_b128 v[6:9], v195 offset:1024
	ds_read_b128 v[10:13], v195 offset:2048
	ds_read_b128 v[14:17], v195 offset:3072
	s_add_u32 s38, s42, 0x100
	s_addc_u32 s39, s43, 0
	s_add_u32 s71, s68, s42
	s_addc_u32 s74, s69, s43
	s_cmp_eq_u32 s70, 12
	s_cselect_b64 s[44:45], -1, 0
	s_and_b64 s[40:41], s[44:45], exec
	s_cselect_b32 s41, s25, s74
	s_cselect_b32 s40, s27, s71
	s_cselect_b32 s71, 0, s39
	s_cselect_b32 s74, 0, s38
	v_lshl_add_u64 v[222:223], v[178:179], 0, s[42:43]
	s_add_i32 m0, s35, 0xc000
	ds_read_b128 v[182:185], v196
	ds_read_b128 v[186:189], v196 offset:1024
	ds_read_b128 v[198:201], v196 offset:2048
	ds_read_b128 v[202:205], v196 offset:3072
	ds_read_b128 v[206:209], v196 offset:4096
	ds_read_b128 v[210:213], v196 offset:5120
	ds_read_b128 v[214:217], v196 offset:6144
	ds_read_b128 v[218:221], v196 offset:7168
	global_load_lds_dwordx4 v[222:223], off
	v_lshl_add_u64 v[222:223], v[180:181], 0, s[42:43]
	s_add_i32 m0, s35, 0xe000
	s_nop 0
	global_load_lds_dwordx4 v[222:223], off
	s_waitcnt vmcnt(8) lgkmcnt(0)
	s_barrier
	s_setprio 1
	s_waitcnt lgkmcnt(0)
	v_mfma_scale_f32_16x16x128_f8f6f4 v[158:161], v[18:25], v[182:189], v[158:161], v1, v1 op_sel_hi:[0,0,0]
	v_mfma_scale_f32_16x16x128_f8f6f4 v[154:157], v[26:33], v[182:189], v[154:157], v1, v1 op_sel_hi:[0,0,0]
	v_mfma_scale_f32_16x16x128_f8f6f4 v[150:153], v[18:25], v[198:205], v[150:153], v1, v1 op_sel_hi:[0,0,0]
	v_mfma_scale_f32_16x16x128_f8f6f4 v[142:145], v[26:33], v[198:205], v[142:145], v1, v1 op_sel_hi:[0,0,0]
	v_mfma_scale_f32_16x16x128_f8f6f4 v[134:137], v[18:25], v[206:213], v[134:137], v1, v1 op_sel_hi:[0,0,0]
	v_mfma_scale_f32_16x16x128_f8f6f4 v[126:129], v[26:33], v[206:213], v[126:129], v1, v1 op_sel_hi:[0,0,0]
	v_mfma_scale_f32_16x16x128_f8f6f4 v[118:121], v[18:25], v[214:221], v[118:121], v1, v1 op_sel_hi:[0,0,0]
	v_mfma_scale_f32_16x16x128_f8f6f4 v[110:113], v[26:33], v[214:221], v[110:113], v1, v1 op_sel_hi:[0,0,0]
	s_setprio 0
	s_setprio 1
	v_mfma_scale_f32_16x16x128_f8f6f4 v[146:149], v[2:9], v[182:189], v[146:149], v1, v1 op_sel_hi:[0,0,0]
	v_mfma_scale_f32_16x16x128_f8f6f4 v[138:141], v[10:17], v[182:189], v[138:141], v1, v1 op_sel_hi:[0,0,0]
	v_mfma_scale_f32_16x16x128_f8f6f4 v[130:133], v[2:9], v[198:205], v[130:133], v1, v1 op_sel_hi:[0,0,0]
	v_mfma_scale_f32_16x16x128_f8f6f4 v[122:125], v[10:17], v[198:205], v[122:125], v1, v1 op_sel_hi:[0,0,0]
	v_mfma_scale_f32_16x16x128_f8f6f4 v[114:117], v[2:9], v[206:213], v[114:117], v1, v1 op_sel_hi:[0,0,0]
	v_mfma_scale_f32_16x16x128_f8f6f4 v[106:109], v[10:17], v[206:213], v[106:109], v1, v1 op_sel_hi:[0,0,0]
	v_mfma_scale_f32_16x16x128_f8f6f4 v[102:105], v[2:9], v[214:221], v[102:105], v1, v1 op_sel_hi:[0,0,0]
	v_mfma_scale_f32_16x16x128_f8f6f4 v[98:101], v[10:17], v[214:221], v[98:101], v1, v1 op_sel_hi:[0,0,0]
	s_setprio 0
	s_barrier
	s_add_i32 s42, s57, s46
	v_lshl_add_u64 v[182:183], s[40:41], 0, v[162:163]
	s_mov_b32 m0, s42
	ds_read_b128 v[198:201], v196 offset:16384
	ds_read_b128 v[202:205], v196 offset:17408
	ds_read_b128 v[206:209], v196 offset:18432
	ds_read_b128 v[210:213], v196 offset:19456
	ds_read_b128 v[214:217], v196 offset:20480
	ds_read_b128 v[218:221], v196 offset:21504
	ds_read_b128 v[222:225], v196 offset:22528
	ds_read_b128 v[226:229], v196 offset:23552
	global_load_lds_dwordx4 v[182:183], off
	s_add_i32 m0, s42, 0x2000
	s_add_u32 s42, s40, 0x40000
	v_lshl_add_u64 v[184:185], s[40:41], 0, v[164:165]
	s_addc_u32 s43, s41, 0
	s_add_i32 s75, s62, s46
	global_load_lds_dwordx4 v[184:185], off
	v_lshl_add_u64 v[186:187], s[42:43], 0, v[162:163]
	s_mov_b32 m0, s75
	s_nop 0
	global_load_lds_dwordx4 v[186:187], off
	v_lshl_add_u64 v[186:187], s[42:43], 0, v[164:165]
	s_add_i32 m0, s75, 0x2000
	s_and_b64 s[42:43], s[6:7], s[44:45]
	s_and_b64 s[42:43], s[42:43], exec
	s_cselect_b32 s42, s28, s36
	s_cselect_b32 s43, s29, s37
	s_add_u32 s42, s42, s74
	s_addc_u32 s43, s43, s71
	global_load_lds_dwordx4 v[186:187], off
	v_lshl_add_u64 v[186:187], s[42:43], 0, v[166:167]
	s_mov_b32 m0, s35
	v_lshl_add_u64 v[188:189], s[42:43], 0, v[168:169]
	global_load_lds_dwordx4 v[186:187], off
	s_mov_b32 m0, s47
	s_nop 0
	global_load_lds_dwordx4 v[188:189], off
	s_waitcnt vmcnt(8) lgkmcnt(0)
	s_barrier
	s_setprio 1
	s_waitcnt lgkmcnt(0)
	v_mfma_scale_f32_16x16x128_f8f6f4 v[94:97], v[18:25], v[198:205], v[94:97], v1, v1 op_sel_hi:[0,0,0]
	v_mfma_scale_f32_16x16x128_f8f6f4 v[90:93], v[26:33], v[198:205], v[90:93], v1, v1 op_sel_hi:[0,0,0]
	v_mfma_scale_f32_16x16x128_f8f6f4 v[86:89], v[18:25], v[206:213], v[86:89], v1, v1 op_sel_hi:[0,0,0]
	v_mfma_scale_f32_16x16x128_f8f6f4 v[78:81], v[26:33], v[206:213], v[78:81], v1, v1 op_sel_hi:[0,0,0]
	v_mfma_scale_f32_16x16x128_f8f6f4 v[62:65], v[18:25], v[214:221], v[62:65], v1, v1 op_sel_hi:[0,0,0]
	v_mfma_scale_f32_16x16x128_f8f6f4 v[54:57], v[26:33], v[214:221], v[54:57], v1, v1 op_sel_hi:[0,0,0]
	v_mfma_scale_f32_16x16x128_f8f6f4 v[46:49], v[18:25], v[222:229], v[46:49], v1, v1 op_sel_hi:[0,0,0]
	v_mfma_scale_f32_16x16x128_f8f6f4 v[38:41], v[26:33], v[222:229], v[38:41], v1, v1 op_sel_hi:[0,0,0]
	s_setprio 0
	s_setprio 1
	v_mfma_scale_f32_16x16x128_f8f6f4 v[82:85], v[2:9], v[198:205], v[82:85], v1, v1 op_sel_hi:[0,0,0]
	v_mfma_scale_f32_16x16x128_f8f6f4 v[74:77], v[10:17], v[198:205], v[74:77], v1, v1 op_sel_hi:[0,0,0]
	v_mfma_scale_f32_16x16x128_f8f6f4 v[58:61], v[2:9], v[206:213], v[58:61], v1, v1 op_sel_hi:[0,0,0]
	v_mfma_scale_f32_16x16x128_f8f6f4 v[50:53], v[10:17], v[206:213], v[50:53], v1, v1 op_sel_hi:[0,0,0]
	v_mfma_scale_f32_16x16x128_f8f6f4 v[42:45], v[2:9], v[214:221], v[42:45], v1, v1 op_sel_hi:[0,0,0]
	v_mfma_scale_f32_16x16x128_f8f6f4 v[34:37], v[10:17], v[214:221], v[34:37], v1, v1 op_sel_hi:[0,0,0]
	v_mfma_scale_f32_16x16x128_f8f6f4 v[70:73], v[2:9], v[222:229], v[70:73], v1, v1 op_sel_hi:[0,0,0]
	v_mfma_scale_f32_16x16x128_f8f6f4 v[66:69], v[10:17], v[222:229], v[66:69], v1, v1 op_sel_hi:[0,0,0]
	s_setprio 0
	s_barrier
; #define PG8_STAGE(bufoff, gbase, voff) do { _Pragma("unroll") for (int _i = 0; _i < 2; ++_i) \
;         __builtin_amdgcn_global_load_lds((const unsigned*)((const char*)(gbase) + (voff)[_i]), (LAS unsigned*)(lds + (bufoff) + ldsw + _i * 8192), 16, 0, 0); } while (0)
; #define PG8_LDA(dst, b, h) do { _Pragma("unroll") for (int m = 0; m < 4; ++m) dst[m] = PG8_LD32(lds + PG8_SA(b, h) + aoff + m * 2048); } while (0)
; #define PG8_LDB(dst, b, h) do { _Pragma("unroll") for (int n = 0; n < 2; ++n) dst[n] = PG8_LD32(lds + PG8_SB(b, h) + boff + n * 2048); } while (0)
; #define PG8_WAIT_V(n) asm volatile("s_waitcnt vmcnt(" #n ")" ::: "memory")
; #define PG8_WAIT_L(n) asm volatile("s_waitcnt lgkmcnt(" #n ")" ::: "memory")
; #define PG8_BAR __builtin_amdgcn_s_barrier()
; #define PG8_SCHED __builtin_amdgcn_sched_barrier(0)
; #define PG8_STA(bufoff, nextflag, h, koff) do { if constexpr (Sched::GATHER) { unsigned _o[2]; _o[0] = (nextflag) ? nxtA[h][0] : curA[h][0]; _o[1] = (nextflag) ? nxtA[h][1] : curA[h][1]; PG8_STAGE(bufoff, Ab + (koff), _o); } \
;         else { PG8_STAGE(bufoff, ((nextflag) ? nA : cA) + (size_t)(h) * hstep + (koff), voffA); } } while (0)
; template <class Epi, class Sched, bool ALIGN_EPI, int DT>
; __device__ __forceinline__ void gemm_phase(LAS unsigned char* lds, const int KB, const Sched& S, const Epi& E) {
;     ...
;             PG8_LDB(B0, 1, 0); PG8_LDB(B1, 1, 1); PG8_SCHED; PG8_LDA(At, 1, 0); PG8_STA(PG8_SA(0, 1), last, 1, k2);
;             PG8_WAIT_V(8); PG8_WAIT_L(0); PG8_BAR; PG8_MMA(0, 0, At, B0); PG8_MMA(0, 1, At, B1); PG8_BAR; PG8_SCHED;
;             PG8_LDA(At, 1, 1); PG8_STAGE(PG8_SB(1, 0), b3, voffB); PG8_STAGE(PG8_SB(1, 1), b3 + hstep, voffB); PG8_STA(PG8_SA(1, 0), last, 0, k3);
;             PG8_WAIT_V(8); PG8_WAIT_L(0); PG8_BAR; PG8_MMA(1, 0, At, B0); PG8_MMA(1, 1, At, B1); PG8_BAR; PG8_SCHED;
;         }
;         if constexpr (ALIGN_EPI) { if (wr == 0) PG8_BAR; }
	s_add_i32 s44, 0, 0x18000
	s_add_i32 s45, 0, 0x1c000
	v_add_u32_e32 v14, s44, v191
	v_add_u32_e32 v30, s45, v191
	ds_read_b128 v[2:5], v14
	ds_read_b128 v[6:9], v14 offset:1024
	ds_read_b128 v[10:13], v14 offset:2048
	ds_read_b128 v[14:17], v14 offset:3072
	ds_read_b128 v[18:21], v30
	ds_read_b128 v[22:25], v30 offset:1024
	ds_read_b128 v[26:29], v30 offset:2048
	ds_read_b128 v[30:33], v30 offset:3072
	s_add_u32 s42, s42, 0x40000
	s_addc_u32 s43, s43, 0
	s_mov_b32 m0, s49
	v_lshl_add_u64 v[230:231], s[42:43], 0, v[166:167]
	ds_read_b128 v[198:201], v196 offset:32768
	ds_read_b128 v[202:205], v196 offset:33792
	ds_read_b128 v[206:209], v196 offset:34816
	ds_read_b128 v[210:213], v196 offset:35840
	ds_read_b128 v[214:217], v196 offset:36864
	ds_read_b128 v[218:221], v196 offset:37888
	ds_read_b128 v[222:225], v196 offset:38912
	ds_read_b128 v[226:229], v196 offset:39936
	global_load_lds_dwordx4 v[230:231], off
	v_lshl_add_u64 v[230:231], s[42:43], 0, v[168:169]
	s_mov_b32 m0, s52
	s_nop 0
	global_load_lds_dwordx4 v[230:231], off
	s_waitcnt vmcnt(8) lgkmcnt(0)
	s_barrier
	s_setprio 1
	s_waitcnt lgkmcnt(0)
	v_mfma_scale_f32_16x16x128_f8f6f4 v[158:161], v[2:9], v[198:205], v[158:161], v1, v1 op_sel_hi:[0,0,0]
	v_mfma_scale_f32_16x16x128_f8f6f4 v[154:157], v[10:17], v[198:205], v[154:157], v1, v1 op_sel_hi:[0,0,0]
	v_mfma_scale_f32_16x16x128_f8f6f4 v[150:153], v[2:9], v[206:213], v[150:153], v1, v1 op_sel_hi:[0,0,0]
	v_mfma_scale_f32_16x16x128_f8f6f4 v[142:145], v[10:17], v[206:213], v[142:145], v1, v1 op_sel_hi:[0,0,0]
	v_mfma_scale_f32_16x16x128_f8f6f4 v[134:137], v[2:9], v[214:221], v[134:137], v1, v1 op_sel_hi:[0,0,0]
	v_mfma_scale_f32_16x16x128_f8f6f4 v[126:129], v[10:17], v[214:221], v[126:129], v1, v1 op_sel_hi:[0,0,0]
	v_mfma_scale_f32_16x16x128_f8f6f4 v[118:121], v[2:9], v[222:229], v[118:121], v1, v1 op_sel_hi:[0,0,0]
	v_mfma_scale_f32_16x16x128_f8f6f4 v[110:113], v[10:17], v[222:229], v[110:113], v1, v1 op_sel_hi:[0,0,0]
	s_setprio 0
	s_setprio 1
	v_mfma_scale_f32_16x16x128_f8f6f4 v[146:149], v[18:25], v[198:205], v[146:149], v1, v1 op_sel_hi:[0,0,0]
	v_mfma_scale_f32_16x16x128_f8f6f4 v[138:141], v[26:33], v[198:205], v[138:141], v1, v1 op_sel_hi:[0,0,0]
	v_mfma_scale_f32_16x16x128_f8f6f4 v[130:133], v[18:25], v[206:213], v[130:133], v1, v1 op_sel_hi:[0,0,0]
	v_mfma_scale_f32_16x16x128_f8f6f4 v[122:125], v[26:33], v[206:213], v[122:125], v1, v1 op_sel_hi:[0,0,0]
	v_mfma_scale_f32_16x16x128_f8f6f4 v[114:117], v[18:25], v[214:221], v[114:117], v1, v1 op_sel_hi:[0,0,0]
	v_mfma_scale_f32_16x16x128_f8f6f4 v[106:109], v[26:33], v[214:221], v[106:109], v1, v1 op_sel_hi:[0,0,0]
	v_mfma_scale_f32_16x16x128_f8f6f4 v[102:105], v[18:25], v[222:229], v[102:105], v1, v1 op_sel_hi:[0,0,0]
	v_mfma_scale_f32_16x16x128_f8f6f4 v[98:101], v[26:33], v[222:229], v[98:101], v1, v1 op_sel_hi:[0,0,0]
	s_setprio 0
	s_barrier
	s_add_i32 s42, s44, s46
	v_lshl_add_u64 v[182:183], v[182:183], 0, s[10:11]
	s_mov_b32 m0, s42
	ds_read_b128 v[198:201], v196 offset:49152
	ds_read_b128 v[202:205], v196 offset:50176
	ds_read_b128 v[206:209], v196 offset:51200
	ds_read_b128 v[210:213], v196 offset:52224
	ds_read_b128 v[214:217], v196 offset:53248
	ds_read_b128 v[218:221], v196 offset:54272
	ds_read_b128 v[222:225], v196 offset:55296
	ds_read_b128 v[226:229], v196 offset:56320
	global_load_lds_dwordx4 v[182:183], off
	s_add_i32 m0, s42, 0x2000
	s_add_u32 s40, s40, 0x40080
	v_lshl_add_u64 v[182:183], v[184:185], 0, s[10:11]
	s_addc_u32 s41, s41, 0
	s_add_i32 s42, s45, s46
	global_load_lds_dwordx4 v[182:183], off
	v_lshl_add_u64 v[182:183], s[40:41], 0, v[162:163]
	s_mov_b32 m0, s42
	s_nop 0
	global_load_lds_dwordx4 v[182:183], off
	v_lshl_add_u64 v[182:183], s[40:41], 0, v[164:165]
	s_add_i32 m0, s42, 0x2000
	s_nop 0
	global_load_lds_dwordx4 v[182:183], off
	v_lshl_add_u64 v[182:183], v[186:187], 0, s[10:11]
	s_mov_b32 m0, s54
	s_nop 0
	global_load_lds_dwordx4 v[182:183], off
	v_lshl_add_u64 v[182:183], v[188:189], 0, s[10:11]
	s_mov_b32 m0, s55
	s_nop 0
	global_load_lds_dwordx4 v[182:183], off
	s_waitcnt vmcnt(8) lgkmcnt(0)
	s_barrier
	s_setprio 1
	s_waitcnt lgkmcnt(0)
	v_mfma_scale_f32_16x16x128_f8f6f4 v[94:97], v[2:9], v[198:205], v[94:97], v1, v1 op_sel_hi:[0,0,0]
	v_mfma_scale_f32_16x16x128_f8f6f4 v[90:93], v[10:17], v[198:205], v[90:93], v1, v1 op_sel_hi:[0,0,0]
	v_mfma_scale_f32_16x16x128_f8f6f4 v[86:89], v[2:9], v[206:213], v[86:89], v1, v1 op_sel_hi:[0,0,0]
	v_mfma_scale_f32_16x16x128_f8f6f4 v[78:81], v[10:17], v[206:213], v[78:81], v1, v1 op_sel_hi:[0,0,0]
	v_mfma_scale_f32_16x16x128_f8f6f4 v[62:65], v[2:9], v[214:221], v[62:65], v1, v1 op_sel_hi:[0,0,0]
	v_mfma_scale_f32_16x16x128_f8f6f4 v[54:57], v[10:17], v[214:221], v[54:57], v1, v1 op_sel_hi:[0,0,0]
	v_mfma_scale_f32_16x16x128_f8f6f4 v[46:49], v[2:9], v[222:229], v[46:49], v1, v1 op_sel_hi:[0,0,0]
	v_mfma_scale_f32_16x16x128_f8f6f4 v[38:41], v[10:17], v[222:229], v[38:41], v1, v1 op_sel_hi:[0,0,0]
	s_setprio 0
	s_setprio 1
	v_mfma_scale_f32_16x16x128_f8f6f4 v[82:85], v[18:25], v[198:205], v[82:85], v1, v1 op_sel_hi:[0,0,0]
	v_mfma_scale_f32_16x16x128_f8f6f4 v[74:77], v[26:33], v[198:205], v[74:77], v1, v1 op_sel_hi:[0,0,0]
	v_mfma_scale_f32_16x16x128_f8f6f4 v[58:61], v[18:25], v[206:213], v[58:61], v1, v1 op_sel_hi:[0,0,0]
	v_mfma_scale_f32_16x16x128_f8f6f4 v[50:53], v[26:33], v[206:213], v[50:53], v1, v1 op_sel_hi:[0,0,0]
	v_mfma_scale_f32_16x16x128_f8f6f4 v[42:45], v[18:25], v[214:221], v[42:45], v1, v1 op_sel_hi:[0,0,0]
	v_mfma_scale_f32_16x16x128_f8f6f4 v[34:37], v[26:33], v[214:221], v[34:37], v1, v1 op_sel_hi:[0,0,0]
	v_mfma_scale_f32_16x16x128_f8f6f4 v[70:73], v[18:25], v[222:229], v[70:73], v1, v1 op_sel_hi:[0,0,0]
	v_mfma_scale_f32_16x16x128_f8f6f4 v[66:69], v[26:33], v[222:229], v[66:69], v1, v1 op_sel_hi:[0,0,0]
	s_setprio 0
	s_barrier
	s_add_i32 s70, s70, 2
	s_cmp_gt_u32 s70, 13
	s_mov_b64 s[42:43], s[38:39]
	s_cbranch_scc0 .LBB0_2108
	s_and_b64 vcc, exec, s[12:13]
	s_cbranch_vccz .LBB0_2111
	s_barrier

; #define PG8_STAGE(bufoff, gbase, voff) do { _Pragma("unroll") for (int _i = 0; _i < 2; ++_i) \
;         __builtin_amdgcn_global_load_lds((const unsigned*)((const char*)(gbase) + (voff)[_i]), (LAS unsigned*)(lds + (bufoff) + ldsw + _i * 8192), 16, 0, 0); } while (0)
; #define PG8_LDA(dst, b, h) do { _Pragma("unroll") for (int m = 0; m < 4; ++m) dst[m] = PG8_LD32(lds + PG8_SA(b, h) + aoff + m * 2048); } while (0)
; #define PG8_LDB(dst, b, h) do { _Pragma("unroll") for (int n = 0; n < 2; ++n) dst[n] = PG8_LD32(lds + PG8_SB(b, h) + boff + n * 2048); } while (0)
; #define PG8_WAIT_V(n) asm volatile("s_waitcnt vmcnt(" #n ")" ::: "memory")
; #define PG8_WAIT_L(n) asm volatile("s_waitcnt lgkmcnt(" #n ")" ::: "memory")
; #define PG8_BAR __builtin_amdgcn_s_barrier()
; #define PG8_SCHED __builtin_amdgcn_sched_barrier(0)
; #define PG8_STA(bufoff, nextflag, h, koff) do { if constexpr (Sched::GATHER) { unsigned _o[2]; _o[0] = (nextflag) ? nxtA[h][0] : curA[h][0]; _o[1] = (nextflag) ? nxtA[h][1] : curA[h][1]; PG8_STAGE(bufoff, Ab + (koff), _o); } \
;         else { PG8_STAGE(bufoff, ((nextflag) ? nA : cA) + (size_t)(h) * hstep + (koff), voffA); } } while (0)
; template <class Epi, class Sched, bool ALIGN_EPI, int DT>
; __device__ __forceinline__ void gemm_phase(LAS unsigned char* lds, const int KB, const Sched& S, const Epi& E) {
;     ...
;             PG8_LDB(B0, 0, 0); PG8_LDB(B1, 0, 1); PG8_SCHED; PG8_LDA(At, 0, 0); PG8_STA(PG8_SA(1, 1), false, 1, k1);
;             PG8_WAIT_V(8); PG8_WAIT_L(0); PG8_BAR; PG8_MMA(0, 0, At, B0); PG8_MMA(0, 1, At, B1); PG8_BAR; PG8_SCHED;
;             PG8_LDA(At, 0, 1); PG8_STAGE(PG8_SB(0, 0), b2, voffB); PG8_STAGE(PG8_SB(0, 1), b2 + hstep, voffB); PG8_STA(PG8_SA(0, 0), last, 0, k2);
;             PG8_WAIT_V(8); PG8_WAIT_L(0); PG8_BAR; PG8_MMA(1, 0, At, B0); PG8_MMA(1, 1, At, B1); PG8_BAR; PG8_SCHED;
.LBB0_2294:
	v_add_u32_e32 v79, s65, v167
	ds_read_b128 v[142:145], v79
	ds_read_b128 v[156:159], v79 offset:1024
	ds_read_b128 v[178:181], v79 offset:2048
	ds_read_b128 v[182:185], v79 offset:3072
	v_add_u32_e32 v79, s66, v167
	ds_read_b128 v[186:189], v79
	ds_read_b128 v[190:193], v79 offset:1024
	ds_read_b128 v[196:199], v79 offset:2048
	ds_read_b128 v[200:203], v79 offset:3072
	s_add_u32 s40, s8, 0x100
	s_addc_u32 s41, s9, 0
	s_cmpk_eq_i32 s8, 0x700
	s_cselect_b64 vcc, -1, 0
	v_lshl_add_u64 v[160:161], v[88:89], 0, s[8:9]
	s_and_b64 s[76:77], vcc, exec
	v_cndmask_b32_e32 v161, v161, v155, vcc
	s_cselect_b32 s75, 0, s40
	v_cndmask_b32_e32 v160, v160, v154, vcc
	v_lshl_add_u64 v[236:237], v[140:141], 0, s[8:9]
	s_add_i32 m0, s42, 0xc000
	ds_read_b128 v[204:207], v169
	ds_read_b128 v[208:211], v169 offset:1024
	ds_read_b128 v[212:215], v169 offset:2048
	ds_read_b128 v[216:219], v169 offset:3072
	ds_read_b128 v[220:223], v169 offset:4096
	ds_read_b128 v[224:227], v169 offset:5120
	ds_read_b128 v[228:231], v169 offset:6144
	ds_read_b128 v[232:235], v169 offset:7168
	global_load_lds_dwordx4 v[236:237], off
	v_lshl_add_u64 v[236:237], v[138:139], 0, s[8:9]
	s_add_i32 m0, s42, 0xe000
	s_nop 0
	global_load_lds_dwordx4 v[236:237], off
	s_waitcnt vmcnt(8) lgkmcnt(0)
	s_barrier
	s_setprio 1
	s_waitcnt lgkmcnt(0)
	v_mfma_i32_16x16x64_i8 v[134:137], v[142:145], v[204:207], v[134:137]
	v_mfma_i32_16x16x64_i8 v[126:129], v[178:181], v[204:207], v[126:129]
	v_mfma_i32_16x16x64_i8 v[118:121], v[142:145], v[212:215], v[118:121]
	v_mfma_i32_16x16x64_i8 v[110:113], v[178:181], v[212:215], v[110:113]
	v_mfma_i32_16x16x64_i8 v[102:105], v[142:145], v[220:223], v[102:105]
	v_mfma_i32_16x16x64_i8 v[94:97], v[178:181], v[220:223], v[94:97]
	v_mfma_i32_16x16x64_i8 v[82:85], v[142:145], v[228:231], v[82:85]
	v_mfma_i32_16x16x64_i8 v[70:73], v[178:181], v[228:231], v[70:73]
	v_mfma_i32_16x16x64_i8 v[134:137], v[156:159], v[208:211], v[134:137]
	v_mfma_i32_16x16x64_i8 v[126:129], v[182:185], v[208:211], v[126:129]
	v_mfma_i32_16x16x64_i8 v[118:121], v[156:159], v[216:219], v[118:121]
	v_mfma_i32_16x16x64_i8 v[110:113], v[182:185], v[216:219], v[110:113]
	v_mfma_i32_16x16x64_i8 v[102:105], v[156:159], v[224:227], v[102:105]
	v_mfma_i32_16x16x64_i8 v[94:97], v[182:185], v[224:227], v[94:97]
	v_mfma_i32_16x16x64_i8 v[82:85], v[156:159], v[232:235], v[82:85]
	v_mfma_i32_16x16x64_i8 v[70:73], v[182:185], v[232:235], v[70:73]
	s_setprio 0
	s_setprio 1
	v_mfma_i32_16x16x64_i8 v[130:133], v[186:189], v[204:207], v[130:133]
	v_mfma_i32_16x16x64_i8 v[122:125], v[196:199], v[204:207], v[122:125]
	v_mfma_i32_16x16x64_i8 v[114:117], v[186:189], v[212:215], v[114:117]
	v_mfma_i32_16x16x64_i8 v[106:109], v[196:199], v[212:215], v[106:109]
	v_mfma_i32_16x16x64_i8 v[98:101], v[186:189], v[220:223], v[98:101]
	v_mfma_i32_16x16x64_i8 v[90:93], v[196:199], v[220:223], v[90:93]
	v_mfma_i32_16x16x64_i8 v[74:77], v[186:189], v[228:231], v[74:77]
	v_mfma_i32_16x16x64_i8 v[66:69], v[196:199], v[228:231], v[66:69]
	v_mfma_i32_16x16x64_i8 v[130:133], v[190:193], v[208:211], v[130:133]
	v_mfma_i32_16x16x64_i8 v[122:125], v[200:203], v[208:211], v[122:125]
	v_mfma_i32_16x16x64_i8 v[114:117], v[190:193], v[216:219], v[114:117]
	v_mfma_i32_16x16x64_i8 v[106:109], v[200:203], v[216:219], v[106:109]
	v_mfma_i32_16x16x64_i8 v[98:101], v[190:193], v[224:227], v[98:101]
	v_mfma_i32_16x16x64_i8 v[90:93], v[200:203], v[224:227], v[90:93]
	v_mfma_i32_16x16x64_i8 v[74:77], v[190:193], v[232:235], v[74:77]
	v_mfma_i32_16x16x64_i8 v[66:69], v[200:203], v[232:235], v[66:69]
	s_setprio 0
	s_barrier
	s_add_i32 s8, s65, s33
	v_lshl_add_u64 v[236:237], v[160:161], 0, v[148:149]
	s_mov_b32 m0, s8
	ds_read_b128 v[204:207], v169 offset:16384
	ds_read_b128 v[208:211], v169 offset:17408
	ds_read_b128 v[212:215], v169 offset:18432
	ds_read_b128 v[216:219], v169 offset:19456
	ds_read_b128 v[220:223], v169 offset:20480
	ds_read_b128 v[224:227], v169 offset:21504
	ds_read_b128 v[228:231], v169 offset:22528
	ds_read_b128 v[232:235], v169 offset:23552
	global_load_lds_dwordx4 v[236:237], off
	v_lshl_add_u64 v[238:239], v[160:161], 0, v[150:151]
	s_add_i32 m0, s8, 0x2000
	v_lshl_add_u64 v[240:241], v[160:161], 0, s[10:11]
	s_add_i32 s8, s66, s33
	global_load_lds_dwordx4 v[238:239], off
	v_lshl_add_u64 v[242:243], v[240:241], 0, v[148:149]
	s_mov_b32 m0, s8
	v_lshl_add_u64 v[240:241], v[240:241], 0, v[150:151]
	global_load_lds_dwordx4 v[242:243], off
	s_add_i32 m0, s8, 0x2000
	s_add_u32 s8, s60, s75
	global_load_lds_dwordx4 v[240:241], off
	v_cndmask_b32_e32 v146, v81, v173, vcc
	s_addc_u32 s9, s61, 0
	s_mov_b32 m0, s42
	v_cndmask_b32_e32 v240, v80, v174, vcc
	global_load_lds_dwordx4 v146, s[8:9]
	s_mov_b32 m0, s43
	v_mov_b32_e32 v241, v147
	global_load_lds_dwordx4 v240, s[8:9]
	s_waitcnt vmcnt(8)
	s_waitcnt lgkmcnt(0)
	v_lshl_add_u64 v[242:243], s[8:9], 0, v[146:147]
	v_lshl_add_u64 v[240:241], s[8:9], 0, v[240:241]
	s_barrier
; #define PG8_LDA(dst, b, h) do { _Pragma("unroll") for (int m = 0; m < 4; ++m) dst[m] = PG8_LD32(lds + PG8_SA(b, h) + aoff + m * 2048); } while (0)
; #define PG8_LDB(dst, b, h) do { _Pragma("unroll") for (int n = 0; n < 2; ++n) dst[n] = PG8_LD32(lds + PG8_SB(b, h) + boff + n * 2048); } while (0)
; #define PG8_WAIT_V(n) asm volatile("s_waitcnt vmcnt(" #n ")" ::: "memory")
; #define PG8_WAIT_L(n) asm volatile("s_waitcnt lgkmcnt(" #n ")" ::: "memory")
; #define PG8_BAR __builtin_amdgcn_s_barrier()
; #define PG8_SCHED __builtin_amdgcn_sched_barrier(0)
; #define PG8_STA(bufoff, nextflag, h, koff) do { if constexpr (Sched::GATHER) { unsigned _o[2]; _o[0] = (nextflag) ? nxtA[h][0] : curA[h][0]; _o[1] = (nextflag) ? nxtA[h][1] : curA[h][1]; PG8_STAGE(bufoff, Ab + (koff), _o); } \
;         else { PG8_STAGE(bufoff, ((nextflag) ? nA : cA) + (size_t)(h) * hstep + (koff), voffA); } } while (0)
; template <class Epi, class Sched, bool ALIGN_EPI, int DT>
; __device__ __forceinline__ void gemm_phase(LAS unsigned char* lds, const int KB, const Sched& S, const Epi& E) {
;     ...
;             PG8_WAIT_V(8); PG8_WAIT_L(0); PG8_BAR; PG8_MMA(1, 0, At, B0); PG8_MMA(1, 1, At, B1); PG8_BAR; PG8_SCHED;
;             PG8_LDB(B0, 1, 0); PG8_LDB(B1, 1, 1); PG8_SCHED; PG8_LDA(At, 1, 0); PG8_STA(PG8_SA(0, 1), last, 1, k2);
;             PG8_WAIT_V(8); PG8_WAIT_L(0); PG8_BAR; PG8_MMA(0, 0, At, B0); PG8_MMA(0, 1, At, B1); PG8_BAR; PG8_SCHED;
	s_setprio 1
	s_waitcnt lgkmcnt(0)
	v_mfma_i32_16x16x64_i8 v[54:57], v[142:145], v[204:207], v[54:57]
	v_mfma_i32_16x16x64_i8 v[50:53], v[178:181], v[204:207], v[50:53]
	v_mfma_i32_16x16x64_i8 v[42:45], v[142:145], v[212:215], v[42:45]
	v_mfma_i32_16x16x64_i8 v[34:37], v[178:181], v[212:215], v[34:37]
	v_mfma_i32_16x16x64_i8 v[26:29], v[142:145], v[220:223], v[26:29]
	v_mfma_i32_16x16x64_i8 v[18:21], v[178:181], v[220:223], v[18:21]
	v_mfma_i32_16x16x64_i8 v[10:13], v[142:145], v[228:231], v[10:13]
	v_mfma_i32_16x16x64_i8 v[2:5], v[178:181], v[228:231], v[2:5]
	v_mfma_i32_16x16x64_i8 v[54:57], v[156:159], v[208:211], v[54:57]
	v_mfma_i32_16x16x64_i8 v[50:53], v[182:185], v[208:211], v[50:53]
	v_mfma_i32_16x16x64_i8 v[42:45], v[156:159], v[216:219], v[42:45]
	v_mfma_i32_16x16x64_i8 v[34:37], v[182:185], v[216:219], v[34:37]
	v_mfma_i32_16x16x64_i8 v[26:29], v[156:159], v[224:227], v[26:29]
	v_mfma_i32_16x16x64_i8 v[18:21], v[182:185], v[224:227], v[18:21]
	v_mfma_i32_16x16x64_i8 v[10:13], v[156:159], v[232:235], v[10:13]
	v_mfma_i32_16x16x64_i8 v[2:5], v[182:185], v[232:235], v[2:5]
	s_setprio 0
	s_setprio 1
	v_mfma_i32_16x16x64_i8 v[62:65], v[186:189], v[204:207], v[62:65]
	v_mfma_i32_16x16x64_i8 v[58:61], v[196:199], v[204:207], v[58:61]
	v_mfma_i32_16x16x64_i8 v[46:49], v[186:189], v[212:215], v[46:49]
	v_mfma_i32_16x16x64_i8 v[38:41], v[196:199], v[212:215], v[38:41]
	v_mfma_i32_16x16x64_i8 v[30:33], v[186:189], v[220:223], v[30:33]
	v_mfma_i32_16x16x64_i8 v[22:25], v[196:199], v[220:223], v[22:25]
	v_mfma_i32_16x16x64_i8 v[14:17], v[186:189], v[228:231], v[14:17]
	v_mfma_i32_16x16x64_i8 v[6:9], v[196:199], v[228:231], v[6:9]
	v_mfma_i32_16x16x64_i8 v[62:65], v[190:193], v[208:211], v[62:65]
	v_mfma_i32_16x16x64_i8 v[58:61], v[200:203], v[208:211], v[58:61]
	v_mfma_i32_16x16x64_i8 v[46:49], v[190:193], v[216:219], v[46:49]
	v_mfma_i32_16x16x64_i8 v[38:41], v[200:203], v[216:219], v[38:41]
	v_mfma_i32_16x16x64_i8 v[30:33], v[190:193], v[224:227], v[30:33]
	v_mfma_i32_16x16x64_i8 v[22:25], v[200:203], v[224:227], v[22:25]
	v_mfma_i32_16x16x64_i8 v[14:17], v[190:193], v[232:235], v[14:17]
	v_mfma_i32_16x16x64_i8 v[6:9], v[200:203], v[232:235], v[6:9]
	s_setprio 0
	s_barrier
	s_add_i32 s75, 0, 0x18000
	v_add_u32_e32 v79, s75, v167
	s_add_i32 s76, 0, 0x1c000
	ds_read_b128 v[142:145], v79
	ds_read_b128 v[156:159], v79 offset:1024
	ds_read_b128 v[178:181], v79 offset:2048
	ds_read_b128 v[182:185], v79 offset:3072
	v_add_u32_e32 v79, s76, v167
	ds_read_b128 v[186:189], v79
	ds_read_b128 v[190:193], v79 offset:1024
	ds_read_b128 v[196:199], v79 offset:2048
	ds_read_b128 v[200:203], v79 offset:3072
	s_mov_b32 m0, s44
	v_cndmask_b32_e32 v79, v78, v175, vcc
	ds_read_b128 v[204:207], v169 offset:32768
	ds_read_b128 v[208:211], v169 offset:33792
	ds_read_b128 v[212:215], v169 offset:34816
	ds_read_b128 v[216:219], v169 offset:35840
	ds_read_b128 v[220:223], v169 offset:36864
	ds_read_b128 v[224:227], v169 offset:37888
	ds_read_b128 v[228:231], v169 offset:38912
	ds_read_b128 v[232:235], v169 offset:39936
	v_cndmask_b32_e32 v87, v86, v176, vcc
	global_load_lds_dwordx4 v79, s[8:9]
	s_mov_b32 m0, s45
	s_nop 0
	global_load_lds_dwordx4 v87, s[8:9]
	s_waitcnt vmcnt(8) lgkmcnt(0)
	s_barrier
	s_setprio 1
	s_waitcnt lgkmcnt(0)
	v_mfma_i32_16x16x64_i8 v[134:137], v[142:145], v[204:207], v[134:137]
	v_mfma_i32_16x16x64_i8 v[126:129], v[178:181], v[204:207], v[126:129]
	v_mfma_i32_16x16x64_i8 v[118:121], v[142:145], v[212:215], v[118:121]
	v_mfma_i32_16x16x64_i8 v[110:113], v[178:181], v[212:215], v[110:113]
	v_mfma_i32_16x16x64_i8 v[102:105], v[142:145], v[220:223], v[102:105]
	v_mfma_i32_16x16x64_i8 v[94:97], v[178:181], v[220:223], v[94:97]
	v_mfma_i32_16x16x64_i8 v[82:85], v[142:145], v[228:231], v[82:85]
	v_mfma_i32_16x16x64_i8 v[70:73], v[178:181], v[228:231], v[70:73]
	v_mfma_i32_16x16x64_i8 v[134:137], v[156:159], v[208:211], v[134:137]
	v_mfma_i32_16x16x64_i8 v[126:129], v[182:185], v[208:211], v[126:129]
	v_mfma_i32_16x16x64_i8 v[118:121], v[156:159], v[216:219], v[118:121]
	v_mfma_i32_16x16x64_i8 v[110:113], v[182:185], v[216:219], v[110:113]
	v_mfma_i32_16x16x64_i8 v[102:105], v[156:159], v[224:227], v[102:105]
	v_mfma_i32_16x16x64_i8 v[94:97], v[182:185], v[224:227], v[94:97]
	v_mfma_i32_16x16x64_i8 v[82:85], v[156:159], v[232:235], v[82:85]
	v_mfma_i32_16x16x64_i8 v[70:73], v[182:185], v[232:235], v[70:73]
	s_setprio 0
	s_setprio 1
	v_mfma_i32_16x16x64_i8 v[130:133], v[186:189], v[204:207], v[130:133]
	v_mfma_i32_16x16x64_i8 v[122:125], v[196:199], v[204:207], v[122:125]
	v_mfma_i32_16x16x64_i8 v[114:117], v[186:189], v[212:215], v[114:117]
	v_mfma_i32_16x16x64_i8 v[106:109], v[196:199], v[212:215], v[106:109]
	v_mfma_i32_16x16x64_i8 v[98:101], v[186:189], v[220:223], v[98:101]
	v_mfma_i32_16x16x64_i8 v[90:93], v[196:199], v[220:223], v[90:93]
	v_mfma_i32_16x16x64_i8 v[74:77], v[186:189], v[228:231], v[74:77]
	v_mfma_i32_16x16x64_i8 v[66:69], v[196:199], v[228:231], v[66:69]
	v_mfma_i32_16x16x64_i8 v[130:133], v[190:193], v[208:211], v[130:133]
	v_mfma_i32_16x16x64_i8 v[122:125], v[200:203], v[208:211], v[122:125]
	v_mfma_i32_16x16x64_i8 v[114:117], v[190:193], v[216:219], v[114:117]
	v_mfma_i32_16x16x64_i8 v[106:109], v[200:203], v[216:219], v[106:109]
	v_mfma_i32_16x16x64_i8 v[98:101], v[190:193], v[224:227], v[98:101]
	v_mfma_i32_16x16x64_i8 v[90:93], v[200:203], v[224:227], v[90:93]
	v_mfma_i32_16x16x64_i8 v[74:77], v[190:193], v[232:235], v[74:77]
	v_mfma_i32_16x16x64_i8 v[66:69], v[200:203], v[232:235], v[66:69]
	s_setprio 0
	s_barrier
; #define PG8_STAGE(bufoff, gbase, voff) do { _Pragma("unroll") for (int _i = 0; _i < 2; ++_i) \
;         __builtin_amdgcn_global_load_lds((const unsigned*)((const char*)(gbase) + (voff)[_i]), (LAS unsigned*)(lds + (bufoff) + ldsw + _i * 8192), 16, 0, 0); } while (0)
; #define PG8_LDA(dst, b, h) do { _Pragma("unroll") for (int m = 0; m < 4; ++m) dst[m] = PG8_LD32(lds + PG8_SA(b, h) + aoff + m * 2048); } while (0)
; #define PG8_WAIT_V(n) asm volatile("s_waitcnt vmcnt(" #n ")" ::: "memory")
; #define PG8_WAIT_L(n) asm volatile("s_waitcnt lgkmcnt(" #n ")" ::: "memory")
; #define PG8_BAR __builtin_amdgcn_s_barrier()
; #define PG8_SCHED __builtin_amdgcn_sched_barrier(0)
; #define PG8_STA(bufoff, nextflag, h, koff) do { if constexpr (Sched::GATHER) { unsigned _o[2]; _o[0] = (nextflag) ? nxtA[h][0] : curA[h][0]; _o[1] = (nextflag) ? nxtA[h][1] : curA[h][1]; PG8_STAGE(bufoff, Ab + (koff), _o); } \
;         else { PG8_STAGE(bufoff, ((nextflag) ? nA : cA) + (size_t)(h) * hstep + (koff), voffA); } } while (0)
; template <class Epi, class Sched, bool ALIGN_EPI, int DT>
; __device__ __forceinline__ void gemm_phase(LAS unsigned char* lds, const int KB, const Sched& S, const Epi& E) {
;     ...
;             PG8_LDA(At, 1, 1); PG8_STAGE(PG8_SB(1, 0), b3, voffB); PG8_STAGE(PG8_SB(1, 1), b3 + hstep, voffB); PG8_STA(PG8_SA(1, 0), last, 0, k3);
;             PG8_WAIT_V(8); PG8_WAIT_L(0); PG8_BAR; PG8_MMA(1, 0, At, B0); PG8_MMA(1, 1, At, B1); PG8_BAR; PG8_SCHED;
;         }
;         if constexpr (ALIGN_EPI) { if (wr == 0) PG8_BAR; }
	s_add_i32 s8, s75, s33
	v_lshl_add_u64 v[236:237], v[236:237], 0, s[20:21]
	s_mov_b32 m0, s8
	ds_read_b128 v[204:207], v169 offset:49152
	ds_read_b128 v[208:211], v169 offset:50176
	ds_read_b128 v[212:215], v169 offset:51200
	ds_read_b128 v[216:219], v169 offset:52224
	ds_read_b128 v[220:223], v169 offset:53248
	ds_read_b128 v[224:227], v169 offset:54272
	ds_read_b128 v[228:231], v169 offset:55296
	ds_read_b128 v[232:235], v169 offset:56320
	global_load_lds_dwordx4 v[236:237], off
	v_lshl_add_u64 v[236:237], v[238:239], 0, s[20:21]
	s_add_i32 m0, s8, 0x2000
	v_lshl_add_u64 v[160:161], v[160:161], 0, s[24:25]
	s_add_i32 s8, s76, s33
	global_load_lds_dwordx4 v[236:237], off
	v_lshl_add_u64 v[236:237], v[160:161], 0, v[148:149]
	s_mov_b32 m0, s8
	v_lshl_add_u64 v[160:161], v[160:161], 0, v[150:151]
	global_load_lds_dwordx4 v[236:237], off
	s_add_i32 m0, s8, 0x2000
	s_nop 0
	global_load_lds_dwordx4 v[160:161], off
	v_lshl_add_u64 v[160:161], v[242:243], 0, s[20:21]
	s_mov_b32 m0, s46
	s_nop 0
	global_load_lds_dwordx4 v[160:161], off
	v_lshl_add_u64 v[160:161], v[240:241], 0, s[20:21]
	s_mov_b32 m0, s47
	s_nop 0
	global_load_lds_dwordx4 v[160:161], off
	s_waitcnt vmcnt(8) lgkmcnt(0)
	s_barrier
	s_setprio 1
	s_waitcnt lgkmcnt(0)
	v_mfma_i32_16x16x64_i8 v[54:57], v[142:145], v[204:207], v[54:57]
	v_mfma_i32_16x16x64_i8 v[50:53], v[178:181], v[204:207], v[50:53]
	v_mfma_i32_16x16x64_i8 v[42:45], v[142:145], v[212:215], v[42:45]
	v_mfma_i32_16x16x64_i8 v[34:37], v[178:181], v[212:215], v[34:37]
	v_mfma_i32_16x16x64_i8 v[26:29], v[142:145], v[220:223], v[26:29]
	v_mfma_i32_16x16x64_i8 v[18:21], v[178:181], v[220:223], v[18:21]
	v_mfma_i32_16x16x64_i8 v[10:13], v[142:145], v[228:231], v[10:13]
	v_mfma_i32_16x16x64_i8 v[2:5], v[178:181], v[228:231], v[2:5]
	v_mfma_i32_16x16x64_i8 v[54:57], v[156:159], v[208:211], v[54:57]
	v_mfma_i32_16x16x64_i8 v[50:53], v[182:185], v[208:211], v[50:53]
	v_mfma_i32_16x16x64_i8 v[42:45], v[156:159], v[216:219], v[42:45]
	v_mfma_i32_16x16x64_i8 v[34:37], v[182:185], v[216:219], v[34:37]
	v_mfma_i32_16x16x64_i8 v[26:29], v[156:159], v[224:227], v[26:29]
	v_mfma_i32_16x16x64_i8 v[18:21], v[182:185], v[224:227], v[18:21]
	v_mfma_i32_16x16x64_i8 v[10:13], v[156:159], v[232:235], v[10:13]
	v_mfma_i32_16x16x64_i8 v[2:5], v[182:185], v[232:235], v[2:5]
	s_setprio 0
	s_setprio 1
	v_mfma_i32_16x16x64_i8 v[62:65], v[186:189], v[204:207], v[62:65]
	v_mfma_i32_16x16x64_i8 v[58:61], v[196:199], v[204:207], v[58:61]
	v_mfma_i32_16x16x64_i8 v[46:49], v[186:189], v[212:215], v[46:49]
	v_mfma_i32_16x16x64_i8 v[38:41], v[196:199], v[212:215], v[38:41]
	v_mfma_i32_16x16x64_i8 v[30:33], v[186:189], v[220:223], v[30:33]
	v_mfma_i32_16x16x64_i8 v[22:25], v[196:199], v[220:223], v[22:25]
	v_mfma_i32_16x16x64_i8 v[14:17], v[186:189], v[228:231], v[14:17]
	v_mfma_i32_16x16x64_i8 v[6:9], v[196:199], v[228:231], v[6:9]
	v_mfma_i32_16x16x64_i8 v[62:65], v[190:193], v[208:211], v[62:65]
	v_mfma_i32_16x16x64_i8 v[58:61], v[200:203], v[208:211], v[58:61]
	v_mfma_i32_16x16x64_i8 v[46:49], v[190:193], v[216:219], v[46:49]
	v_mfma_i32_16x16x64_i8 v[38:41], v[200:203], v[216:219], v[38:41]
	v_mfma_i32_16x16x64_i8 v[30:33], v[190:193], v[224:227], v[30:33]
	v_mfma_i32_16x16x64_i8 v[22:25], v[200:203], v[224:227], v[22:25]
	v_mfma_i32_16x16x64_i8 v[14:17], v[190:193], v[232:235], v[14:17]
	v_mfma_i32_16x16x64_i8 v[6:9], v[200:203], v[232:235], v[6:9]
	s_setprio 0
	s_barrier
	s_add_i32 s37, s37, 2
	s_cmp_gt_u32 s37, 13
	s_mov_b64 s[8:9], s[40:41]
	s_cbranch_scc0 .LBB0_2294
	s_and_b64 vcc, exec, s[26:27]
	s_cbranch_vccz .LBB0_2297
	s_barrier

; #define PG8_STAGE(bufoff, gbase, voff) do { _Pragma("unroll") for (int _i = 0; _i < 2; ++_i) \
;         __builtin_amdgcn_global_load_lds((const unsigned*)((const char*)(gbase) + (voff)[_i]), (LAS unsigned*)(lds + (bufoff) + ldsw + _i * 8192), 16, 0, 0); } while (0)
; #define PG8_LDA(dst, b, h) do { _Pragma("unroll") for (int m = 0; m < 4; ++m) dst[m] = PG8_LD32(lds + PG8_SA(b, h) + aoff + m * 2048); } while (0)
; #define PG8_LDB(dst, b, h) do { _Pragma("unroll") for (int n = 0; n < 2; ++n) dst[n] = PG8_LD32(lds + PG8_SB(b, h) + boff + n * 2048); } while (0)
; #define PG8_WAIT_V(n) asm volatile("s_waitcnt vmcnt(" #n ")" ::: "memory")
; #define PG8_WAIT_L(n) asm volatile("s_waitcnt lgkmcnt(" #n ")" ::: "memory")
; #define PG8_BAR __builtin_amdgcn_s_barrier()
; #define PG8_SCHED __builtin_amdgcn_sched_barrier(0)
; #define PG8_STA(bufoff, nextflag, h, koff) do { if constexpr (Sched::GATHER) { unsigned _o[2]; _o[0] = (nextflag) ? nxtA[h][0] : curA[h][0]; _o[1] = (nextflag) ? nxtA[h][1] : curA[h][1]; PG8_STAGE(bufoff, Ab + (koff), _o); } \
;         else { PG8_STAGE(bufoff, ((nextflag) ? nA : cA) + (size_t)(h) * hstep + (koff), voffA); } } while (0)
; template <class Epi, class Sched, bool ALIGN_EPI, int DT>
; __device__ __forceinline__ void gemm_phase(LAS unsigned char* lds, const int KB, const Sched& S, const Epi& E) {
;     ...
;             PG8_LDB(B0, 0, 0); PG8_LDB(B1, 0, 1); PG8_SCHED; PG8_LDA(At, 0, 0); PG8_STA(PG8_SA(1, 1), false, 1, k1);
;             PG8_WAIT_V(8); PG8_WAIT_L(0); PG8_BAR; PG8_MMA(0, 0, At, B0); PG8_MMA(0, 1, At, B1); PG8_BAR; PG8_SCHED;
;             PG8_LDA(At, 0, 1); PG8_STAGE(PG8_SB(0, 0), b2, voffB); PG8_STAGE(PG8_SB(0, 1), b2 + hstep, voffB); PG8_STA(PG8_SA(0, 0), last, 0, k2);
;             PG8_WAIT_V(8); PG8_WAIT_L(0); PG8_BAR; PG8_MMA(1, 0, At, B0); PG8_MMA(1, 1, At, B1); PG8_BAR; PG8_SCHED;
.LBB0_2387:
	ds_read_b128 v[18:21], v198
	ds_read_b128 v[22:25], v198 offset:1024
	ds_read_b128 v[26:29], v198 offset:2048
	ds_read_b128 v[30:33], v198 offset:3072
	ds_read_b128 v[2:5], v199
	ds_read_b128 v[6:9], v199 offset:1024
	ds_read_b128 v[10:13], v199 offset:2048
	ds_read_b128 v[14:17], v199 offset:3072
	s_add_u32 s42, s44, 0x100
	s_addc_u32 s43, s45, 0
	s_add_i32 s76, s63, s4
	s_add_i32 m0, s33, 0xc000
	s_add_i32 s77, s33, 0xe000
	s_add_i32 s74, s76, 0x2000
	s_cmp_eq_u32 s71, 18
	v_lshl_add_u64 v[184:185], v[178:179], 0, s[44:45]
	s_cselect_b64 vcc, -1, 0
	s_cselect_b32 s75, 0, s42
	v_cndmask_b32_e32 v185, v185, v177, vcc
	v_cndmask_b32_e32 v184, v184, v176, vcc
	v_lshl_add_u64 v[226:227], v[180:181], 0, s[44:45]
	ds_read_b128 v[186:189], v200
	ds_read_b128 v[190:193], v200 offset:1024
	ds_read_b128 v[202:205], v200 offset:2048
	ds_read_b128 v[206:209], v200 offset:3072
	ds_read_b128 v[210:213], v200 offset:4096
	ds_read_b128 v[214:217], v200 offset:5120
	ds_read_b128 v[218:221], v200 offset:6144
	ds_read_b128 v[222:225], v200 offset:7168
	global_load_lds_dwordx4 v[226:227], off
	v_lshl_add_u64 v[226:227], v[182:183], 0, s[44:45]
	s_mov_b32 m0, s77
	s_nop 0
	global_load_lds_dwordx4 v[226:227], off
	s_waitcnt vmcnt(8) lgkmcnt(0)
	s_barrier
	s_setprio 1
	s_waitcnt lgkmcnt(0)
	v_mfma_scale_f32_16x16x128_f8f6f4 v[158:161], v[18:25], v[186:193], v[158:161], v1, v1 op_sel_hi:[0,0,0]
	v_mfma_scale_f32_16x16x128_f8f6f4 v[154:157], v[26:33], v[186:193], v[154:157], v1, v1 op_sel_hi:[0,0,0]
	v_mfma_scale_f32_16x16x128_f8f6f4 v[150:153], v[18:25], v[202:209], v[150:153], v1, v1 op_sel_hi:[0,0,0]
	v_mfma_scale_f32_16x16x128_f8f6f4 v[142:145], v[26:33], v[202:209], v[142:145], v1, v1 op_sel_hi:[0,0,0]
	v_mfma_scale_f32_16x16x128_f8f6f4 v[134:137], v[18:25], v[210:217], v[134:137], v1, v1 op_sel_hi:[0,0,0]
	v_mfma_scale_f32_16x16x128_f8f6f4 v[126:129], v[26:33], v[210:217], v[126:129], v1, v1 op_sel_hi:[0,0,0]
	v_mfma_scale_f32_16x16x128_f8f6f4 v[118:121], v[18:25], v[218:225], v[118:121], v1, v1 op_sel_hi:[0,0,0]
	v_mfma_scale_f32_16x16x128_f8f6f4 v[110:113], v[26:33], v[218:225], v[110:113], v1, v1 op_sel_hi:[0,0,0]
	s_setprio 0
	s_setprio 1
	v_mfma_scale_f32_16x16x128_f8f6f4 v[146:149], v[2:9], v[186:193], v[146:149], v1, v1 op_sel_hi:[0,0,0]
	v_mfma_scale_f32_16x16x128_f8f6f4 v[138:141], v[10:17], v[186:193], v[138:141], v1, v1 op_sel_hi:[0,0,0]
	v_mfma_scale_f32_16x16x128_f8f6f4 v[130:133], v[2:9], v[202:209], v[130:133], v1, v1 op_sel_hi:[0,0,0]
	v_mfma_scale_f32_16x16x128_f8f6f4 v[122:125], v[10:17], v[202:209], v[122:125], v1, v1 op_sel_hi:[0,0,0]
	v_mfma_scale_f32_16x16x128_f8f6f4 v[114:117], v[2:9], v[210:217], v[114:117], v1, v1 op_sel_hi:[0,0,0]
	v_mfma_scale_f32_16x16x128_f8f6f4 v[106:109], v[10:17], v[210:217], v[106:109], v1, v1 op_sel_hi:[0,0,0]
	v_mfma_scale_f32_16x16x128_f8f6f4 v[102:105], v[2:9], v[218:225], v[102:105], v1, v1 op_sel_hi:[0,0,0]
	v_mfma_scale_f32_16x16x128_f8f6f4 v[98:101], v[10:17], v[218:225], v[98:101], v1, v1 op_sel_hi:[0,0,0]
	s_setprio 0
	s_barrier
	s_mov_b32 m0, s76
	v_lshl_add_u64 v[188:189], v[184:185], 0, v[170:171]
	ds_read_b128 v[202:205], v200 offset:16384
	ds_read_b128 v[206:209], v200 offset:17408
	ds_read_b128 v[210:213], v200 offset:18432
	ds_read_b128 v[214:217], v200 offset:19456
	ds_read_b128 v[218:221], v200 offset:20480
	ds_read_b128 v[222:225], v200 offset:21504
	ds_read_b128 v[226:229], v200 offset:22528
	ds_read_b128 v[230:233], v200 offset:23552
	global_load_lds_dwordx4 v[188:189], off
	v_lshl_add_u64 v[186:187], v[184:185], 0, v[164:165]
	s_mov_b32 m0, s74
	s_cselect_b32 s45, s9, s41
	s_cselect_b32 s44, s8, s40
	v_lshl_add_u64 v[190:191], v[184:185], 0, s[12:13]
	s_add_i32 s74, s64, s4
	global_load_lds_dwordx4 v[186:187], off
	v_lshl_add_u64 v[192:193], v[190:191], 0, v[170:171]
	s_mov_b32 m0, s74
	v_lshl_add_u64 v[190:191], v[190:191], 0, v[164:165]
	global_load_lds_dwordx4 v[192:193], off
	s_add_i32 m0, s74, 0x2000
	s_add_u32 s44, s44, s75
	s_addc_u32 s45, s45, 0
	global_load_lds_dwordx4 v[190:191], off
	v_lshl_add_u64 v[190:191], s[44:45], 0, v[166:167]
	s_mov_b32 m0, s33
	v_lshl_add_u64 v[192:193], s[44:45], 0, v[168:169]
	global_load_lds_dwordx4 v[190:191], off
	s_mov_b32 m0, s39
	s_nop 0
	global_load_lds_dwordx4 v[192:193], off
	s_waitcnt vmcnt(8) lgkmcnt(0)
	s_barrier
	s_setprio 1
	s_waitcnt lgkmcnt(0)
	v_mfma_scale_f32_16x16x128_f8f6f4 v[94:97], v[18:25], v[202:209], v[94:97], v1, v1 op_sel_hi:[0,0,0]
	v_mfma_scale_f32_16x16x128_f8f6f4 v[90:93], v[26:33], v[202:209], v[90:93], v1, v1 op_sel_hi:[0,0,0]
	v_mfma_scale_f32_16x16x128_f8f6f4 v[86:89], v[18:25], v[210:217], v[86:89], v1, v1 op_sel_hi:[0,0,0]
	v_mfma_scale_f32_16x16x128_f8f6f4 v[78:81], v[26:33], v[210:217], v[78:81], v1, v1 op_sel_hi:[0,0,0]
	v_mfma_scale_f32_16x16x128_f8f6f4 v[62:65], v[18:25], v[218:225], v[62:65], v1, v1 op_sel_hi:[0,0,0]
	v_mfma_scale_f32_16x16x128_f8f6f4 v[54:57], v[26:33], v[218:225], v[54:57], v1, v1 op_sel_hi:[0,0,0]
	v_mfma_scale_f32_16x16x128_f8f6f4 v[46:49], v[18:25], v[226:233], v[46:49], v1, v1 op_sel_hi:[0,0,0]
	v_mfma_scale_f32_16x16x128_f8f6f4 v[38:41], v[26:33], v[226:233], v[38:41], v1, v1 op_sel_hi:[0,0,0]
	s_setprio 0
	s_setprio 1
	v_mfma_scale_f32_16x16x128_f8f6f4 v[82:85], v[2:9], v[202:209], v[82:85], v1, v1 op_sel_hi:[0,0,0]
	v_mfma_scale_f32_16x16x128_f8f6f4 v[74:77], v[10:17], v[202:209], v[74:77], v1, v1 op_sel_hi:[0,0,0]
	v_mfma_scale_f32_16x16x128_f8f6f4 v[58:61], v[2:9], v[210:217], v[58:61], v1, v1 op_sel_hi:[0,0,0]
	v_mfma_scale_f32_16x16x128_f8f6f4 v[50:53], v[10:17], v[210:217], v[50:53], v1, v1 op_sel_hi:[0,0,0]
	v_mfma_scale_f32_16x16x128_f8f6f4 v[42:45], v[2:9], v[218:225], v[42:45], v1, v1 op_sel_hi:[0,0,0]
	v_mfma_scale_f32_16x16x128_f8f6f4 v[34:37], v[10:17], v[218:225], v[34:37], v1, v1 op_sel_hi:[0,0,0]
	v_mfma_scale_f32_16x16x128_f8f6f4 v[70:73], v[2:9], v[226:233], v[70:73], v1, v1 op_sel_hi:[0,0,0]
	v_mfma_scale_f32_16x16x128_f8f6f4 v[66:69], v[10:17], v[226:233], v[66:69], v1, v1 op_sel_hi:[0,0,0]
	s_setprio 0
	s_barrier
; #define PG8_STAGE(bufoff, gbase, voff) do { _Pragma("unroll") for (int _i = 0; _i < 2; ++_i) \
;         __builtin_amdgcn_global_load_lds((const unsigned*)((const char*)(gbase) + (voff)[_i]), (LAS unsigned*)(lds + (bufoff) + ldsw + _i * 8192), 16, 0, 0); } while (0)
; #define PG8_LDA(dst, b, h) do { _Pragma("unroll") for (int m = 0; m < 4; ++m) dst[m] = PG8_LD32(lds + PG8_SA(b, h) + aoff + m * 2048); } while (0)
; #define PG8_LDB(dst, b, h) do { _Pragma("unroll") for (int n = 0; n < 2; ++n) dst[n] = PG8_LD32(lds + PG8_SB(b, h) + boff + n * 2048); } while (0)
; #define PG8_WAIT_V(n) asm volatile("s_waitcnt vmcnt(" #n ")" ::: "memory")
; #define PG8_WAIT_L(n) asm volatile("s_waitcnt lgkmcnt(" #n ")" ::: "memory")
; #define PG8_BAR __builtin_amdgcn_s_barrier()
; #define PG8_SCHED __builtin_amdgcn_sched_barrier(0)
; #define PG8_STA(bufoff, nextflag, h, koff) do { if constexpr (Sched::GATHER) { unsigned _o[2]; _o[0] = (nextflag) ? nxtA[h][0] : curA[h][0]; _o[1] = (nextflag) ? nxtA[h][1] : curA[h][1]; PG8_STAGE(bufoff, Ab + (koff), _o); } \
;         else { PG8_STAGE(bufoff, ((nextflag) ? nA : cA) + (size_t)(h) * hstep + (koff), voffA); } } while (0)
; template <class Epi, class Sched, bool ALIGN_EPI, int DT>
; __device__ __forceinline__ void gemm_phase(LAS unsigned char* lds, const int KB, const Sched& S, const Epi& E) {
;     ...
;             PG8_LDB(B0, 1, 0); PG8_LDB(B1, 1, 1); PG8_SCHED; PG8_LDA(At, 1, 0); PG8_STA(PG8_SA(0, 1), last, 1, k2);
;             PG8_WAIT_V(8); PG8_WAIT_L(0); PG8_BAR; PG8_MMA(0, 0, At, B0); PG8_MMA(0, 1, At, B1); PG8_BAR; PG8_SCHED;
;             PG8_LDA(At, 1, 1); PG8_STAGE(PG8_SB(1, 0), b3, voffB); PG8_STAGE(PG8_SB(1, 1), b3 + hstep, voffB); PG8_STA(PG8_SA(1, 0), last, 0, k3);
;             PG8_WAIT_V(8); PG8_WAIT_L(0); PG8_BAR; PG8_MMA(1, 0, At, B0); PG8_MMA(1, 1, At, B1); PG8_BAR; PG8_SCHED;
;         }
;         if constexpr (ALIGN_EPI) { if (wr == 0) PG8_BAR; }
	s_add_i32 s74, 0, 0x18000
	s_add_i32 s75, 0, 0x1c000
	v_add_u32_e32 v14, s74, v196
	v_add_u32_e32 v30, s75, v196
	ds_read_b128 v[2:5], v14
	ds_read_b128 v[6:9], v14 offset:1024
	ds_read_b128 v[10:13], v14 offset:2048
	ds_read_b128 v[14:17], v14 offset:3072
	ds_read_b128 v[18:21], v30
	ds_read_b128 v[22:25], v30 offset:1024
	ds_read_b128 v[26:29], v30 offset:2048
	ds_read_b128 v[30:33], v30 offset:3072
	s_add_u32 s44, s44, 0x58000
	s_addc_u32 s45, s45, 0
	s_mov_b32 m0, s46
	v_lshl_add_u64 v[234:235], s[44:45], 0, v[166:167]
	ds_read_b128 v[202:205], v200 offset:32768
	ds_read_b128 v[206:209], v200 offset:33792
	ds_read_b128 v[210:213], v200 offset:34816
	ds_read_b128 v[214:217], v200 offset:35840
	ds_read_b128 v[218:221], v200 offset:36864
	ds_read_b128 v[222:225], v200 offset:37888
	ds_read_b128 v[226:229], v200 offset:38912
	ds_read_b128 v[230:233], v200 offset:39936
	global_load_lds_dwordx4 v[234:235], off
	v_lshl_add_u64 v[234:235], s[44:45], 0, v[168:169]
	s_mov_b32 m0, s47
	s_nop 0
	global_load_lds_dwordx4 v[234:235], off
	s_waitcnt vmcnt(8) lgkmcnt(0)
	s_barrier
	s_setprio 1
	s_waitcnt lgkmcnt(0)
	v_mfma_scale_f32_16x16x128_f8f6f4 v[158:161], v[2:9], v[202:209], v[158:161], v1, v1 op_sel_hi:[0,0,0]
	v_mfma_scale_f32_16x16x128_f8f6f4 v[154:157], v[10:17], v[202:209], v[154:157], v1, v1 op_sel_hi:[0,0,0]
	v_mfma_scale_f32_16x16x128_f8f6f4 v[150:153], v[2:9], v[210:217], v[150:153], v1, v1 op_sel_hi:[0,0,0]
	v_mfma_scale_f32_16x16x128_f8f6f4 v[142:145], v[10:17], v[210:217], v[142:145], v1, v1 op_sel_hi:[0,0,0]
	v_mfma_scale_f32_16x16x128_f8f6f4 v[134:137], v[2:9], v[218:225], v[134:137], v1, v1 op_sel_hi:[0,0,0]
	v_mfma_scale_f32_16x16x128_f8f6f4 v[126:129], v[10:17], v[218:225], v[126:129], v1, v1 op_sel_hi:[0,0,0]
	v_mfma_scale_f32_16x16x128_f8f6f4 v[118:121], v[2:9], v[226:233], v[118:121], v1, v1 op_sel_hi:[0,0,0]
	v_mfma_scale_f32_16x16x128_f8f6f4 v[110:113], v[10:17], v[226:233], v[110:113], v1, v1 op_sel_hi:[0,0,0]
	s_setprio 0
	s_setprio 1
	v_mfma_scale_f32_16x16x128_f8f6f4 v[146:149], v[18:25], v[202:209], v[146:149], v1, v1 op_sel_hi:[0,0,0]
	v_mfma_scale_f32_16x16x128_f8f6f4 v[138:141], v[26:33], v[202:209], v[138:141], v1, v1 op_sel_hi:[0,0,0]
	v_mfma_scale_f32_16x16x128_f8f6f4 v[130:133], v[18:25], v[210:217], v[130:133], v1, v1 op_sel_hi:[0,0,0]
	v_mfma_scale_f32_16x16x128_f8f6f4 v[122:125], v[26:33], v[210:217], v[122:125], v1, v1 op_sel_hi:[0,0,0]
	v_mfma_scale_f32_16x16x128_f8f6f4 v[114:117], v[18:25], v[218:225], v[114:117], v1, v1 op_sel_hi:[0,0,0]
	v_mfma_scale_f32_16x16x128_f8f6f4 v[106:109], v[26:33], v[218:225], v[106:109], v1, v1 op_sel_hi:[0,0,0]
	v_mfma_scale_f32_16x16x128_f8f6f4 v[102:105], v[18:25], v[226:233], v[102:105], v1, v1 op_sel_hi:[0,0,0]
	v_mfma_scale_f32_16x16x128_f8f6f4 v[98:101], v[26:33], v[226:233], v[98:101], v1, v1 op_sel_hi:[0,0,0]
	s_setprio 0
	s_barrier
	s_add_i32 s44, s74, s4
	v_lshl_add_u64 v[188:189], v[188:189], 0, s[16:17]
	s_mov_b32 m0, s44
	ds_read_b128 v[202:205], v200 offset:49152
	ds_read_b128 v[206:209], v200 offset:50176
	ds_read_b128 v[210:213], v200 offset:51200
	ds_read_b128 v[214:217], v200 offset:52224
	ds_read_b128 v[218:221], v200 offset:53248
	ds_read_b128 v[222:225], v200 offset:54272
	ds_read_b128 v[226:229], v200 offset:55296
	ds_read_b128 v[230:233], v200 offset:56320
	global_load_lds_dwordx4 v[188:189], off
	v_lshl_add_u64 v[186:187], v[186:187], 0, s[16:17]
	s_add_i32 m0, s44, 0x2000
	v_lshl_add_u64 v[184:185], v[184:185], 0, s[18:19]
	s_add_i32 s44, s75, s4
	global_load_lds_dwordx4 v[186:187], off
	v_lshl_add_u64 v[186:187], v[184:185], 0, v[170:171]
	s_mov_b32 m0, s44
	v_lshl_add_u64 v[184:185], v[184:185], 0, v[164:165]
	global_load_lds_dwordx4 v[186:187], off
	s_add_i32 m0, s44, 0x2000
	s_nop 0
	global_load_lds_dwordx4 v[184:185], off
	v_lshl_add_u64 v[184:185], v[190:191], 0, s[16:17]
	s_mov_b32 m0, s52
	s_nop 0
	global_load_lds_dwordx4 v[184:185], off
	v_lshl_add_u64 v[184:185], v[192:193], 0, s[16:17]
	s_mov_b32 m0, s53
	s_nop 0
	global_load_lds_dwordx4 v[184:185], off
	s_waitcnt vmcnt(8) lgkmcnt(0)
	s_barrier
	s_setprio 1
	s_waitcnt lgkmcnt(0)
	v_mfma_scale_f32_16x16x128_f8f6f4 v[94:97], v[2:9], v[202:209], v[94:97], v1, v1 op_sel_hi:[0,0,0]
	v_mfma_scale_f32_16x16x128_f8f6f4 v[90:93], v[10:17], v[202:209], v[90:93], v1, v1 op_sel_hi:[0,0,0]
	v_mfma_scale_f32_16x16x128_f8f6f4 v[86:89], v[2:9], v[210:217], v[86:89], v1, v1 op_sel_hi:[0,0,0]
	v_mfma_scale_f32_16x16x128_f8f6f4 v[78:81], v[10:17], v[210:217], v[78:81], v1, v1 op_sel_hi:[0,0,0]
	v_mfma_scale_f32_16x16x128_f8f6f4 v[62:65], v[2:9], v[218:225], v[62:65], v1, v1 op_sel_hi:[0,0,0]
	v_mfma_scale_f32_16x16x128_f8f6f4 v[54:57], v[10:17], v[218:225], v[54:57], v1, v1 op_sel_hi:[0,0,0]
	v_mfma_scale_f32_16x16x128_f8f6f4 v[46:49], v[2:9], v[226:233], v[46:49], v1, v1 op_sel_hi:[0,0,0]
	v_mfma_scale_f32_16x16x128_f8f6f4 v[38:41], v[10:17], v[226:233], v[38:41], v1, v1 op_sel_hi:[0,0,0]
	s_setprio 0
	s_setprio 1
	v_mfma_scale_f32_16x16x128_f8f6f4 v[82:85], v[18:25], v[202:209], v[82:85], v1, v1 op_sel_hi:[0,0,0]
	v_mfma_scale_f32_16x16x128_f8f6f4 v[74:77], v[26:33], v[202:209], v[74:77], v1, v1 op_sel_hi:[0,0,0]
	v_mfma_scale_f32_16x16x128_f8f6f4 v[58:61], v[18:25], v[210:217], v[58:61], v1, v1 op_sel_hi:[0,0,0]
	v_mfma_scale_f32_16x16x128_f8f6f4 v[50:53], v[26:33], v[210:217], v[50:53], v1, v1 op_sel_hi:[0,0,0]
	v_mfma_scale_f32_16x16x128_f8f6f4 v[42:45], v[18:25], v[218:225], v[42:45], v1, v1 op_sel_hi:[0,0,0]
	v_mfma_scale_f32_16x16x128_f8f6f4 v[34:37], v[26:33], v[218:225], v[34:37], v1, v1 op_sel_hi:[0,0,0]
	v_mfma_scale_f32_16x16x128_f8f6f4 v[70:73], v[18:25], v[226:233], v[70:73], v1, v1 op_sel_hi:[0,0,0]
	v_mfma_scale_f32_16x16x128_f8f6f4 v[66:69], v[26:33], v[226:233], v[66:69], v1, v1 op_sel_hi:[0,0,0]
	s_setprio 0
	s_barrier
	s_add_i32 s71, s71, 2
	s_cmp_gt_u32 s71, 19
	s_mov_b64 s[44:45], s[42:43]
	s_cbranch_scc0 .LBB0_2387
	s_and_b64 vcc, exec, s[20:21]
	s_cbranch_vccz .LBB0_2390
	s_barrier
